# GEMM MMA segments: the duplicate s_waitcnt lgkmcnt(0) right behind the asm-volatile one removed (one issue slot fewer ahead of each MFMA run); on top of v110
# baseline (speedup 1.0000x reference)
.LBB0_389:
	s_add_u32 s0, s30, 0xfffc0080
	s_addc_u32 s1, s31, -1
	s_add_i32 s33, 0, 0x10000
	s_cmp_eq_u32 s79, 12
	s_cselect_b32 s67, s7, s1
	s_cselect_b32 s66, s9, s0
	s_cselect_b32 s65, s23, s78
	s_cselect_b32 s64, s25, s77
	v_lshl_add_u64 v[156:157], s[30:31], 0, v[148:149]
	s_add_i32 m0, s40, 0xc000
	ds_read_b128 v[174:177], v161
	ds_read_b128 v[178:181], v161 offset:1024
	ds_read_b128 v[182:185], v161 offset:2048
	ds_read_b128 v[186:189], v161 offset:3072
	ds_read_b128 v[190:193], v161 offset:4096
	ds_read_b128 v[198:201], v161 offset:5120
	ds_read_b128 v[202:205], v161 offset:6144
	ds_read_b128 v[206:209], v161 offset:7168
	global_load_lds_dwordx4 v[156:157], off
	v_lshl_add_u64 v[156:157], s[30:31], 0, v[150:151]
	s_add_i32 m0, s40, 0xe000
	s_nop 0
	global_load_lds_dwordx4 v[156:157], off
	s_waitcnt lgkmcnt(8)
	s_barrier
	s_waitcnt lgkmcnt(0)
	v_mfma_f32_16x16x32_bf16 v[126:129], v[152:155], v[174:177], v[126:129]
	v_mfma_f32_16x16x32_bf16 v[122:125], v[166:169], v[174:177], v[122:125]
	v_mfma_f32_16x16x32_bf16 v[110:113], v[152:155], v[182:185], v[110:113]
	v_mfma_f32_16x16x32_bf16 v[106:109], v[166:169], v[182:185], v[106:109]
	v_mfma_f32_16x16x32_bf16 v[94:97], v[152:155], v[190:193], v[94:97]
	v_mfma_f32_16x16x32_bf16 v[90:93], v[166:169], v[190:193], v[90:93]
	v_mfma_f32_16x16x32_bf16 v[78:81], v[152:155], v[202:205], v[78:81]
	v_mfma_f32_16x16x32_bf16 v[74:77], v[166:169], v[202:205], v[74:77]
	v_mfma_f32_16x16x32_bf16 v[126:129], v[162:165], v[178:181], v[126:129]
	v_mfma_f32_16x16x32_bf16 v[122:125], v[170:173], v[178:181], v[122:125]
	v_mfma_f32_16x16x32_bf16 v[110:113], v[162:165], v[186:189], v[110:113]
	v_mfma_f32_16x16x32_bf16 v[106:109], v[170:173], v[186:189], v[106:109]
	v_mfma_f32_16x16x32_bf16 v[94:97], v[162:165], v[198:201], v[94:97]
	v_mfma_f32_16x16x32_bf16 v[90:93], v[170:173], v[198:201], v[90:93]
	v_mfma_f32_16x16x32_bf16 v[78:81], v[162:165], v[206:209], v[78:81]
	v_mfma_f32_16x16x32_bf16 v[74:77], v[170:173], v[206:209], v[74:77]
	s_barrier
	s_add_i32 s36, 0, 0x14000
	v_add_u32_e32 v156, s36, v158
	s_add_i32 s0, s33, s38
	ds_read_b128 v[210:213], v156
	ds_read_b128 v[214:217], v156 offset:1024
	ds_read_b128 v[218:221], v156 offset:2048
	ds_read_b128 v[238:241], v156 offset:3072
	v_lshl_add_u64 v[156:157], s[64:65], 0, v[132:133]
	s_mov_b32 m0, s0
	v_lshl_add_u64 v[242:243], s[64:65], 0, v[136:137]
	global_load_lds_dwordx4 v[156:157], off
	s_add_i32 m0, s0, 0x2000
	s_nop 0
	global_load_lds_dwordx4 v[242:243], off
	s_barrier
	s_waitcnt lgkmcnt(0)
	v_mfma_f32_16x16x32_bf16 v[118:121], v[210:213], v[174:177], v[118:121]
	v_mfma_f32_16x16x32_bf16 v[114:117], v[218:221], v[174:177], v[114:117]
	v_mfma_f32_16x16x32_bf16 v[102:105], v[210:213], v[182:185], v[102:105]
	v_mfma_f32_16x16x32_bf16 v[98:101], v[218:221], v[182:185], v[98:101]
	v_mfma_f32_16x16x32_bf16 v[86:89], v[210:213], v[190:193], v[86:89]
	v_mfma_f32_16x16x32_bf16 v[82:85], v[218:221], v[190:193], v[82:85]
	v_mfma_f32_16x16x32_bf16 v[70:73], v[210:213], v[202:205], v[70:73]
	v_mfma_f32_16x16x32_bf16 v[66:69], v[218:221], v[202:205], v[66:69]
	v_mfma_f32_16x16x32_bf16 v[118:121], v[214:217], v[178:181], v[118:121]
	v_mfma_f32_16x16x32_bf16 v[114:117], v[238:241], v[178:181], v[114:117]
	v_mfma_f32_16x16x32_bf16 v[102:105], v[214:217], v[186:189], v[102:105]
	v_mfma_f32_16x16x32_bf16 v[98:101], v[238:241], v[186:189], v[98:101]
	v_mfma_f32_16x16x32_bf16 v[86:89], v[214:217], v[198:201], v[86:89]
	v_mfma_f32_16x16x32_bf16 v[82:85], v[238:241], v[198:201], v[82:85]
	v_mfma_f32_16x16x32_bf16 v[70:73], v[214:217], v[206:209], v[70:73]
	v_mfma_f32_16x16x32_bf16 v[66:69], v[238:241], v[206:209], v[66:69]
	s_mov_b32 m0, s40
	v_lshl_add_u64 v[244:245], s[66:67], 0, v[130:131]
	s_barrier
	ds_read_b128 v[174:177], v161 offset:16384
	ds_read_b128 v[178:181], v161 offset:17408
	ds_read_b128 v[182:185], v161 offset:18432
	ds_read_b128 v[186:189], v161 offset:19456
	ds_read_b128 v[190:193], v161 offset:20480
	ds_read_b128 v[198:201], v161 offset:21504
	ds_read_b128 v[202:205], v161 offset:22528
	ds_read_b128 v[206:209], v161 offset:23552
	global_load_lds_dwordx4 v[244:245], off
	v_lshl_add_u64 v[246:247], s[66:67], 0, v[134:135]
	s_mov_b32 m0, s43
	s_nop 0
	global_load_lds_dwordx4 v[246:247], off
	s_waitcnt vmcnt(10)
	s_barrier
	s_waitcnt lgkmcnt(0)
	v_mfma_f32_16x16x32_bf16 v[62:65], v[152:155], v[174:177], v[62:65]
	v_mfma_f32_16x16x32_bf16 v[58:61], v[166:169], v[174:177], v[58:61]
	v_mfma_f32_16x16x32_bf16 v[46:49], v[152:155], v[182:185], v[46:49]
	v_mfma_f32_16x16x32_bf16 v[42:45], v[166:169], v[182:185], v[42:45]
	v_mfma_f32_16x16x32_bf16 v[30:33], v[152:155], v[190:193], v[30:33]
	v_mfma_f32_16x16x32_bf16 v[26:29], v[166:169], v[190:193], v[26:29]
	v_mfma_f32_16x16x32_bf16 v[14:17], v[152:155], v[202:205], v[14:17]
	v_mfma_f32_16x16x32_bf16 v[10:13], v[166:169], v[202:205], v[10:13]
	v_mfma_f32_16x16x32_bf16 v[62:65], v[162:165], v[178:181], v[62:65]
	v_mfma_f32_16x16x32_bf16 v[58:61], v[170:173], v[178:181], v[58:61]
	v_mfma_f32_16x16x32_bf16 v[46:49], v[162:165], v[186:189], v[46:49]
	v_mfma_f32_16x16x32_bf16 v[42:45], v[170:173], v[186:189], v[42:45]
	v_mfma_f32_16x16x32_bf16 v[30:33], v[162:165], v[198:201], v[30:33]
	v_mfma_f32_16x16x32_bf16 v[26:29], v[170:173], v[198:201], v[26:29]
	v_mfma_f32_16x16x32_bf16 v[14:17], v[162:165], v[206:209], v[14:17]
	v_mfma_f32_16x16x32_bf16 v[10:13], v[170:173], v[206:209], v[10:13]
	s_barrier
	s_add_u32 s0, s64, 0x40000
	s_addc_u32 s1, s65, 0
	s_add_i32 s33, s36, s38
	v_lshl_add_u64 v[152:153], s[0:1], 0, v[132:133]
	s_mov_b32 m0, s33
	s_nop 0
	global_load_lds_dwordx4 v[152:153], off
	v_lshl_add_u64 v[152:153], s[0:1], 0, v[136:137]
	s_add_i32 m0, s33, 0x2000
	s_nop 0
	global_load_lds_dwordx4 v[152:153], off
	v_add_u32_e32 v170, 0x18000, v158
	ds_read_b128 v[152:155], v170
	ds_read_b128 v[162:165], v170 offset:1024
	ds_read_b128 v[166:169], v170 offset:2048
	ds_read_b128 v[170:173], v170 offset:3072
	s_waitcnt vmcnt(6)
	s_barrier
	v_mfma_f32_16x16x32_bf16 v[54:57], v[210:213], v[174:177], v[54:57]
	v_mfma_f32_16x16x32_bf16 v[50:53], v[218:221], v[174:177], v[50:53]
	v_mfma_f32_16x16x32_bf16 v[38:41], v[210:213], v[182:185], v[38:41]
	v_mfma_f32_16x16x32_bf16 v[34:37], v[218:221], v[182:185], v[34:37]
	v_mfma_f32_16x16x32_bf16 v[22:25], v[210:213], v[190:193], v[22:25]
	v_mfma_f32_16x16x32_bf16 v[18:21], v[218:221], v[190:193], v[18:21]
	v_mfma_f32_16x16x32_bf16 v[6:9], v[210:213], v[202:205], v[6:9]
	v_mfma_f32_16x16x32_bf16 v[2:5], v[218:221], v[202:205], v[2:5]
	v_mfma_f32_16x16x32_bf16 v[54:57], v[214:217], v[178:181], v[54:57]
	v_mfma_f32_16x16x32_bf16 v[50:53], v[238:241], v[178:181], v[50:53]
	v_mfma_f32_16x16x32_bf16 v[38:41], v[214:217], v[186:189], v[38:41]
	v_mfma_f32_16x16x32_bf16 v[34:37], v[238:241], v[186:189], v[34:37]
	v_mfma_f32_16x16x32_bf16 v[22:25], v[214:217], v[198:201], v[22:25]
	v_mfma_f32_16x16x32_bf16 v[18:21], v[238:241], v[198:201], v[18:21]
	v_mfma_f32_16x16x32_bf16 v[6:9], v[214:217], v[206:209], v[6:9]
	v_mfma_f32_16x16x32_bf16 v[2:5], v[238:241], v[206:209], v[2:5]
	s_add_i32 s33, 0, 0x18000
	s_barrier
	s_add_u32 s0, s66, 0x40000
	s_addc_u32 s1, s67, 0
	s_mov_b32 m0, s69
	v_lshl_add_u64 v[210:211], s[0:1], 0, v[130:131]
	ds_read_b128 v[174:177], v161 offset:32768
	ds_read_b128 v[178:181], v161 offset:33792
	ds_read_b128 v[182:185], v161 offset:34816
	ds_read_b128 v[186:189], v161 offset:35840
	ds_read_b128 v[190:193], v161 offset:36864
	ds_read_b128 v[198:201], v161 offset:37888
	ds_read_b128 v[202:205], v161 offset:38912
	ds_read_b128 v[206:209], v161 offset:39936
	global_load_lds_dwordx4 v[210:211], off
	v_lshl_add_u64 v[210:211], s[0:1], 0, v[134:135]
	s_mov_b32 m0, s70
	s_nop 0
	global_load_lds_dwordx4 v[210:211], off
	s_waitcnt lgkmcnt(8)
	s_barrier
	s_waitcnt lgkmcnt(0)
	v_mfma_f32_16x16x32_bf16 v[126:129], v[152:155], v[174:177], v[126:129]
	v_mfma_f32_16x16x32_bf16 v[122:125], v[166:169], v[174:177], v[122:125]
	v_mfma_f32_16x16x32_bf16 v[110:113], v[152:155], v[182:185], v[110:113]
	v_mfma_f32_16x16x32_bf16 v[106:109], v[166:169], v[182:185], v[106:109]
	v_mfma_f32_16x16x32_bf16 v[94:97], v[152:155], v[190:193], v[94:97]
	v_mfma_f32_16x16x32_bf16 v[90:93], v[166:169], v[190:193], v[90:93]
	v_mfma_f32_16x16x32_bf16 v[78:81], v[152:155], v[202:205], v[78:81]
	v_mfma_f32_16x16x32_bf16 v[74:77], v[166:169], v[202:205], v[74:77]
	v_mfma_f32_16x16x32_bf16 v[126:129], v[162:165], v[178:181], v[126:129]
	v_mfma_f32_16x16x32_bf16 v[122:125], v[170:173], v[178:181], v[122:125]
	v_mfma_f32_16x16x32_bf16 v[110:113], v[162:165], v[186:189], v[110:113]
	v_mfma_f32_16x16x32_bf16 v[106:109], v[170:173], v[186:189], v[106:109]
	v_mfma_f32_16x16x32_bf16 v[94:97], v[162:165], v[198:201], v[94:97]
	v_mfma_f32_16x16x32_bf16 v[90:93], v[170:173], v[198:201], v[90:93]
	v_mfma_f32_16x16x32_bf16 v[78:81], v[162:165], v[206:209], v[78:81]
	v_mfma_f32_16x16x32_bf16 v[74:77], v[170:173], v[206:209], v[74:77]
	s_barrier
	s_add_i32 s36, 0, 0x1c000
	s_add_i32 s0, s33, s38
	v_add_u32_e32 v194, s36, v158
	v_lshl_add_u64 v[156:157], v[156:157], 0, s[54:55]
	s_mov_b32 m0, s0
	ds_read_b128 v[210:213], v194
	ds_read_b128 v[214:217], v194 offset:1024
	ds_read_b128 v[218:221], v194 offset:2048
	ds_read_b128 v[238:241], v194 offset:3072
	global_load_lds_dwordx4 v[156:157], off
	v_lshl_add_u64 v[156:157], v[242:243], 0, s[54:55]
	s_add_i32 m0, s0, 0x2000
	s_nop 0
	global_load_lds_dwordx4 v[156:157], off
	s_barrier
	s_waitcnt lgkmcnt(0)
	v_mfma_f32_16x16x32_bf16 v[118:121], v[210:213], v[174:177], v[118:121]
	v_mfma_f32_16x16x32_bf16 v[114:117], v[218:221], v[174:177], v[114:117]
	v_mfma_f32_16x16x32_bf16 v[102:105], v[210:213], v[182:185], v[102:105]
	v_mfma_f32_16x16x32_bf16 v[98:101], v[218:221], v[182:185], v[98:101]
	v_mfma_f32_16x16x32_bf16 v[86:89], v[210:213], v[190:193], v[86:89]
	v_mfma_f32_16x16x32_bf16 v[82:85], v[218:221], v[190:193], v[82:85]
	v_mfma_f32_16x16x32_bf16 v[70:73], v[210:213], v[202:205], v[70:73]
	v_mfma_f32_16x16x32_bf16 v[66:69], v[218:221], v[202:205], v[66:69]
	v_mfma_f32_16x16x32_bf16 v[118:121], v[214:217], v[178:181], v[118:121]
	v_mfma_f32_16x16x32_bf16 v[114:117], v[238:241], v[178:181], v[114:117]
	v_mfma_f32_16x16x32_bf16 v[102:105], v[214:217], v[186:189], v[102:105]
	v_mfma_f32_16x16x32_bf16 v[98:101], v[238:241], v[186:189], v[98:101]
	v_mfma_f32_16x16x32_bf16 v[86:89], v[214:217], v[198:201], v[86:89]
	v_mfma_f32_16x16x32_bf16 v[82:85], v[238:241], v[198:201], v[82:85]
	v_mfma_f32_16x16x32_bf16 v[70:73], v[214:217], v[206:209], v[70:73]
	v_mfma_f32_16x16x32_bf16 v[66:69], v[238:241], v[206:209], v[66:69]
	s_mov_b32 m0, s71
	v_lshl_add_u64 v[156:157], v[244:245], 0, s[54:55]
	s_barrier
	ds_read_b128 v[174:177], v161 offset:49152
	ds_read_b128 v[178:181], v161 offset:50176
	ds_read_b128 v[182:185], v161 offset:51200
	ds_read_b128 v[186:189], v161 offset:52224
	ds_read_b128 v[190:193], v161 offset:53248
	ds_read_b128 v[198:201], v161 offset:54272
	ds_read_b128 v[202:205], v161 offset:55296
	ds_read_b128 v[206:209], v161 offset:56320
	global_load_lds_dwordx4 v[156:157], off
	v_lshl_add_u64 v[156:157], v[246:247], 0, s[54:55]
	s_mov_b32 m0, s72
	s_nop 0
	global_load_lds_dwordx4 v[156:157], off
	s_waitcnt vmcnt(10)
	s_barrier
	s_waitcnt lgkmcnt(0)
	v_mfma_f32_16x16x32_bf16 v[62:65], v[152:155], v[174:177], v[62:65]
	v_mfma_f32_16x16x32_bf16 v[58:61], v[166:169], v[174:177], v[58:61]
	v_mfma_f32_16x16x32_bf16 v[46:49], v[152:155], v[182:185], v[46:49]
	v_mfma_f32_16x16x32_bf16 v[42:45], v[166:169], v[182:185], v[42:45]
	v_mfma_f32_16x16x32_bf16 v[30:33], v[152:155], v[190:193], v[30:33]
	v_mfma_f32_16x16x32_bf16 v[26:29], v[166:169], v[190:193], v[26:29]
	v_mfma_f32_16x16x32_bf16 v[14:17], v[152:155], v[202:205], v[14:17]
	v_mfma_f32_16x16x32_bf16 v[10:13], v[166:169], v[202:205], v[10:13]
	v_mfma_f32_16x16x32_bf16 v[62:65], v[162:165], v[178:181], v[62:65]
	v_mfma_f32_16x16x32_bf16 v[58:61], v[170:173], v[178:181], v[58:61]
	v_mfma_f32_16x16x32_bf16 v[46:49], v[162:165], v[186:189], v[46:49]
	v_mfma_f32_16x16x32_bf16 v[42:45], v[170:173], v[186:189], v[42:45]
	v_mfma_f32_16x16x32_bf16 v[30:33], v[162:165], v[198:201], v[30:33]
	v_mfma_f32_16x16x32_bf16 v[26:29], v[170:173], v[198:201], v[26:29]
	v_mfma_f32_16x16x32_bf16 v[14:17], v[162:165], v[206:209], v[14:17]
	v_mfma_f32_16x16x32_bf16 v[10:13], v[170:173], v[206:209], v[10:13]
	s_barrier
	s_add_u32 s0, s64, 0x40080
	s_addc_u32 s1, s65, 0
	s_add_i32 s33, s36, s38
	v_lshl_add_u64 v[152:153], s[0:1], 0, v[132:133]
	s_mov_b32 m0, s33
	s_nop 0
	global_load_lds_dwordx4 v[152:153], off
	v_lshl_add_u64 v[152:153], s[0:1], 0, v[136:137]
	s_add_i32 m0, s33, 0x2000
	s_nop 0
	global_load_lds_dwordx4 v[152:153], off
	v_add_u32_e32 v170, 0x10000, v158
	ds_read_b128 v[152:155], v170
	ds_read_b128 v[162:165], v170 offset:1024
	ds_read_b128 v[166:169], v170 offset:2048
	ds_read_b128 v[170:173], v170 offset:3072
	s_waitcnt vmcnt(6)
	s_barrier
	v_mfma_f32_16x16x32_bf16 v[54:57], v[210:213], v[174:177], v[54:57]
	v_mfma_f32_16x16x32_bf16 v[50:53], v[218:221], v[174:177], v[50:53]
	v_mfma_f32_16x16x32_bf16 v[38:41], v[210:213], v[182:185], v[38:41]
	v_mfma_f32_16x16x32_bf16 v[34:37], v[218:221], v[182:185], v[34:37]
	v_mfma_f32_16x16x32_bf16 v[22:25], v[210:213], v[190:193], v[22:25]
	v_mfma_f32_16x16x32_bf16 v[18:21], v[218:221], v[190:193], v[18:21]
	v_mfma_f32_16x16x32_bf16 v[6:9], v[210:213], v[202:205], v[6:9]
	v_mfma_f32_16x16x32_bf16 v[2:5], v[218:221], v[202:205], v[2:5]
	v_mfma_f32_16x16x32_bf16 v[54:57], v[214:217], v[178:181], v[54:57]
	v_mfma_f32_16x16x32_bf16 v[50:53], v[238:241], v[178:181], v[50:53]
	v_mfma_f32_16x16x32_bf16 v[38:41], v[214:217], v[186:189], v[38:41]
	v_mfma_f32_16x16x32_bf16 v[34:37], v[238:241], v[186:189], v[34:37]
	v_mfma_f32_16x16x32_bf16 v[22:25], v[214:217], v[198:201], v[22:25]
	v_mfma_f32_16x16x32_bf16 v[18:21], v[238:241], v[198:201], v[18:21]
	v_mfma_f32_16x16x32_bf16 v[6:9], v[214:217], v[206:209], v[6:9]
	v_mfma_f32_16x16x32_bf16 v[2:5], v[238:241], v[206:209], v[2:5]
	s_add_i32 s79, s79, 2
	s_add_u32 s30, s30, 0x100
	s_addc_u32 s31, s31, 0
	s_add_u32 s77, s77, 0x100
	s_addc_u32 s78, s78, 0
	s_cmp_gt_u32 s79, 13
	s_barrier
	s_cbranch_scc0 .LBB0_389
	s_waitcnt lgkmcnt(0)
	s_lshl_b32 s0, s8, 8
	v_lshl_add_u32 v162, s6, 8, v139
	v_or_b32_e32 v152, s0, v138
	s_addk_i32 s0, 0xf200
	v_ashrrev_i32_e32 v155, 5, v162
	s_lshr_b32 s23, s0, 8
	v_and_b32_e32 v155, -8, v155
	v_add_u32_e32 v156, s23, v155
	v_add_u32_e32 v154, 0xfffffe00, v152
	s_movk_i32 s1, 0x3ff
	v_ashrrev_i32_e32 v157, 31, v156
	v_cmp_lt_u32_e64 s[8:9], s1, v154
	s_movk_i32 s1, 0xdff
	v_ashrrev_i32_e32 v153, 31, v152
	v_lshlrev_b64 v[156:157], 17, v[156:157]
	v_cmp_lt_i32_e64 s[6:7], s1, v152
	v_lshl_add_u64 v[152:153], v[152:153], 1, s[18:19]
	v_lshl_add_u64 v[156:157], s[20:21], 0, v[156:157]
	s_and_saveexec_b64 s[0:1], s[8:9]
	s_xor_b64 s[30:31], exec, s[0:1]
	s_cbranch_execz .LBB0_396
	s_and_saveexec_b64 s[0:1], s[6:7]
	s_xor_b64 s[64:65], exec, s[0:1]
	s_cbranch_execz .LBB0_393
	v_mul_f32_e32 v155, 0xbfb8aa3b, v126
	v_exp_f32_e32 v155, v155
	v_mul_f32_e32 v163, 0xbfb8aa3b, v122
	v_exp_f32_e32 v163, v163
	v_mul_f32_e32 v165, 0xbfb8aa3b, v114
	v_add_f32_e32 v155, 1.0, v155
	v_rcp_f32_e32 v168, v155
	v_add_f32_e32 v155, 1.0, v163
	v_rcp_f32_e32 v170, v155
	v_mul_f32_e32 v155, 0xbfb8aa3b, v127
	v_exp_f32_e32 v155, v155
	v_mul_f32_e32 v163, 0xbfb8aa3b, v123
	v_exp_f32_e32 v163, v163
	v_mul_f32_e32 v164, 0xbfb8aa3b, v118
	v_exp_f32_e32 v166, v165
	v_mul_f32_e32 v165, 0xbfb8aa3b, v119
	v_exp_f32_e32 v164, v164
	v_exp_f32_e32 v165, v165
	v_mul_f32_e32 v167, 0xbfb8aa3b, v115
	v_add_f32_e32 v155, 1.0, v155
	v_rcp_f32_e32 v169, v155
	v_exp_f32_e32 v167, v167
	v_add_f32_e32 v163, 1.0, v163
	v_rcp_f32_e32 v171, v163
	v_pk_add_f32 v[164:165], v[164:165], 1.0 op_sel_hi:[1,0]
	v_mul_f32_e32 v178, 0xbfb8aa3b, v117
	v_rcp_f32_e32 v155, v164
	v_pk_mul_f32 v[168:169], v[168:169], v[164:165]
	v_rcp_f32_e32 v163, v165
	v_pk_add_f32 v[164:165], v[166:167], 1.0 op_sel_hi:[1,0]
	s_nop 0
	v_rcp_f32_e32 v176, v164
	v_pk_mul_f32 v[166:167], v[170:171], v[164:165]
	v_mul_f32_e32 v164, 0xbfb8aa3b, v128
	v_rcp_f32_e32 v177, v165
	v_exp_f32_e32 v165, v164
	v_mul_f32_e32 v164, 0xbfb8aa3b, v124
	v_exp_f32_e32 v171, v164
	v_mul_f32_e32 v164, 0xbfb8aa3b, v120
	v_add_f32_e32 v165, 1.0, v165
	v_rcp_f32_e32 v172, v165
	v_add_f32_e32 v165, 1.0, v171
	v_rcp_f32_e32 v174, v165
	v_mul_f32_e32 v165, 0xbfb8aa3b, v129
	v_exp_f32_e32 v171, v165
	v_mul_f32_e32 v165, 0xbfb8aa3b, v125
	v_exp_f32_e32 v175, v165
	v_mul_f32_e32 v165, 0xbfb8aa3b, v121
	v_exp_f32_e32 v164, v164
	v_exp_f32_e32 v165, v165
	v_add_f32_e32 v171, 1.0, v171
	v_rcp_f32_e32 v173, v171
	v_mul_f32_e32 v170, 0xbfb8aa3b, v116
	v_exp_f32_e32 v170, v170
	v_exp_f32_e32 v171, v178
	v_pk_add_f32 v[164:165], v[164:165], 1.0 op_sel_hi:[1,0]
	v_cvt_pk_bf16_f32 v166, v166, v167
	v_rcp_f32_e32 v178, v164
	v_pk_mul_f32 v[172:173], v[172:173], v[164:165]
	v_add_f32_e32 v164, 1.0, v175
	v_rcp_f32_e32 v175, v164
	v_rcp_f32_e32 v179, v165
	v_pk_add_f32 v[164:165], v[170:171], 1.0 op_sel_hi:[1,0]
	s_nop 0
	v_rcp_f32_e32 v180, v164
	v_rcp_f32_e32 v181, v165
	v_pk_mul_f32 v[170:171], v[174:175], v[164:165]
	v_lshl_add_u64 v[174:175], v[140:141], 1, v[156:157]
	v_cvt_pk_bf16_f32 v164, v168, v169
	v_cvt_pk_bf16_f32 v165, v172, v173
	v_cvt_pk_bf16_f32 v167, v170, v171
	v_add_co_u32_e32 v168, vcc, 0x10000, v174
	global_store_dwordx4 v[174:175], v[164:167], off
	s_nop 0
	v_addc_co_u32_e32 v169, vcc, 0, v175, vcc
	v_cvt_pk_bf16_f32 v164, v155, v163
	v_cvt_pk_bf16_f32 v165, v178, v179
	v_cvt_pk_bf16_f32 v166, v176, v177
	v_cvt_pk_bf16_f32 v167, v180, v181
	global_store_dwordx4 v[168:169], v[164:167], off

.LBB0_475:
	s_add_u32 s0, s30, 0xfffc0080
	s_addc_u32 s1, s31, -1
	s_add_i32 s33, 0, 0x10000
	s_cmp_eq_u32 s79, 12
	s_cselect_b32 s67, s5, s1
	s_cselect_b32 s66, s7, s0
	s_cselect_b32 s65, s9, s78
	s_cselect_b32 s64, s23, s77
	v_lshl_add_u64 v[156:157], s[30:31], 0, v[148:149]
	s_add_i32 m0, s40, 0xc000
	ds_read_b128 v[174:177], v161
	ds_read_b128 v[178:181], v161 offset:1024
	ds_read_b128 v[182:185], v161 offset:2048
	ds_read_b128 v[186:189], v161 offset:3072
	ds_read_b128 v[190:193], v161 offset:4096
	ds_read_b128 v[198:201], v161 offset:5120
	ds_read_b128 v[202:205], v161 offset:6144
	ds_read_b128 v[206:209], v161 offset:7168
	global_load_lds_dwordx4 v[156:157], off
	v_lshl_add_u64 v[156:157], s[30:31], 0, v[150:151]
	s_add_i32 m0, s40, 0xe000
	s_nop 0
	global_load_lds_dwordx4 v[156:157], off
	s_waitcnt lgkmcnt(8)
	s_barrier
	s_waitcnt lgkmcnt(0)
	v_mfma_f32_16x16x32_bf16 v[126:129], v[152:155], v[174:177], v[126:129]
	v_mfma_f32_16x16x32_bf16 v[122:125], v[166:169], v[174:177], v[122:125]
	v_mfma_f32_16x16x32_bf16 v[110:113], v[152:155], v[182:185], v[110:113]
	v_mfma_f32_16x16x32_bf16 v[106:109], v[166:169], v[182:185], v[106:109]
	v_mfma_f32_16x16x32_bf16 v[94:97], v[152:155], v[190:193], v[94:97]
	v_mfma_f32_16x16x32_bf16 v[90:93], v[166:169], v[190:193], v[90:93]
	v_mfma_f32_16x16x32_bf16 v[78:81], v[152:155], v[202:205], v[78:81]
	v_mfma_f32_16x16x32_bf16 v[74:77], v[166:169], v[202:205], v[74:77]
	v_mfma_f32_16x16x32_bf16 v[126:129], v[162:165], v[178:181], v[126:129]
	v_mfma_f32_16x16x32_bf16 v[122:125], v[170:173], v[178:181], v[122:125]
	v_mfma_f32_16x16x32_bf16 v[110:113], v[162:165], v[186:189], v[110:113]
	v_mfma_f32_16x16x32_bf16 v[106:109], v[170:173], v[186:189], v[106:109]
	v_mfma_f32_16x16x32_bf16 v[94:97], v[162:165], v[198:201], v[94:97]
	v_mfma_f32_16x16x32_bf16 v[90:93], v[170:173], v[198:201], v[90:93]
	v_mfma_f32_16x16x32_bf16 v[78:81], v[162:165], v[206:209], v[78:81]
	v_mfma_f32_16x16x32_bf16 v[74:77], v[170:173], v[206:209], v[74:77]
	s_barrier
	s_add_i32 s36, 0, 0x14000
	v_add_u32_e32 v156, s36, v158
	s_add_i32 s0, s33, s38
	ds_read_b128 v[210:213], v156
	ds_read_b128 v[214:217], v156 offset:1024
	ds_read_b128 v[218:221], v156 offset:2048
	ds_read_b128 v[238:241], v156 offset:3072
	v_lshl_add_u64 v[156:157], s[64:65], 0, v[132:133]
	s_mov_b32 m0, s0
	v_lshl_add_u64 v[242:243], s[64:65], 0, v[136:137]
	global_load_lds_dwordx4 v[156:157], off
	s_add_i32 m0, s0, 0x2000
	s_nop 0
	global_load_lds_dwordx4 v[242:243], off
	s_barrier
	s_waitcnt lgkmcnt(0)
	v_mfma_f32_16x16x32_bf16 v[118:121], v[210:213], v[174:177], v[118:121]
	v_mfma_f32_16x16x32_bf16 v[114:117], v[218:221], v[174:177], v[114:117]
	v_mfma_f32_16x16x32_bf16 v[102:105], v[210:213], v[182:185], v[102:105]
	v_mfma_f32_16x16x32_bf16 v[98:101], v[218:221], v[182:185], v[98:101]
	v_mfma_f32_16x16x32_bf16 v[86:89], v[210:213], v[190:193], v[86:89]
	v_mfma_f32_16x16x32_bf16 v[82:85], v[218:221], v[190:193], v[82:85]
	v_mfma_f32_16x16x32_bf16 v[70:73], v[210:213], v[202:205], v[70:73]
	v_mfma_f32_16x16x32_bf16 v[66:69], v[218:221], v[202:205], v[66:69]
	v_mfma_f32_16x16x32_bf16 v[118:121], v[214:217], v[178:181], v[118:121]
	v_mfma_f32_16x16x32_bf16 v[114:117], v[238:241], v[178:181], v[114:117]
	v_mfma_f32_16x16x32_bf16 v[102:105], v[214:217], v[186:189], v[102:105]
	v_mfma_f32_16x16x32_bf16 v[98:101], v[238:241], v[186:189], v[98:101]
	v_mfma_f32_16x16x32_bf16 v[86:89], v[214:217], v[198:201], v[86:89]
	v_mfma_f32_16x16x32_bf16 v[82:85], v[238:241], v[198:201], v[82:85]
	v_mfma_f32_16x16x32_bf16 v[70:73], v[214:217], v[206:209], v[70:73]
	v_mfma_f32_16x16x32_bf16 v[66:69], v[238:241], v[206:209], v[66:69]
	s_mov_b32 m0, s40
	v_lshl_add_u64 v[244:245], s[66:67], 0, v[130:131]
	s_barrier
	ds_read_b128 v[174:177], v161 offset:16384
	ds_read_b128 v[178:181], v161 offset:17408
	ds_read_b128 v[182:185], v161 offset:18432
	ds_read_b128 v[186:189], v161 offset:19456
	ds_read_b128 v[190:193], v161 offset:20480
	ds_read_b128 v[198:201], v161 offset:21504
	ds_read_b128 v[202:205], v161 offset:22528
	ds_read_b128 v[206:209], v161 offset:23552
	global_load_lds_dwordx4 v[244:245], off
	v_lshl_add_u64 v[246:247], s[66:67], 0, v[134:135]
	s_mov_b32 m0, s43
	s_nop 0
	global_load_lds_dwordx4 v[246:247], off
	s_waitcnt vmcnt(10)
	s_barrier
	s_waitcnt lgkmcnt(0)
	v_mfma_f32_16x16x32_bf16 v[62:65], v[152:155], v[174:177], v[62:65]
	v_mfma_f32_16x16x32_bf16 v[58:61], v[166:169], v[174:177], v[58:61]
	v_mfma_f32_16x16x32_bf16 v[46:49], v[152:155], v[182:185], v[46:49]
	v_mfma_f32_16x16x32_bf16 v[42:45], v[166:169], v[182:185], v[42:45]
	v_mfma_f32_16x16x32_bf16 v[30:33], v[152:155], v[190:193], v[30:33]
	v_mfma_f32_16x16x32_bf16 v[26:29], v[166:169], v[190:193], v[26:29]
	v_mfma_f32_16x16x32_bf16 v[14:17], v[152:155], v[202:205], v[14:17]
	v_mfma_f32_16x16x32_bf16 v[10:13], v[166:169], v[202:205], v[10:13]
	v_mfma_f32_16x16x32_bf16 v[62:65], v[162:165], v[178:181], v[62:65]
	v_mfma_f32_16x16x32_bf16 v[58:61], v[170:173], v[178:181], v[58:61]
	v_mfma_f32_16x16x32_bf16 v[46:49], v[162:165], v[186:189], v[46:49]
	v_mfma_f32_16x16x32_bf16 v[42:45], v[170:173], v[186:189], v[42:45]
	v_mfma_f32_16x16x32_bf16 v[30:33], v[162:165], v[198:201], v[30:33]
	v_mfma_f32_16x16x32_bf16 v[26:29], v[170:173], v[198:201], v[26:29]
	v_mfma_f32_16x16x32_bf16 v[14:17], v[162:165], v[206:209], v[14:17]
	v_mfma_f32_16x16x32_bf16 v[10:13], v[170:173], v[206:209], v[10:13]
	s_barrier
	s_add_u32 s0, s64, 0x40000
	s_addc_u32 s1, s65, 0
	s_add_i32 s33, s36, s38
	v_lshl_add_u64 v[152:153], s[0:1], 0, v[132:133]
	s_mov_b32 m0, s33
	s_nop 0
	global_load_lds_dwordx4 v[152:153], off
	v_lshl_add_u64 v[152:153], s[0:1], 0, v[136:137]
	s_add_i32 m0, s33, 0x2000
	s_nop 0
	global_load_lds_dwordx4 v[152:153], off
	v_add_u32_e32 v170, 0x18000, v158
	ds_read_b128 v[152:155], v170
	ds_read_b128 v[162:165], v170 offset:1024
	ds_read_b128 v[166:169], v170 offset:2048
	ds_read_b128 v[170:173], v170 offset:3072
	s_waitcnt vmcnt(6)
	s_barrier
	v_mfma_f32_16x16x32_bf16 v[54:57], v[210:213], v[174:177], v[54:57]
	v_mfma_f32_16x16x32_bf16 v[50:53], v[218:221], v[174:177], v[50:53]
	v_mfma_f32_16x16x32_bf16 v[38:41], v[210:213], v[182:185], v[38:41]
	v_mfma_f32_16x16x32_bf16 v[34:37], v[218:221], v[182:185], v[34:37]
	v_mfma_f32_16x16x32_bf16 v[22:25], v[210:213], v[190:193], v[22:25]
	v_mfma_f32_16x16x32_bf16 v[18:21], v[218:221], v[190:193], v[18:21]
	v_mfma_f32_16x16x32_bf16 v[6:9], v[210:213], v[202:205], v[6:9]
	v_mfma_f32_16x16x32_bf16 v[2:5], v[218:221], v[202:205], v[2:5]
	v_mfma_f32_16x16x32_bf16 v[54:57], v[214:217], v[178:181], v[54:57]
	v_mfma_f32_16x16x32_bf16 v[50:53], v[238:241], v[178:181], v[50:53]
	v_mfma_f32_16x16x32_bf16 v[38:41], v[214:217], v[186:189], v[38:41]
	v_mfma_f32_16x16x32_bf16 v[34:37], v[238:241], v[186:189], v[34:37]
	v_mfma_f32_16x16x32_bf16 v[22:25], v[214:217], v[198:201], v[22:25]
	v_mfma_f32_16x16x32_bf16 v[18:21], v[238:241], v[198:201], v[18:21]
	v_mfma_f32_16x16x32_bf16 v[6:9], v[214:217], v[206:209], v[6:9]
	v_mfma_f32_16x16x32_bf16 v[2:5], v[238:241], v[206:209], v[2:5]
	s_add_i32 s33, 0, 0x18000
	s_barrier
	s_add_u32 s0, s66, 0x40000
	s_addc_u32 s1, s67, 0
	s_mov_b32 m0, s69
	v_lshl_add_u64 v[210:211], s[0:1], 0, v[130:131]
	ds_read_b128 v[174:177], v161 offset:32768
	ds_read_b128 v[178:181], v161 offset:33792
	ds_read_b128 v[182:185], v161 offset:34816
	ds_read_b128 v[186:189], v161 offset:35840
	ds_read_b128 v[190:193], v161 offset:36864
	ds_read_b128 v[198:201], v161 offset:37888
	ds_read_b128 v[202:205], v161 offset:38912
	ds_read_b128 v[206:209], v161 offset:39936
	global_load_lds_dwordx4 v[210:211], off
	v_lshl_add_u64 v[210:211], s[0:1], 0, v[134:135]
	s_mov_b32 m0, s70
	s_nop 0
	global_load_lds_dwordx4 v[210:211], off
	s_waitcnt lgkmcnt(8)
	s_barrier
	s_waitcnt lgkmcnt(0)
	v_mfma_f32_16x16x32_bf16 v[126:129], v[152:155], v[174:177], v[126:129]
	v_mfma_f32_16x16x32_bf16 v[122:125], v[166:169], v[174:177], v[122:125]
	v_mfma_f32_16x16x32_bf16 v[110:113], v[152:155], v[182:185], v[110:113]
	v_mfma_f32_16x16x32_bf16 v[106:109], v[166:169], v[182:185], v[106:109]
	v_mfma_f32_16x16x32_bf16 v[94:97], v[152:155], v[190:193], v[94:97]
	v_mfma_f32_16x16x32_bf16 v[90:93], v[166:169], v[190:193], v[90:93]
	v_mfma_f32_16x16x32_bf16 v[78:81], v[152:155], v[202:205], v[78:81]
	v_mfma_f32_16x16x32_bf16 v[74:77], v[166:169], v[202:205], v[74:77]
	v_mfma_f32_16x16x32_bf16 v[126:129], v[162:165], v[178:181], v[126:129]
	v_mfma_f32_16x16x32_bf16 v[122:125], v[170:173], v[178:181], v[122:125]
	v_mfma_f32_16x16x32_bf16 v[110:113], v[162:165], v[186:189], v[110:113]
	v_mfma_f32_16x16x32_bf16 v[106:109], v[170:173], v[186:189], v[106:109]
	v_mfma_f32_16x16x32_bf16 v[94:97], v[162:165], v[198:201], v[94:97]
	v_mfma_f32_16x16x32_bf16 v[90:93], v[170:173], v[198:201], v[90:93]
	v_mfma_f32_16x16x32_bf16 v[78:81], v[162:165], v[206:209], v[78:81]
	v_mfma_f32_16x16x32_bf16 v[74:77], v[170:173], v[206:209], v[74:77]
	s_barrier
	s_add_i32 s36, 0, 0x1c000
	s_add_i32 s0, s33, s38
	v_add_u32_e32 v194, s36, v158
	v_lshl_add_u64 v[156:157], v[156:157], 0, s[54:55]
	s_mov_b32 m0, s0
	ds_read_b128 v[210:213], v194
	ds_read_b128 v[214:217], v194 offset:1024
	ds_read_b128 v[218:221], v194 offset:2048
	ds_read_b128 v[238:241], v194 offset:3072
	global_load_lds_dwordx4 v[156:157], off
	v_lshl_add_u64 v[156:157], v[242:243], 0, s[54:55]
	s_add_i32 m0, s0, 0x2000
	s_nop 0
	global_load_lds_dwordx4 v[156:157], off
	s_barrier
	s_waitcnt lgkmcnt(0)
	v_mfma_f32_16x16x32_bf16 v[118:121], v[210:213], v[174:177], v[118:121]
	v_mfma_f32_16x16x32_bf16 v[114:117], v[218:221], v[174:177], v[114:117]
	v_mfma_f32_16x16x32_bf16 v[102:105], v[210:213], v[182:185], v[102:105]
	v_mfma_f32_16x16x32_bf16 v[98:101], v[218:221], v[182:185], v[98:101]
	v_mfma_f32_16x16x32_bf16 v[86:89], v[210:213], v[190:193], v[86:89]
	v_mfma_f32_16x16x32_bf16 v[82:85], v[218:221], v[190:193], v[82:85]
	v_mfma_f32_16x16x32_bf16 v[70:73], v[210:213], v[202:205], v[70:73]
	v_mfma_f32_16x16x32_bf16 v[66:69], v[218:221], v[202:205], v[66:69]
	v_mfma_f32_16x16x32_bf16 v[118:121], v[214:217], v[178:181], v[118:121]
	v_mfma_f32_16x16x32_bf16 v[114:117], v[238:241], v[178:181], v[114:117]
	v_mfma_f32_16x16x32_bf16 v[102:105], v[214:217], v[186:189], v[102:105]
	v_mfma_f32_16x16x32_bf16 v[98:101], v[238:241], v[186:189], v[98:101]
	v_mfma_f32_16x16x32_bf16 v[86:89], v[214:217], v[198:201], v[86:89]
	v_mfma_f32_16x16x32_bf16 v[82:85], v[238:241], v[198:201], v[82:85]
	v_mfma_f32_16x16x32_bf16 v[70:73], v[214:217], v[206:209], v[70:73]
	v_mfma_f32_16x16x32_bf16 v[66:69], v[238:241], v[206:209], v[66:69]
	s_mov_b32 m0, s71
	v_lshl_add_u64 v[156:157], v[244:245], 0, s[54:55]
	s_barrier
	ds_read_b128 v[174:177], v161 offset:49152
	ds_read_b128 v[178:181], v161 offset:50176
	ds_read_b128 v[182:185], v161 offset:51200
	ds_read_b128 v[186:189], v161 offset:52224
	ds_read_b128 v[190:193], v161 offset:53248
	ds_read_b128 v[198:201], v161 offset:54272
	ds_read_b128 v[202:205], v161 offset:55296
	ds_read_b128 v[206:209], v161 offset:56320
	global_load_lds_dwordx4 v[156:157], off
	v_lshl_add_u64 v[156:157], v[246:247], 0, s[54:55]
	s_mov_b32 m0, s72
	s_nop 0
	global_load_lds_dwordx4 v[156:157], off
	s_waitcnt vmcnt(10)
	s_barrier
	s_waitcnt lgkmcnt(0)
	v_mfma_f32_16x16x32_bf16 v[62:65], v[152:155], v[174:177], v[62:65]
	v_mfma_f32_16x16x32_bf16 v[58:61], v[166:169], v[174:177], v[58:61]
	v_mfma_f32_16x16x32_bf16 v[46:49], v[152:155], v[182:185], v[46:49]
	v_mfma_f32_16x16x32_bf16 v[42:45], v[166:169], v[182:185], v[42:45]
	v_mfma_f32_16x16x32_bf16 v[30:33], v[152:155], v[190:193], v[30:33]
	v_mfma_f32_16x16x32_bf16 v[26:29], v[166:169], v[190:193], v[26:29]
	v_mfma_f32_16x16x32_bf16 v[14:17], v[152:155], v[202:205], v[14:17]
	v_mfma_f32_16x16x32_bf16 v[10:13], v[166:169], v[202:205], v[10:13]
	v_mfma_f32_16x16x32_bf16 v[62:65], v[162:165], v[178:181], v[62:65]
	v_mfma_f32_16x16x32_bf16 v[58:61], v[170:173], v[178:181], v[58:61]
	v_mfma_f32_16x16x32_bf16 v[46:49], v[162:165], v[186:189], v[46:49]
	v_mfma_f32_16x16x32_bf16 v[42:45], v[170:173], v[186:189], v[42:45]
	v_mfma_f32_16x16x32_bf16 v[30:33], v[162:165], v[198:201], v[30:33]
	v_mfma_f32_16x16x32_bf16 v[26:29], v[170:173], v[198:201], v[26:29]
	v_mfma_f32_16x16x32_bf16 v[14:17], v[162:165], v[206:209], v[14:17]
	v_mfma_f32_16x16x32_bf16 v[10:13], v[170:173], v[206:209], v[10:13]
	s_barrier
	s_add_u32 s0, s64, 0x40080
	s_addc_u32 s1, s65, 0
	s_add_i32 s33, s36, s38
	v_lshl_add_u64 v[152:153], s[0:1], 0, v[132:133]
	s_mov_b32 m0, s33
	s_nop 0
	global_load_lds_dwordx4 v[152:153], off
	v_lshl_add_u64 v[152:153], s[0:1], 0, v[136:137]
	s_add_i32 m0, s33, 0x2000
	s_nop 0
	global_load_lds_dwordx4 v[152:153], off
	v_add_u32_e32 v170, 0x10000, v158
	ds_read_b128 v[152:155], v170
	ds_read_b128 v[162:165], v170 offset:1024
	ds_read_b128 v[166:169], v170 offset:2048
	ds_read_b128 v[170:173], v170 offset:3072
	s_waitcnt vmcnt(6)
	s_barrier
	v_mfma_f32_16x16x32_bf16 v[54:57], v[210:213], v[174:177], v[54:57]
	v_mfma_f32_16x16x32_bf16 v[50:53], v[218:221], v[174:177], v[50:53]
	v_mfma_f32_16x16x32_bf16 v[38:41], v[210:213], v[182:185], v[38:41]
	v_mfma_f32_16x16x32_bf16 v[34:37], v[218:221], v[182:185], v[34:37]
	v_mfma_f32_16x16x32_bf16 v[22:25], v[210:213], v[190:193], v[22:25]
	v_mfma_f32_16x16x32_bf16 v[18:21], v[218:221], v[190:193], v[18:21]
	v_mfma_f32_16x16x32_bf16 v[6:9], v[210:213], v[202:205], v[6:9]
	v_mfma_f32_16x16x32_bf16 v[2:5], v[218:221], v[202:205], v[2:5]
	v_mfma_f32_16x16x32_bf16 v[54:57], v[214:217], v[178:181], v[54:57]
	v_mfma_f32_16x16x32_bf16 v[50:53], v[238:241], v[178:181], v[50:53]
	v_mfma_f32_16x16x32_bf16 v[38:41], v[214:217], v[186:189], v[38:41]
	v_mfma_f32_16x16x32_bf16 v[34:37], v[238:241], v[186:189], v[34:37]
	v_mfma_f32_16x16x32_bf16 v[22:25], v[214:217], v[198:201], v[22:25]
	v_mfma_f32_16x16x32_bf16 v[18:21], v[238:241], v[198:201], v[18:21]
	v_mfma_f32_16x16x32_bf16 v[6:9], v[214:217], v[206:209], v[6:9]
	v_mfma_f32_16x16x32_bf16 v[2:5], v[238:241], v[206:209], v[2:5]
	s_add_i32 s79, s79, 2
	s_add_u32 s30, s30, 0x100
	s_addc_u32 s31, s31, 0
	s_add_u32 s77, s77, 0x100
	s_addc_u32 s78, s78, 0
	s_cmp_gt_u32 s79, 13
	s_barrier
	s_cbranch_scc0 .LBB0_475
	s_waitcnt lgkmcnt(0)
	s_lshl_b32 s0, s6, 8
	v_lshl_add_u32 v162, s4, 8, v139
	v_or_b32_e32 v152, s0, v138
	s_addk_i32 s0, 0xf200
	v_ashrrev_i32_e32 v155, 5, v162
	s_lshr_b32 s9, s0, 8
	v_and_b32_e32 v155, -8, v155
	v_add_u32_e32 v154, 0xfffffe00, v152
	s_movk_i32 s1, 0x3ff
	v_add_u32_e32 v156, s9, v155
	v_cmp_lt_u32_e64 s[6:7], s1, v154
	s_movk_i32 s1, 0xdff
	v_ashrrev_i32_e32 v157, 31, v156
	v_cmp_lt_i32_e64 s[4:5], s1, v152
	v_ashrrev_i32_e32 v153, 31, v152
	v_lshlrev_b64 v[156:157], 17, v[156:157]
	s_and_saveexec_b64 s[0:1], s[6:7]
	s_xor_b64 s[30:31], exec, s[0:1]
	s_cbranch_execz .LBB0_482
	s_and_saveexec_b64 s[0:1], s[4:5]
	s_xor_b64 s[64:65], exec, s[0:1]
	s_cbranch_execz .LBB0_479
	v_mul_f32_e32 v155, 0xbfb8aa3b, v126
	v_exp_f32_e32 v155, v155
	v_mul_f32_e32 v163, 0xbfb8aa3b, v122
	v_exp_f32_e32 v163, v163
	v_mul_f32_e32 v165, 0xbfb8aa3b, v114
	v_add_f32_e32 v155, 1.0, v155
	v_rcp_f32_e32 v168, v155
	v_add_f32_e32 v155, 1.0, v163
	v_rcp_f32_e32 v170, v155
	v_mul_f32_e32 v155, 0xbfb8aa3b, v127
	v_exp_f32_e32 v155, v155
	v_mul_f32_e32 v163, 0xbfb8aa3b, v123
	v_exp_f32_e32 v163, v163
	v_mul_f32_e32 v164, 0xbfb8aa3b, v118
	v_exp_f32_e32 v166, v165
	v_mul_f32_e32 v165, 0xbfb8aa3b, v119
	v_exp_f32_e32 v164, v164
	v_exp_f32_e32 v165, v165
	v_mul_f32_e32 v167, 0xbfb8aa3b, v115
	v_add_f32_e32 v155, 1.0, v155
	v_rcp_f32_e32 v169, v155
	v_exp_f32_e32 v167, v167
	v_add_f32_e32 v163, 1.0, v163
	v_rcp_f32_e32 v171, v163
	v_pk_add_f32 v[164:165], v[164:165], 1.0 op_sel_hi:[1,0]
	v_mul_f32_e32 v178, 0xbfb8aa3b, v117
	v_rcp_f32_e32 v155, v164
	v_pk_mul_f32 v[168:169], v[168:169], v[164:165]
	v_rcp_f32_e32 v163, v165
	v_pk_add_f32 v[164:165], v[166:167], 1.0 op_sel_hi:[1,0]
	s_nop 0
	v_rcp_f32_e32 v176, v164
	v_pk_mul_f32 v[166:167], v[170:171], v[164:165]
	v_mul_f32_e32 v164, 0xbfb8aa3b, v128
	v_rcp_f32_e32 v177, v165
	v_exp_f32_e32 v165, v164
	v_mul_f32_e32 v164, 0xbfb8aa3b, v124
	v_exp_f32_e32 v171, v164
	v_mul_f32_e32 v164, 0xbfb8aa3b, v120
	v_add_f32_e32 v165, 1.0, v165
	v_rcp_f32_e32 v172, v165
	v_add_f32_e32 v165, 1.0, v171
	v_rcp_f32_e32 v174, v165
	v_mul_f32_e32 v165, 0xbfb8aa3b, v129
	v_exp_f32_e32 v171, v165
	v_mul_f32_e32 v165, 0xbfb8aa3b, v125
	v_exp_f32_e32 v175, v165
	v_mul_f32_e32 v165, 0xbfb8aa3b, v121
	v_exp_f32_e32 v164, v164
	v_exp_f32_e32 v165, v165
	v_add_f32_e32 v171, 1.0, v171
	v_rcp_f32_e32 v173, v171
	v_mul_f32_e32 v170, 0xbfb8aa3b, v116
	v_exp_f32_e32 v170, v170
	v_exp_f32_e32 v171, v178
	v_pk_add_f32 v[164:165], v[164:165], 1.0 op_sel_hi:[1,0]
	v_cvt_pk_bf16_f32 v166, v166, v167
	v_rcp_f32_e32 v178, v164
	v_pk_mul_f32 v[172:173], v[172:173], v[164:165]
	v_add_f32_e32 v164, 1.0, v175
	v_rcp_f32_e32 v175, v164
	v_rcp_f32_e32 v179, v165
	v_pk_add_f32 v[164:165], v[170:171], 1.0 op_sel_hi:[1,0]
	s_nop 0
	v_rcp_f32_e32 v180, v164
	v_rcp_f32_e32 v181, v165
	v_pk_mul_f32 v[170:171], v[174:175], v[164:165]
	v_lshl_add_u64 v[174:175], v[140:141], 0, v[156:157]
	v_cvt_pk_bf16_f32 v164, v168, v169
	v_cvt_pk_bf16_f32 v165, v172, v173
	v_cvt_pk_bf16_f32 v167, v170, v171
	v_add_co_u32_e32 v168, vcc, 0x10000, v174
	global_store_dwordx4 v[174:175], v[164:167], off
	s_nop 0
	v_addc_co_u32_e32 v169, vcc, 0, v175, vcc
	v_cvt_pk_bf16_f32 v164, v155, v163
	v_cvt_pk_bf16_f32 v165, v178, v179
	v_cvt_pk_bf16_f32 v166, v176, v177
	v_cvt_pk_bf16_f32 v167, v180, v181
	global_store_dwordx4 v[168:169], v[164:167], off

.LBB0_1332:
	s_add_u32 s0, s6, 0xfffe0080
	s_addc_u32 s1, s7, -1
	s_add_i32 s33, 0, 0x10000
	s_cmp_eq_u32 s86, 4
	s_cselect_b32 s31, s23, s1
	s_cselect_b32 s30, s22, s0
	s_cselect_b32 s29, s15, s82
	s_cselect_b32 s28, s17, s21
	v_lshl_add_u64 v[178:179], s[6:7], 0, v[214:215]
	s_add_i32 m0, s70, 0xc000
	ds_read_b128 v[146:149], v240
	ds_read_b128 v[150:153], v240 offset:1024
	ds_read_b128 v[154:157], v240 offset:2048
	ds_read_b128 v[158:161], v240 offset:3072
	ds_read_b128 v[162:165], v240 offset:4096
	ds_read_b128 v[166:169], v240 offset:5120
	ds_read_b128 v[170:173], v240 offset:6144
	ds_read_b128 v[174:177], v240 offset:7168
	global_load_lds_dwordx4 v[178:179], off
	v_lshl_add_u64 v[178:179], s[6:7], 0, v[216:217]
	s_add_i32 m0, s70, 0xe000
	s_nop 0
	global_load_lds_dwordx4 v[178:179], off
	s_waitcnt lgkmcnt(8)
	s_barrier
	s_waitcnt lgkmcnt(0)
	v_mfma_f32_16x16x32_bf16 v[62:65], v[130:133], v[146:149], v[62:65]
	v_mfma_f32_16x16x32_bf16 v[58:61], v[138:141], v[146:149], v[58:61]
	v_mfma_f32_16x16x32_bf16 v[54:57], v[130:133], v[154:157], v[54:57]
	v_mfma_f32_16x16x32_bf16 v[50:53], v[138:141], v[154:157], v[50:53]
	v_mfma_f32_16x16x32_bf16 v[46:49], v[130:133], v[162:165], v[46:49]
	v_mfma_f32_16x16x32_bf16 v[42:45], v[138:141], v[162:165], v[42:45]
	v_mfma_f32_16x16x32_bf16 v[38:41], v[130:133], v[170:173], v[38:41]
	v_mfma_f32_16x16x32_bf16 v[34:37], v[138:141], v[170:173], v[34:37]
	v_mfma_f32_16x16x32_bf16 v[62:65], v[134:137], v[150:153], v[62:65]
	v_mfma_f32_16x16x32_bf16 v[58:61], v[142:145], v[150:153], v[58:61]
	v_mfma_f32_16x16x32_bf16 v[54:57], v[134:137], v[158:161], v[54:57]
	v_mfma_f32_16x16x32_bf16 v[50:53], v[142:145], v[158:161], v[50:53]
	v_mfma_f32_16x16x32_bf16 v[46:49], v[134:137], v[166:169], v[46:49]
	v_mfma_f32_16x16x32_bf16 v[42:45], v[142:145], v[166:169], v[42:45]
	v_mfma_f32_16x16x32_bf16 v[38:41], v[134:137], v[174:177], v[38:41]
	v_mfma_f32_16x16x32_bf16 v[34:37], v[142:145], v[174:177], v[34:37]
	s_barrier
	s_add_i32 s36, 0, 0x14000
	s_add_i32 s0, s33, s66
	v_add_u32_e32 v190, s36, v237
	v_lshl_add_u64 v[218:219], s[28:29], 0, v[202:203]
	s_mov_b32 m0, s0
	ds_read_b128 v[178:181], v190
	ds_read_b128 v[182:185], v190 offset:1024
	ds_read_b128 v[186:189], v190 offset:2048
	ds_read_b128 v[190:193], v190 offset:3072
	global_load_lds_dwordx4 v[218:219], off
	v_lshl_add_u64 v[220:221], s[28:29], 0, v[198:199]
	s_add_i32 m0, s0, 0x2000
	s_nop 0
	global_load_lds_dwordx4 v[220:221], off
	s_barrier
	s_waitcnt lgkmcnt(0)
	v_mfma_f32_16x16x32_bf16 v[30:33], v[178:181], v[146:149], v[30:33]
	v_mfma_f32_16x16x32_bf16 v[26:29], v[186:189], v[146:149], v[26:29]
	v_mfma_f32_16x16x32_bf16 v[22:25], v[178:181], v[154:157], v[22:25]
	v_mfma_f32_16x16x32_bf16 v[18:21], v[186:189], v[154:157], v[18:21]
	v_mfma_f32_16x16x32_bf16 v[14:17], v[178:181], v[162:165], v[14:17]
	v_mfma_f32_16x16x32_bf16 v[10:13], v[186:189], v[162:165], v[10:13]
	v_mfma_f32_16x16x32_bf16 v[6:9], v[178:181], v[170:173], v[6:9]
	v_mfma_f32_16x16x32_bf16 v[2:5], v[186:189], v[170:173], v[2:5]
	v_mfma_f32_16x16x32_bf16 v[30:33], v[182:185], v[150:153], v[30:33]
	v_mfma_f32_16x16x32_bf16 v[26:29], v[190:193], v[150:153], v[26:29]
	v_mfma_f32_16x16x32_bf16 v[22:25], v[182:185], v[158:161], v[22:25]
	v_mfma_f32_16x16x32_bf16 v[18:21], v[190:193], v[158:161], v[18:21]
	v_mfma_f32_16x16x32_bf16 v[14:17], v[182:185], v[166:169], v[14:17]
	v_mfma_f32_16x16x32_bf16 v[10:13], v[190:193], v[166:169], v[10:13]
	v_mfma_f32_16x16x32_bf16 v[6:9], v[182:185], v[174:177], v[6:9]
	v_mfma_f32_16x16x32_bf16 v[2:5], v[190:193], v[174:177], v[2:5]
	s_mov_b32 m0, s70
	v_lshl_add_u64 v[224:225], s[30:31], 0, v[204:205]
	s_barrier
	ds_read_b128 v[146:149], v240 offset:16384
	ds_read_b128 v[150:153], v240 offset:17408
	ds_read_b128 v[154:157], v240 offset:18432
	ds_read_b128 v[158:161], v240 offset:19456
	ds_read_b128 v[162:165], v240 offset:20480
	ds_read_b128 v[166:169], v240 offset:21504
	ds_read_b128 v[170:173], v240 offset:22528
	ds_read_b128 v[174:177], v240 offset:23552
	global_load_lds_dwordx4 v[224:225], off
	v_lshl_add_u64 v[230:231], s[30:31], 0, v[200:201]
	s_mov_b32 m0, s71
	s_nop 0
	global_load_lds_dwordx4 v[230:231], off
	s_waitcnt vmcnt(10)
	s_barrier
	s_waitcnt lgkmcnt(0)
	v_mfma_f32_16x16x32_bf16 v[66:69], v[130:133], v[146:149], v[66:69]
	v_mfma_f32_16x16x32_bf16 v[70:73], v[138:141], v[146:149], v[70:73]
	v_mfma_f32_16x16x32_bf16 v[74:77], v[130:133], v[154:157], v[74:77]
	v_mfma_f32_16x16x32_bf16 v[78:81], v[138:141], v[154:157], v[78:81]
	v_mfma_f32_16x16x32_bf16 v[82:85], v[130:133], v[162:165], v[82:85]
	v_mfma_f32_16x16x32_bf16 v[86:89], v[138:141], v[162:165], v[86:89]
	v_mfma_f32_16x16x32_bf16 v[90:93], v[130:133], v[170:173], v[90:93]
	v_mfma_f32_16x16x32_bf16 v[94:97], v[138:141], v[170:173], v[94:97]
	v_mfma_f32_16x16x32_bf16 v[66:69], v[134:137], v[150:153], v[66:69]
	v_mfma_f32_16x16x32_bf16 v[70:73], v[142:145], v[150:153], v[70:73]
	v_mfma_f32_16x16x32_bf16 v[74:77], v[134:137], v[158:161], v[74:77]
	v_mfma_f32_16x16x32_bf16 v[78:81], v[142:145], v[158:161], v[78:81]
	v_mfma_f32_16x16x32_bf16 v[82:85], v[134:137], v[166:169], v[82:85]
	v_mfma_f32_16x16x32_bf16 v[86:89], v[142:145], v[166:169], v[86:89]
	v_mfma_f32_16x16x32_bf16 v[90:93], v[134:137], v[174:177], v[90:93]
	v_mfma_f32_16x16x32_bf16 v[94:97], v[142:145], v[174:177], v[94:97]
	s_barrier
	s_add_u32 s0, s28, 0x20000
	s_addc_u32 s1, s29, 0
	s_add_i32 s33, s36, s66
	v_lshl_add_u64 v[130:131], s[0:1], 0, v[202:203]
	s_mov_b32 m0, s33
	s_nop 0
	global_load_lds_dwordx4 v[130:131], off
	v_lshl_add_u64 v[130:131], s[0:1], 0, v[198:199]
	s_add_i32 m0, s33, 0x2000
	s_nop 0
	global_load_lds_dwordx4 v[130:131], off
	v_add_u32_e32 v142, 0x18000, v237
	ds_read_b128 v[130:133], v142
	ds_read_b128 v[134:137], v142 offset:1024
	ds_read_b128 v[138:141], v142 offset:2048
	ds_read_b128 v[142:145], v142 offset:3072
	s_waitcnt vmcnt(6)
	s_barrier
	v_mfma_f32_16x16x32_bf16 v[98:101], v[178:181], v[146:149], v[98:101]
	v_mfma_f32_16x16x32_bf16 v[102:105], v[186:189], v[146:149], v[102:105]
	v_mfma_f32_16x16x32_bf16 v[106:109], v[178:181], v[154:157], v[106:109]
	v_mfma_f32_16x16x32_bf16 v[110:113], v[186:189], v[154:157], v[110:113]
	v_mfma_f32_16x16x32_bf16 v[114:117], v[178:181], v[162:165], v[114:117]
	v_mfma_f32_16x16x32_bf16 v[118:121], v[186:189], v[162:165], v[118:121]
	v_mfma_f32_16x16x32_bf16 v[122:125], v[178:181], v[170:173], v[122:125]
	v_mfma_f32_16x16x32_bf16 v[126:129], v[186:189], v[170:173], v[126:129]
	v_mfma_f32_16x16x32_bf16 v[98:101], v[182:185], v[150:153], v[98:101]
	v_mfma_f32_16x16x32_bf16 v[102:105], v[190:193], v[150:153], v[102:105]
	v_mfma_f32_16x16x32_bf16 v[106:109], v[182:185], v[158:161], v[106:109]
	v_mfma_f32_16x16x32_bf16 v[110:113], v[190:193], v[158:161], v[110:113]
	v_mfma_f32_16x16x32_bf16 v[114:117], v[182:185], v[166:169], v[114:117]
	v_mfma_f32_16x16x32_bf16 v[118:121], v[190:193], v[166:169], v[118:121]
	v_mfma_f32_16x16x32_bf16 v[122:125], v[182:185], v[174:177], v[122:125]
	v_mfma_f32_16x16x32_bf16 v[126:129], v[190:193], v[174:177], v[126:129]
	s_add_i32 s33, 0, 0x18000
	s_barrier
	s_add_u32 s0, s30, 0x20000
	s_addc_u32 s1, s31, 0
	s_mov_b32 m0, s72
	v_lshl_add_u64 v[178:179], s[0:1], 0, v[204:205]
	ds_read_b128 v[146:149], v240 offset:32768
	ds_read_b128 v[150:153], v240 offset:33792
	ds_read_b128 v[154:157], v240 offset:34816
	ds_read_b128 v[158:161], v240 offset:35840
	ds_read_b128 v[162:165], v240 offset:36864
	ds_read_b128 v[166:169], v240 offset:37888
	ds_read_b128 v[170:173], v240 offset:38912
	ds_read_b128 v[174:177], v240 offset:39936
	global_load_lds_dwordx4 v[178:179], off
	v_lshl_add_u64 v[178:179], s[0:1], 0, v[200:201]
	s_mov_b32 m0, s73
	s_nop 0
	global_load_lds_dwordx4 v[178:179], off
	s_waitcnt lgkmcnt(8)
	s_barrier
	s_waitcnt lgkmcnt(0)
	v_mfma_f32_16x16x32_bf16 v[62:65], v[130:133], v[146:149], v[62:65]
	v_mfma_f32_16x16x32_bf16 v[58:61], v[138:141], v[146:149], v[58:61]
	v_mfma_f32_16x16x32_bf16 v[54:57], v[130:133], v[154:157], v[54:57]
	v_mfma_f32_16x16x32_bf16 v[50:53], v[138:141], v[154:157], v[50:53]
	v_mfma_f32_16x16x32_bf16 v[46:49], v[130:133], v[162:165], v[46:49]
	v_mfma_f32_16x16x32_bf16 v[42:45], v[138:141], v[162:165], v[42:45]
	v_mfma_f32_16x16x32_bf16 v[38:41], v[130:133], v[170:173], v[38:41]
	v_mfma_f32_16x16x32_bf16 v[34:37], v[138:141], v[170:173], v[34:37]
	v_mfma_f32_16x16x32_bf16 v[62:65], v[134:137], v[150:153], v[62:65]
	v_mfma_f32_16x16x32_bf16 v[58:61], v[142:145], v[150:153], v[58:61]
	v_mfma_f32_16x16x32_bf16 v[54:57], v[134:137], v[158:161], v[54:57]
	v_mfma_f32_16x16x32_bf16 v[50:53], v[142:145], v[158:161], v[50:53]
	v_mfma_f32_16x16x32_bf16 v[46:49], v[134:137], v[166:169], v[46:49]
	v_mfma_f32_16x16x32_bf16 v[42:45], v[142:145], v[166:169], v[42:45]
	v_mfma_f32_16x16x32_bf16 v[38:41], v[134:137], v[174:177], v[38:41]
	v_mfma_f32_16x16x32_bf16 v[34:37], v[142:145], v[174:177], v[34:37]
	s_barrier
	s_add_i32 s30, 0, 0x1c000
	s_add_i32 s0, s33, s66
	v_add_u32_e32 v190, s30, v237
	v_lshl_add_u64 v[218:219], v[218:219], 0, s[54:55]
	s_mov_b32 m0, s0
	ds_read_b128 v[178:181], v190
	ds_read_b128 v[182:185], v190 offset:1024
	ds_read_b128 v[186:189], v190 offset:2048
	ds_read_b128 v[190:193], v190 offset:3072
	global_load_lds_dwordx4 v[218:219], off
	v_lshl_add_u64 v[218:219], v[220:221], 0, s[54:55]
	s_add_i32 m0, s0, 0x2000
	s_nop 0
	global_load_lds_dwordx4 v[218:219], off
	s_barrier
	s_waitcnt lgkmcnt(0)
	v_mfma_f32_16x16x32_bf16 v[30:33], v[178:181], v[146:149], v[30:33]
	v_mfma_f32_16x16x32_bf16 v[26:29], v[186:189], v[146:149], v[26:29]
	v_mfma_f32_16x16x32_bf16 v[22:25], v[178:181], v[154:157], v[22:25]
	v_mfma_f32_16x16x32_bf16 v[18:21], v[186:189], v[154:157], v[18:21]
	v_mfma_f32_16x16x32_bf16 v[14:17], v[178:181], v[162:165], v[14:17]
	v_mfma_f32_16x16x32_bf16 v[10:13], v[186:189], v[162:165], v[10:13]
	v_mfma_f32_16x16x32_bf16 v[6:9], v[178:181], v[170:173], v[6:9]
	v_mfma_f32_16x16x32_bf16 v[2:5], v[186:189], v[170:173], v[2:5]
	v_mfma_f32_16x16x32_bf16 v[30:33], v[182:185], v[150:153], v[30:33]
	v_mfma_f32_16x16x32_bf16 v[26:29], v[190:193], v[150:153], v[26:29]
	v_mfma_f32_16x16x32_bf16 v[22:25], v[182:185], v[158:161], v[22:25]
	v_mfma_f32_16x16x32_bf16 v[18:21], v[190:193], v[158:161], v[18:21]
	v_mfma_f32_16x16x32_bf16 v[14:17], v[182:185], v[166:169], v[14:17]
	v_mfma_f32_16x16x32_bf16 v[10:13], v[190:193], v[166:169], v[10:13]
	v_mfma_f32_16x16x32_bf16 v[6:9], v[182:185], v[174:177], v[6:9]
	v_mfma_f32_16x16x32_bf16 v[2:5], v[190:193], v[174:177], v[2:5]
	s_mov_b32 m0, s76
	v_lshl_add_u64 v[218:219], v[224:225], 0, s[54:55]
	s_barrier
	ds_read_b128 v[146:149], v240 offset:49152
	ds_read_b128 v[150:153], v240 offset:50176
	ds_read_b128 v[154:157], v240 offset:51200
	ds_read_b128 v[158:161], v240 offset:52224
	ds_read_b128 v[162:165], v240 offset:53248
	ds_read_b128 v[166:169], v240 offset:54272
	ds_read_b128 v[170:173], v240 offset:55296
	ds_read_b128 v[174:177], v240 offset:56320
	global_load_lds_dwordx4 v[218:219], off
	v_lshl_add_u64 v[218:219], v[230:231], 0, s[54:55]
	s_mov_b32 m0, s77
	s_nop 0
	global_load_lds_dwordx4 v[218:219], off
	s_waitcnt vmcnt(10)
	s_barrier
	s_waitcnt lgkmcnt(0)
	v_mfma_f32_16x16x32_bf16 v[66:69], v[130:133], v[146:149], v[66:69]
	v_mfma_f32_16x16x32_bf16 v[70:73], v[138:141], v[146:149], v[70:73]
	v_mfma_f32_16x16x32_bf16 v[74:77], v[130:133], v[154:157], v[74:77]
	v_mfma_f32_16x16x32_bf16 v[78:81], v[138:141], v[154:157], v[78:81]
	v_mfma_f32_16x16x32_bf16 v[82:85], v[130:133], v[162:165], v[82:85]
	v_mfma_f32_16x16x32_bf16 v[86:89], v[138:141], v[162:165], v[86:89]
	v_mfma_f32_16x16x32_bf16 v[90:93], v[130:133], v[170:173], v[90:93]
	v_mfma_f32_16x16x32_bf16 v[94:97], v[138:141], v[170:173], v[94:97]
	v_mfma_f32_16x16x32_bf16 v[66:69], v[134:137], v[150:153], v[66:69]
	v_mfma_f32_16x16x32_bf16 v[70:73], v[142:145], v[150:153], v[70:73]
	v_mfma_f32_16x16x32_bf16 v[74:77], v[134:137], v[158:161], v[74:77]
	v_mfma_f32_16x16x32_bf16 v[78:81], v[142:145], v[158:161], v[78:81]
	v_mfma_f32_16x16x32_bf16 v[82:85], v[134:137], v[166:169], v[82:85]
	v_mfma_f32_16x16x32_bf16 v[86:89], v[142:145], v[166:169], v[86:89]
	v_mfma_f32_16x16x32_bf16 v[90:93], v[134:137], v[174:177], v[90:93]
	v_mfma_f32_16x16x32_bf16 v[94:97], v[142:145], v[174:177], v[94:97]
	s_barrier
	s_add_u32 s0, s28, 0x20080
	s_addc_u32 s1, s29, 0
	s_add_i32 s28, s30, s66
	v_lshl_add_u64 v[130:131], s[0:1], 0, v[202:203]
	s_mov_b32 m0, s28
	s_nop 0
	global_load_lds_dwordx4 v[130:131], off
	v_lshl_add_u64 v[130:131], s[0:1], 0, v[198:199]
	s_add_i32 m0, s28, 0x2000
	s_nop 0
	global_load_lds_dwordx4 v[130:131], off
	v_add_u32_e32 v142, 0x10000, v237
	ds_read_b128 v[130:133], v142
	ds_read_b128 v[134:137], v142 offset:1024
	ds_read_b128 v[138:141], v142 offset:2048
	ds_read_b128 v[142:145], v142 offset:3072
	s_waitcnt vmcnt(6)
	s_barrier
	v_mfma_f32_16x16x32_bf16 v[98:101], v[178:181], v[146:149], v[98:101]
	v_mfma_f32_16x16x32_bf16 v[102:105], v[186:189], v[146:149], v[102:105]
	v_mfma_f32_16x16x32_bf16 v[106:109], v[178:181], v[154:157], v[106:109]
	v_mfma_f32_16x16x32_bf16 v[110:113], v[186:189], v[154:157], v[110:113]
	v_mfma_f32_16x16x32_bf16 v[114:117], v[178:181], v[162:165], v[114:117]
	v_mfma_f32_16x16x32_bf16 v[118:121], v[186:189], v[162:165], v[118:121]
	v_mfma_f32_16x16x32_bf16 v[122:125], v[178:181], v[170:173], v[122:125]
	v_mfma_f32_16x16x32_bf16 v[126:129], v[186:189], v[170:173], v[126:129]
	v_mfma_f32_16x16x32_bf16 v[98:101], v[182:185], v[150:153], v[98:101]
	v_mfma_f32_16x16x32_bf16 v[102:105], v[190:193], v[150:153], v[102:105]
	v_mfma_f32_16x16x32_bf16 v[106:109], v[182:185], v[158:161], v[106:109]
	v_mfma_f32_16x16x32_bf16 v[110:113], v[190:193], v[158:161], v[110:113]
	v_mfma_f32_16x16x32_bf16 v[114:117], v[182:185], v[166:169], v[114:117]
	v_mfma_f32_16x16x32_bf16 v[118:121], v[190:193], v[166:169], v[118:121]
	v_mfma_f32_16x16x32_bf16 v[122:125], v[182:185], v[174:177], v[122:125]
	v_mfma_f32_16x16x32_bf16 v[126:129], v[190:193], v[174:177], v[126:129]
	s_add_i32 s86, s86, 2
	s_add_u32 s6, s6, 0x100
	s_addc_u32 s7, s7, 0
	s_add_u32 s21, s21, 0x100
	s_addc_u32 s82, s82, 0
	s_cmp_gt_u32 s86, 5
	s_barrier
	s_cbranch_scc0 .LBB0_1332
	s_waitcnt lgkmcnt(0)
	s_cmp_lg_u32 s27, 0
	s_cselect_b64 s[6:7], -1, 0
	s_cmp_eq_u32 s27, 0
	v_lshl_add_u32 v218, s26, 8, v1
	s_cselect_b32 s0, 0, 0x10000
	s_add_u32 s26, s74, s0
	v_ashrrev_i32_e32 v130, 5, v218
	s_addc_u32 s27, s75, 0
	v_and_b32_e32 v136, -8, v130
	s_lshl_b32 s0, s79, 1
	v_add_u32_e32 v130, s0, v136
	v_ashrrev_i32_e32 v131, 31, v130
	v_lshlrev_b64 v[130:131], 17, v[130:131]
	v_lshl_add_u64 v[132:133], v[206:207], 1, s[26:27]
	v_lshl_add_u64 v[134:135], v[132:133], 0, v[130:131]
	s_or_b32 s1, s0, 1
	global_load_dwordx4 v[186:189], v[134:135], off
	v_add_u32_e32 v134, s1, v136
	v_ashrrev_i32_e32 v135, 31, v134
	v_lshlrev_b64 v[134:135], 17, v[134:135]
	v_lshl_add_u64 v[132:133], v[132:133], 0, v[134:135]
	global_load_dwordx4 v[178:181], v[132:133], off
	v_lshl_add_u64 v[132:133], v[208:209], 1, s[26:27]
	v_lshl_add_u64 v[136:137], v[132:133], 0, v[130:131]
	global_load_dwordx4 v[174:177], v[136:137], off
	v_lshl_add_u64 v[132:133], v[132:133], 0, v[134:135]
	global_load_dwordx4 v[170:173], v[132:133], off
	v_lshl_add_u64 v[132:133], v[210:211], 1, s[26:27]
	v_lshl_add_u64 v[136:137], v[132:133], 0, v[130:131]
	v_lshl_add_u64 v[132:133], v[132:133], 0, v[134:135]
	global_load_dwordx4 v[162:165], v[136:137], off
	global_load_dwordx4 v[150:153], v[132:133], off
	v_lshl_add_u64 v[132:133], v[212:213], 1, s[26:27]
	v_lshl_add_u64 v[130:131], v[132:133], 0, v[130:131]
	global_load_dwordx4 v[142:145], v[130:131], off
	v_lshl_add_u64 v[130:131], v[132:133], 0, v[134:135]
	v_add_u32_e32 v220, 0x80, v218
	global_load_dwordx4 v[134:137], v[130:131], off
	v_ashrrev_i32_e32 v130, 5, v220
	v_and_b32_e32 v146, -8, v130
	v_add_u32_e32 v130, s0, v146
	v_ashrrev_i32_e32 v131, 31, v130
	v_lshlrev_b64 v[182:183], 17, v[130:131]
	v_lshlrev_b32_e32 v130, 7, v220
	s_movk_i32 s0, 0x4000
	v_and_or_b32 v130, v130, s0, v238
	v_lshlrev_b32_e32 v194, 1, v130
	v_lshl_add_u64 v[130:131], s[26:27], 0, v[194:195]
	v_lshl_add_u64 v[132:133], v[130:131], 0, v[182:183]
	global_load_dwordx4 v[138:141], v[132:133], off
	v_add_u32_e32 v132, s1, v146
	v_ashrrev_i32_e32 v133, 31, v132
	v_lshlrev_b64 v[190:191], 17, v[132:133]
	v_lshl_add_u64 v[130:131], v[130:131], 0, v[190:191]
	global_load_dwordx4 v[130:133], v[130:131], off
	v_or_b32_e32 v146, 0x2000, v194
	v_mov_b32_e32 v147, v195
	v_lshl_add_u64 v[146:147], s[26:27], 0, v[146:147]
	v_lshl_add_u64 v[148:149], v[146:147], 0, v[182:183]
	global_load_dwordx4 v[166:169], v[148:149], off
	v_lshl_add_u64 v[146:147], v[146:147], 0, v[190:191]
	global_load_dwordx4 v[154:157], v[146:147], off
	v_or_b32_e32 v146, 0x4000, v194
	v_mov_b32_e32 v147, v195
	v_lshl_add_u64 v[146:147], s[26:27], 0, v[146:147]
	v_lshl_add_u64 v[148:149], v[146:147], 0, v[182:183]
	global_load_dwordx4 v[158:161], v[148:149], off
	v_or_b32_e32 v194, 0x6000, v194
	v_lshl_add_u64 v[192:193], s[26:27], 0, v[194:195]
	v_lshl_add_u64 v[146:147], v[146:147], 0, v[190:191]
	v_lshl_add_u64 v[190:191], v[192:193], 0, v[190:191]
	v_lshl_add_u64 v[182:183], v[192:193], 0, v[182:183]
	global_load_dwordx4 v[190:193], v[190:191], off
	s_and_b64 vcc, exec, s[6:7]
	global_load_dwordx4 v[146:149], v[146:147], off
	s_waitcnt vmcnt(0)
	v_lshlrev_b32_e32 v224, 16, v186
	global_load_dwordx4 v[182:185], v[182:183], off
	v_and_b32_e32 v225, 0xffff0000, v186
	v_lshlrev_b32_e32 v186, 16, v187
	v_and_b32_e32 v187, 0xffff0000, v187
	v_pk_mul_f32 v[64:65], v[64:65], v[186:187]
	v_lshlrev_b32_e32 v186, 16, v188
	v_and_b32_e32 v187, 0xffff0000, v188
	v_pk_mul_f32 v[58:59], v[58:59], v[186:187]
	v_lshlrev_b32_e32 v186, 16, v189
	v_and_b32_e32 v187, 0xffff0000, v189
	v_pk_mul_f32 v[60:61], v[60:61], v[186:187]
	v_lshlrev_b32_e32 v186, 16, v178
	v_and_b32_e32 v187, 0xffff0000, v178
	v_lshlrev_b32_e32 v178, 16, v179
	v_and_b32_e32 v179, 0xffff0000, v179
	v_pk_mul_f32 v[32:33], v[32:33], v[178:179]
	v_lshlrev_b32_e32 v178, 16, v180
	v_and_b32_e32 v179, 0xffff0000, v180
	v_pk_mul_f32 v[26:27], v[26:27], v[178:179]
	v_lshlrev_b32_e32 v178, 16, v181
	v_and_b32_e32 v179, 0xffff0000, v181
	v_pk_mul_f32 v[28:29], v[28:29], v[178:179]
	v_lshlrev_b32_e32 v178, 16, v174
	v_and_b32_e32 v179, 0xffff0000, v174
	v_lshlrev_b32_e32 v174, 16, v175
	v_and_b32_e32 v175, 0xffff0000, v175
	v_pk_mul_f32 v[56:57], v[56:57], v[174:175]
	v_lshlrev_b32_e32 v174, 16, v176
	v_and_b32_e32 v175, 0xffff0000, v176
	v_pk_mul_f32 v[50:51], v[50:51], v[174:175]
	v_lshlrev_b32_e32 v174, 16, v177
	v_and_b32_e32 v175, 0xffff0000, v177
	v_pk_mul_f32 v[52:53], v[52:53], v[174:175]
	v_lshlrev_b32_e32 v174, 16, v170
	v_and_b32_e32 v175, 0xffff0000, v170
	v_lshlrev_b32_e32 v170, 16, v171
	v_and_b32_e32 v171, 0xffff0000, v171
	v_pk_mul_f32 v[24:25], v[24:25], v[170:171]
	v_lshlrev_b32_e32 v170, 16, v172
	v_and_b32_e32 v171, 0xffff0000, v172
	v_pk_mul_f32 v[18:19], v[18:19], v[170:171]
	v_lshlrev_b32_e32 v170, 16, v173
	v_and_b32_e32 v171, 0xffff0000, v173
	v_pk_mul_f32 v[20:21], v[20:21], v[170:171]
	v_lshlrev_b32_e32 v170, 16, v162
	v_and_b32_e32 v171, 0xffff0000, v162
	v_lshlrev_b32_e32 v162, 16, v163
	v_and_b32_e32 v163, 0xffff0000, v163
	v_pk_mul_f32 v[48:49], v[48:49], v[162:163]
	v_lshlrev_b32_e32 v162, 16, v164
	v_and_b32_e32 v163, 0xffff0000, v164
	v_pk_mul_f32 v[42:43], v[42:43], v[162:163]
	v_lshlrev_b32_e32 v162, 16, v165
	v_and_b32_e32 v163, 0xffff0000, v165
	v_pk_mul_f32 v[44:45], v[44:45], v[162:163]
	v_lshlrev_b32_e32 v162, 16, v150
	v_and_b32_e32 v163, 0xffff0000, v150
	v_lshlrev_b32_e32 v150, 16, v151
	v_and_b32_e32 v151, 0xffff0000, v151
	v_pk_mul_f32 v[16:17], v[16:17], v[150:151]
	v_lshlrev_b32_e32 v150, 16, v152
	v_and_b32_e32 v151, 0xffff0000, v152
	v_pk_mul_f32 v[10:11], v[10:11], v[150:151]
	v_lshlrev_b32_e32 v150, 16, v153
	v_and_b32_e32 v151, 0xffff0000, v153
	v_pk_mul_f32 v[12:13], v[12:13], v[150:151]
	v_lshlrev_b32_e32 v150, 16, v142
	v_and_b32_e32 v151, 0xffff0000, v142
	v_lshlrev_b32_e32 v142, 16, v143
	v_and_b32_e32 v143, 0xffff0000, v143
	v_pk_mul_f32 v[40:41], v[40:41], v[142:143]
	v_lshlrev_b32_e32 v142, 16, v144
	v_and_b32_e32 v143, 0xffff0000, v144
	v_pk_mul_f32 v[34:35], v[34:35], v[142:143]
	v_lshlrev_b32_e32 v142, 16, v145
	v_and_b32_e32 v143, 0xffff0000, v145
	v_pk_mul_f32 v[36:37], v[36:37], v[142:143]
	v_lshlrev_b32_e32 v142, 16, v134
	v_and_b32_e32 v143, 0xffff0000, v134
	v_lshlrev_b32_e32 v134, 16, v135
	v_and_b32_e32 v135, 0xffff0000, v135
	v_pk_mul_f32 v[8:9], v[8:9], v[134:135]
	v_lshlrev_b32_e32 v134, 16, v136
	v_and_b32_e32 v135, 0xffff0000, v136
	v_pk_mul_f32 v[2:3], v[2:3], v[134:135]
	v_lshlrev_b32_e32 v134, 16, v137
	v_and_b32_e32 v135, 0xffff0000, v137
	v_pk_mul_f32 v[4:5], v[4:5], v[134:135]
	v_lshlrev_b32_e32 v134, 16, v138
	v_and_b32_e32 v135, 0xffff0000, v138
	v_pk_mul_f32 v[66:67], v[66:67], v[134:135]
	v_lshlrev_b32_e32 v134, 16, v139
	v_and_b32_e32 v135, 0xffff0000, v139
	v_pk_mul_f32 v[68:69], v[68:69], v[134:135]
	v_lshlrev_b32_e32 v134, 16, v140
	v_and_b32_e32 v135, 0xffff0000, v140
	v_pk_mul_f32 v[70:71], v[70:71], v[134:135]
	v_lshlrev_b32_e32 v134, 16, v141
	v_and_b32_e32 v135, 0xffff0000, v141
	v_pk_mul_f32 v[72:73], v[72:73], v[134:135]
	v_lshlrev_b32_e32 v134, 16, v130
	v_and_b32_e32 v135, 0xffff0000, v130
	v_lshlrev_b32_e32 v130, 16, v131
	v_and_b32_e32 v131, 0xffff0000, v131
	v_pk_mul_f32 v[100:101], v[100:101], v[130:131]
	v_lshlrev_b32_e32 v130, 16, v132
	v_and_b32_e32 v131, 0xffff0000, v132
	v_pk_mul_f32 v[102:103], v[102:103], v[130:131]
	v_lshlrev_b32_e32 v130, 16, v133
	v_and_b32_e32 v131, 0xffff0000, v133
	v_pk_mul_f32 v[104:105], v[104:105], v[130:131]
	v_lshlrev_b32_e32 v130, 16, v166
	v_and_b32_e32 v131, 0xffff0000, v166
	v_pk_mul_f32 v[74:75], v[74:75], v[130:131]
	v_lshlrev_b32_e32 v130, 16, v167
	v_and_b32_e32 v131, 0xffff0000, v167
	v_pk_mul_f32 v[76:77], v[76:77], v[130:131]
	v_lshlrev_b32_e32 v130, 16, v168
	v_and_b32_e32 v131, 0xffff0000, v168
	v_pk_mul_f32 v[78:79], v[78:79], v[130:131]
	v_lshlrev_b32_e32 v130, 16, v169
	v_and_b32_e32 v131, 0xffff0000, v169
	v_pk_mul_f32 v[80:81], v[80:81], v[130:131]
	v_lshlrev_b32_e32 v130, 16, v154
	v_and_b32_e32 v131, 0xffff0000, v154
	v_pk_mul_f32 v[106:107], v[106:107], v[130:131]
	v_lshlrev_b32_e32 v130, 16, v155
	v_and_b32_e32 v131, 0xffff0000, v155
	v_pk_mul_f32 v[108:109], v[108:109], v[130:131]
	v_lshlrev_b32_e32 v130, 16, v156
	v_and_b32_e32 v131, 0xffff0000, v156
	v_pk_mul_f32 v[110:111], v[110:111], v[130:131]
	v_lshlrev_b32_e32 v130, 16, v157
	v_and_b32_e32 v131, 0xffff0000, v157
	v_pk_mul_f32 v[112:113], v[112:113], v[130:131]
	v_lshlrev_b32_e32 v130, 16, v158
	v_and_b32_e32 v131, 0xffff0000, v158
	v_pk_mul_f32 v[82:83], v[82:83], v[130:131]
	v_lshlrev_b32_e32 v130, 16, v159
	v_and_b32_e32 v131, 0xffff0000, v159
	v_pk_mul_f32 v[84:85], v[84:85], v[130:131]
	v_lshlrev_b32_e32 v130, 16, v160
	v_and_b32_e32 v131, 0xffff0000, v160
	v_pk_mul_f32 v[86:87], v[86:87], v[130:131]
	v_lshlrev_b32_e32 v130, 16, v161
	v_and_b32_e32 v131, 0xffff0000, v161
	v_pk_mul_f32 v[88:89], v[88:89], v[130:131]
	v_lshlrev_b32_e32 v130, 16, v146
	v_and_b32_e32 v131, 0xffff0000, v146
	v_pk_mul_f32 v[114:115], v[114:115], v[130:131]
	v_lshlrev_b32_e32 v130, 16, v147
	v_and_b32_e32 v131, 0xffff0000, v147
	v_pk_mul_f32 v[116:117], v[116:117], v[130:131]
	v_lshlrev_b32_e32 v130, 16, v148
	v_and_b32_e32 v131, 0xffff0000, v148
	v_pk_mul_f32 v[118:119], v[118:119], v[130:131]
	v_lshlrev_b32_e32 v130, 16, v149
	v_and_b32_e32 v131, 0xffff0000, v149
	v_pk_mul_f32 v[120:121], v[120:121], v[130:131]
	s_waitcnt vmcnt(0)
	v_lshlrev_b32_e32 v130, 16, v182
	v_and_b32_e32 v131, 0xffff0000, v182
	v_pk_mul_f32 v[90:91], v[90:91], v[130:131]
	v_lshlrev_b32_e32 v130, 16, v183
	v_and_b32_e32 v131, 0xffff0000, v183
	v_pk_mul_f32 v[92:93], v[92:93], v[130:131]
	v_lshlrev_b32_e32 v130, 16, v184
	v_and_b32_e32 v131, 0xffff0000, v184
	v_pk_mul_f32 v[94:95], v[94:95], v[130:131]
	v_lshlrev_b32_e32 v130, 16, v185
	v_and_b32_e32 v131, 0xffff0000, v185
	v_pk_mul_f32 v[96:97], v[96:97], v[130:131]
	v_lshlrev_b32_e32 v130, 16, v190
	v_and_b32_e32 v131, 0xffff0000, v190
	v_pk_mul_f32 v[122:123], v[122:123], v[130:131]
	v_lshlrev_b32_e32 v130, 16, v191
	v_and_b32_e32 v131, 0xffff0000, v191
	v_pk_mul_f32 v[124:125], v[124:125], v[130:131]
	v_lshlrev_b32_e32 v130, 16, v192
	v_and_b32_e32 v131, 0xffff0000, v192
	v_pk_mul_f32 v[126:127], v[126:127], v[130:131]
	v_lshlrev_b32_e32 v130, 16, v193
	v_and_b32_e32 v131, 0xffff0000, v193
	v_pk_mul_f32 v[62:63], v[62:63], v[224:225]
	v_pk_mul_f32 v[30:31], v[30:31], v[186:187]
	v_pk_mul_f32 v[54:55], v[54:55], v[178:179]
	v_pk_mul_f32 v[22:23], v[22:23], v[174:175]
	v_pk_mul_f32 v[46:47], v[46:47], v[170:171]
	v_pk_mul_f32 v[14:15], v[14:15], v[162:163]
	v_pk_mul_f32 v[38:39], v[38:39], v[150:151]
	v_pk_mul_f32 v[6:7], v[6:7], v[142:143]
	v_pk_mul_f32 v[98:99], v[98:99], v[134:135]
	v_pk_mul_f32 v[128:129], v[128:129], v[130:131]
	s_cbranch_vccz .LBB0_1335
	v_lshl_or_b32 v134, s79, 8, v239
	v_ashrrev_i32_e32 v219, 31, v218
	v_lshlrev_b64 v[130:131], 11, v[218:219]
	v_ashrrev_i32_e32 v135, 31, v134
	v_lshl_add_u64 v[136:137], s[8:9], 0, v[130:131]
	v_lshlrev_b64 v[134:135], 1, v[134:135]
	v_cvt_pk_bf16_f32 v130, v62, v63
	v_cvt_pk_bf16_f32 v131, v64, v65
	v_cvt_pk_bf16_f32 v132, v58, v59
	v_cvt_pk_bf16_f32 v133, v60, v61
	v_lshl_add_u64 v[136:137], v[136:137], 0, v[134:135]
	global_store_dwordx4 v[136:137], v[130:133], off
	v_ashrrev_i32_e32 v221, 31, v220
	s_mov_b64 s[0:1], 0x48000
	v_cvt_pk_bf16_f32 v130, v30, v31
	v_cvt_pk_bf16_f32 v131, v32, v33
	v_cvt_pk_bf16_f32 v132, v26, v27
	v_cvt_pk_bf16_f32 v133, v28, v29
	global_store_dwordx4 v[136:137], v[130:133], off offset:256
	s_nop 1
	v_or_b32_e32 v130, 16, v218
	v_ashrrev_i32_e32 v131, 31, v130
	v_lshlrev_b64 v[130:131], 11, v[130:131]
	v_lshl_add_u64 v[138:139], s[8:9], 0, v[130:131]
	v_cvt_pk_bf16_f32 v130, v54, v55
	v_cvt_pk_bf16_f32 v131, v56, v57
	v_cvt_pk_bf16_f32 v132, v50, v51
	v_cvt_pk_bf16_f32 v133, v52, v53
	v_lshl_add_u64 v[138:139], v[138:139], 0, v[134:135]
	global_store_dwordx4 v[138:139], v[130:133], off
	s_nop 1
	v_cvt_pk_bf16_f32 v130, v22, v23
	v_cvt_pk_bf16_f32 v131, v24, v25
	v_cvt_pk_bf16_f32 v132, v18, v19
	v_cvt_pk_bf16_f32 v133, v20, v21
	global_store_dwordx4 v[138:139], v[130:133], off offset:256
	s_nop 1
	v_or_b32_e32 v130, 32, v218
	v_ashrrev_i32_e32 v131, 31, v130
	v_lshlrev_b64 v[130:131], 11, v[130:131]
	v_lshl_add_u64 v[138:139], s[8:9], 0, v[130:131]
	v_cvt_pk_bf16_f32 v130, v46, v47
	v_cvt_pk_bf16_f32 v131, v48, v49
	v_cvt_pk_bf16_f32 v132, v42, v43
	v_cvt_pk_bf16_f32 v133, v44, v45
	v_lshl_add_u64 v[138:139], v[138:139], 0, v[134:135]
	global_store_dwordx4 v[138:139], v[130:133], off
	s_nop 1
	v_cvt_pk_bf16_f32 v130, v14, v15
	v_cvt_pk_bf16_f32 v131, v16, v17
	v_cvt_pk_bf16_f32 v132, v10, v11
	v_cvt_pk_bf16_f32 v133, v12, v13
	global_store_dwordx4 v[138:139], v[130:133], off offset:256
	s_nop 1
	v_or_b32_e32 v130, 48, v218
	v_ashrrev_i32_e32 v131, 31, v130
	v_lshlrev_b64 v[130:131], 11, v[130:131]
	v_lshl_add_u64 v[138:139], s[8:9], 0, v[130:131]
	v_cvt_pk_bf16_f32 v130, v38, v39
	v_cvt_pk_bf16_f32 v131, v40, v41
	v_cvt_pk_bf16_f32 v132, v34, v35
	v_cvt_pk_bf16_f32 v133, v36, v37
	v_lshl_add_u64 v[138:139], v[138:139], 0, v[134:135]
	global_store_dwordx4 v[138:139], v[130:133], off
	s_nop 1
	v_cvt_pk_bf16_f32 v130, v6, v7
	v_cvt_pk_bf16_f32 v131, v8, v9
	v_cvt_pk_bf16_f32 v132, v2, v3
	v_cvt_pk_bf16_f32 v133, v4, v5
	global_store_dwordx4 v[138:139], v[130:133], off offset:256
	s_nop 1
	v_lshlrev_b64 v[130:131], 11, v[220:221]
	v_lshl_add_u64 v[138:139], s[8:9], 0, v[130:131]
	v_cvt_pk_bf16_f32 v130, v66, v67
	v_cvt_pk_bf16_f32 v131, v68, v69
	v_cvt_pk_bf16_f32 v132, v70, v71
	v_cvt_pk_bf16_f32 v133, v72, v73
	v_lshl_add_u64 v[134:135], v[138:139], 0, v[134:135]
	global_store_dwordx4 v[134:135], v[130:133], off
	s_nop 1
	v_cvt_pk_bf16_f32 v130, v98, v99
	v_cvt_pk_bf16_f32 v131, v100, v101
	v_cvt_pk_bf16_f32 v132, v102, v103
	v_cvt_pk_bf16_f32 v133, v104, v105
	global_store_dwordx4 v[134:135], v[130:133], off offset:256
	v_lshl_add_u64 v[134:135], v[136:137], 0, s[0:1]
	s_mov_b32 s0, 0x48000
	v_add_co_u32_e32 v138, vcc, s0, v136
	v_cvt_pk_bf16_f32 v130, v74, v75
	v_cvt_pk_bf16_f32 v131, v76, v77
	v_cvt_pk_bf16_f32 v132, v78, v79
	v_cvt_pk_bf16_f32 v133, v80, v81
	v_addc_co_u32_e32 v139, vcc, 0, v137, vcc
	global_store_dwordx4 v[138:139], v[130:133], off
	s_mov_b64 s[0:1], 0x50000
	s_nop 0
	v_cvt_pk_bf16_f32 v130, v106, v107
	v_cvt_pk_bf16_f32 v131, v108, v109
	v_cvt_pk_bf16_f32 v132, v110, v111
	v_cvt_pk_bf16_f32 v133, v112, v113
	global_store_dwordx4 v[134:135], v[130:133], off offset:256
	v_lshl_add_u64 v[134:135], v[136:137], 0, s[0:1]
	s_mov_b32 s0, 0x50000
	v_add_co_u32_e32 v138, vcc, s0, v136
	v_cvt_pk_bf16_f32 v130, v82, v83
	v_cvt_pk_bf16_f32 v131, v84, v85
	v_cvt_pk_bf16_f32 v132, v86, v87
	v_cvt_pk_bf16_f32 v133, v88, v89
	v_addc_co_u32_e32 v139, vcc, 0, v137, vcc
	global_store_dwordx4 v[138:139], v[130:133], off
	s_mov_b64 s[0:1], 0x58000
	s_nop 0
	v_cvt_pk_bf16_f32 v130, v114, v115
	v_cvt_pk_bf16_f32 v131, v116, v117
	v_cvt_pk_bf16_f32 v132, v118, v119
	v_cvt_pk_bf16_f32 v133, v120, v121
	global_store_dwordx4 v[134:135], v[130:133], off offset:256
	v_lshl_add_u64 v[134:135], v[136:137], 0, s[0:1]
	s_mov_b32 s0, 0x58000
	v_add_co_u32_e32 v136, vcc, s0, v136
	v_cvt_pk_bf16_f32 v130, v90, v91
	v_cvt_pk_bf16_f32 v131, v92, v93
	v_cvt_pk_bf16_f32 v132, v94, v95
	v_cvt_pk_bf16_f32 v133, v96, v97
	v_addc_co_u32_e32 v137, vcc, 0, v137, vcc
	global_store_dwordx4 v[136:137], v[130:133], off
	s_nop 1
	v_cvt_pk_bf16_f32 v130, v122, v123
	v_cvt_pk_bf16_f32 v131, v124, v125
	v_cvt_pk_bf16_f32 v132, v126, v127
	v_cvt_pk_bf16_f32 v133, v128, v129
	global_store_dwordx4 v[134:135], v[130:133], off offset:256

.LBB0_1765:
	s_add_u32 s0, s24, 0xfffc0080
	s_addc_u32 s1, s25, -1
	s_add_i32 s33, 0, 0x10000
	s_cmp_eq_u32 s82, 12
	s_cselect_b32 s29, s19, s1
	s_cselect_b32 s28, s76, s0
	s_cselect_b32 s27, s15, s79
	s_cselect_b32 s26, s77, s78
	v_lshl_add_u64 v[192:193], s[24:25], 0, v[136:137]
	s_add_i32 m0, s13, 0xc000
	ds_read_b128 v[160:163], v143
	ds_read_b128 v[164:167], v143 offset:1024
	ds_read_b128 v[168:171], v143 offset:2048
	ds_read_b128 v[172:175], v143 offset:3072
	ds_read_b128 v[176:179], v143 offset:4096
	ds_read_b128 v[180:183], v143 offset:5120
	ds_read_b128 v[184:187], v143 offset:6144
	ds_read_b128 v[188:191], v143 offset:7168
	global_load_lds_dwordx4 v[192:193], off
	v_lshl_add_u64 v[192:193], s[24:25], 0, v[138:139]
	s_add_i32 m0, s13, 0xe000
	s_nop 0
	global_load_lds_dwordx4 v[192:193], off
	s_waitcnt lgkmcnt(8)
	s_barrier
	s_waitcnt lgkmcnt(0)
	v_mfma_f32_16x16x32_bf16 v[126:129], v[144:147], v[160:163], v[126:129]
	v_mfma_f32_16x16x32_bf16 v[122:125], v[152:155], v[160:163], v[122:125]
	v_mfma_f32_16x16x32_bf16 v[118:121], v[144:147], v[168:171], v[118:121]
	v_mfma_f32_16x16x32_bf16 v[114:117], v[152:155], v[168:171], v[114:117]
	v_mfma_f32_16x16x32_bf16 v[102:105], v[144:147], v[176:179], v[102:105]
	v_mfma_f32_16x16x32_bf16 v[98:101], v[152:155], v[176:179], v[98:101]
	v_mfma_f32_16x16x32_bf16 v[86:89], v[144:147], v[184:187], v[86:89]
	v_mfma_f32_16x16x32_bf16 v[82:85], v[152:155], v[184:187], v[82:85]
	v_mfma_f32_16x16x32_bf16 v[126:129], v[148:151], v[164:167], v[126:129]
	v_mfma_f32_16x16x32_bf16 v[122:125], v[156:159], v[164:167], v[122:125]
	v_mfma_f32_16x16x32_bf16 v[118:121], v[148:151], v[172:175], v[118:121]
	v_mfma_f32_16x16x32_bf16 v[114:117], v[156:159], v[172:175], v[114:117]
	v_mfma_f32_16x16x32_bf16 v[102:105], v[148:151], v[180:183], v[102:105]
	v_mfma_f32_16x16x32_bf16 v[98:101], v[156:159], v[180:183], v[98:101]
	v_mfma_f32_16x16x32_bf16 v[86:89], v[148:151], v[188:191], v[86:89]
	v_mfma_f32_16x16x32_bf16 v[82:85], v[156:159], v[188:191], v[82:85]
	s_barrier
	s_add_i32 s36, 0, 0x14000
	v_add_u32_e32 v192, s36, v141
	s_add_i32 s0, s33, s64
	ds_read_b128 v[198:201], v192
	ds_read_b128 v[202:205], v192 offset:1024
	ds_read_b128 v[206:209], v192 offset:2048
	ds_read_b128 v[210:213], v192 offset:3072
	v_lshl_add_u64 v[192:193], s[26:27], 0, v[194:195]
	s_mov_b32 m0, s0
	v_lshl_add_u64 v[214:215], s[26:27], 0, v[130:131]
	global_load_lds_dwordx4 v[192:193], off
	s_add_i32 m0, s0, 0x2000
	s_nop 0
	global_load_lds_dwordx4 v[214:215], off
	s_barrier
	s_waitcnt lgkmcnt(0)
	v_mfma_f32_16x16x32_bf16 v[110:113], v[198:201], v[160:163], v[110:113]
	v_mfma_f32_16x16x32_bf16 v[106:109], v[206:209], v[160:163], v[106:109]
	v_mfma_f32_16x16x32_bf16 v[94:97], v[198:201], v[168:171], v[94:97]
	v_mfma_f32_16x16x32_bf16 v[90:93], v[206:209], v[168:171], v[90:93]
	v_mfma_f32_16x16x32_bf16 v[78:81], v[198:201], v[176:179], v[78:81]
	v_mfma_f32_16x16x32_bf16 v[74:77], v[206:209], v[176:179], v[74:77]
	v_mfma_f32_16x16x32_bf16 v[70:73], v[198:201], v[184:187], v[70:73]
	v_mfma_f32_16x16x32_bf16 v[66:69], v[206:209], v[184:187], v[66:69]
	v_mfma_f32_16x16x32_bf16 v[110:113], v[202:205], v[164:167], v[110:113]
	v_mfma_f32_16x16x32_bf16 v[106:109], v[210:213], v[164:167], v[106:109]
	v_mfma_f32_16x16x32_bf16 v[94:97], v[202:205], v[172:175], v[94:97]
	v_mfma_f32_16x16x32_bf16 v[90:93], v[210:213], v[172:175], v[90:93]
	v_mfma_f32_16x16x32_bf16 v[78:81], v[202:205], v[180:183], v[78:81]
	v_mfma_f32_16x16x32_bf16 v[74:77], v[210:213], v[180:183], v[74:77]
	v_mfma_f32_16x16x32_bf16 v[70:73], v[202:205], v[188:191], v[70:73]
	v_mfma_f32_16x16x32_bf16 v[66:69], v[210:213], v[188:191], v[66:69]
	s_mov_b32 m0, s13
	v_lshl_add_u64 v[216:217], s[28:29], 0, v[134:135]
	s_barrier
	ds_read_b128 v[160:163], v143 offset:16384
	ds_read_b128 v[164:167], v143 offset:17408
	ds_read_b128 v[168:171], v143 offset:18432
	ds_read_b128 v[172:175], v143 offset:19456
	ds_read_b128 v[176:179], v143 offset:20480
	ds_read_b128 v[180:183], v143 offset:21504
	ds_read_b128 v[184:187], v143 offset:22528
	ds_read_b128 v[188:191], v143 offset:23552
	global_load_lds_dwordx4 v[216:217], off
	v_lshl_add_u64 v[218:219], s[28:29], 0, v[132:133]
	s_mov_b32 m0, s68
	s_nop 0
	global_load_lds_dwordx4 v[218:219], off
	s_waitcnt vmcnt(10)
	s_barrier
	s_waitcnt lgkmcnt(0)
	v_mfma_f32_16x16x32_bf16 v[62:65], v[144:147], v[160:163], v[62:65]
	v_mfma_f32_16x16x32_bf16 v[58:61], v[152:155], v[160:163], v[58:61]
	v_mfma_f32_16x16x32_bf16 v[54:57], v[144:147], v[168:171], v[54:57]
	v_mfma_f32_16x16x32_bf16 v[50:53], v[152:155], v[168:171], v[50:53]
	v_mfma_f32_16x16x32_bf16 v[38:41], v[144:147], v[176:179], v[38:41]
	v_mfma_f32_16x16x32_bf16 v[34:37], v[152:155], v[176:179], v[34:37]
	v_mfma_f32_16x16x32_bf16 v[22:25], v[144:147], v[184:187], v[22:25]
	v_mfma_f32_16x16x32_bf16 v[18:21], v[152:155], v[184:187], v[18:21]
	v_mfma_f32_16x16x32_bf16 v[62:65], v[148:151], v[164:167], v[62:65]
	v_mfma_f32_16x16x32_bf16 v[58:61], v[156:159], v[164:167], v[58:61]
	v_mfma_f32_16x16x32_bf16 v[54:57], v[148:151], v[172:175], v[54:57]
	v_mfma_f32_16x16x32_bf16 v[50:53], v[156:159], v[172:175], v[50:53]
	v_mfma_f32_16x16x32_bf16 v[38:41], v[148:151], v[180:183], v[38:41]
	v_mfma_f32_16x16x32_bf16 v[34:37], v[156:159], v[180:183], v[34:37]
	v_mfma_f32_16x16x32_bf16 v[22:25], v[148:151], v[188:191], v[22:25]
	v_mfma_f32_16x16x32_bf16 v[18:21], v[156:159], v[188:191], v[18:21]
	s_barrier
	s_add_u32 s0, s26, 0x40000
	s_addc_u32 s1, s27, 0
	s_add_i32 s33, s36, s64
	v_lshl_add_u64 v[144:145], s[0:1], 0, v[194:195]
	s_mov_b32 m0, s33
	s_nop 0
	global_load_lds_dwordx4 v[144:145], off
	v_lshl_add_u64 v[144:145], s[0:1], 0, v[130:131]
	s_add_i32 m0, s33, 0x2000
	s_nop 0
	global_load_lds_dwordx4 v[144:145], off
	v_add_u32_e32 v156, 0x18000, v141
	ds_read_b128 v[144:147], v156
	ds_read_b128 v[148:151], v156 offset:1024
	ds_read_b128 v[152:155], v156 offset:2048
	ds_read_b128 v[156:159], v156 offset:3072
	s_waitcnt vmcnt(6)
	s_barrier
	v_mfma_f32_16x16x32_bf16 v[46:49], v[198:201], v[160:163], v[46:49]
	v_mfma_f32_16x16x32_bf16 v[42:45], v[206:209], v[160:163], v[42:45]
	v_mfma_f32_16x16x32_bf16 v[30:33], v[198:201], v[168:171], v[30:33]
	v_mfma_f32_16x16x32_bf16 v[26:29], v[206:209], v[168:171], v[26:29]
	v_mfma_f32_16x16x32_bf16 v[14:17], v[198:201], v[176:179], v[14:17]
	v_mfma_f32_16x16x32_bf16 v[10:13], v[206:209], v[176:179], v[10:13]
	v_mfma_f32_16x16x32_bf16 v[6:9], v[198:201], v[184:187], v[6:9]
	v_mfma_f32_16x16x32_bf16 v[2:5], v[206:209], v[184:187], v[2:5]
	v_mfma_f32_16x16x32_bf16 v[46:49], v[202:205], v[164:167], v[46:49]
	v_mfma_f32_16x16x32_bf16 v[42:45], v[210:213], v[164:167], v[42:45]
	v_mfma_f32_16x16x32_bf16 v[30:33], v[202:205], v[172:175], v[30:33]
	v_mfma_f32_16x16x32_bf16 v[26:29], v[210:213], v[172:175], v[26:29]
	v_mfma_f32_16x16x32_bf16 v[14:17], v[202:205], v[180:183], v[14:17]
	v_mfma_f32_16x16x32_bf16 v[10:13], v[210:213], v[180:183], v[10:13]
	v_mfma_f32_16x16x32_bf16 v[6:9], v[202:205], v[188:191], v[6:9]
	v_mfma_f32_16x16x32_bf16 v[2:5], v[210:213], v[188:191], v[2:5]
	s_add_i32 s33, 0, 0x18000
	s_barrier
	s_add_u32 s0, s28, 0x40000
	s_addc_u32 s1, s29, 0
	s_mov_b32 m0, s69
	v_lshl_add_u64 v[198:199], s[0:1], 0, v[134:135]
	ds_read_b128 v[160:163], v143 offset:32768
	ds_read_b128 v[164:167], v143 offset:33792
	ds_read_b128 v[168:171], v143 offset:34816
	ds_read_b128 v[172:175], v143 offset:35840
	ds_read_b128 v[176:179], v143 offset:36864
	ds_read_b128 v[180:183], v143 offset:37888
	ds_read_b128 v[184:187], v143 offset:38912
	ds_read_b128 v[188:191], v143 offset:39936
	global_load_lds_dwordx4 v[198:199], off
	v_lshl_add_u64 v[198:199], s[0:1], 0, v[132:133]
	s_mov_b32 m0, s70
	s_nop 0
	global_load_lds_dwordx4 v[198:199], off
	s_waitcnt lgkmcnt(8)
	s_barrier
	s_waitcnt lgkmcnt(0)
	v_mfma_f32_16x16x32_bf16 v[126:129], v[144:147], v[160:163], v[126:129]
	v_mfma_f32_16x16x32_bf16 v[122:125], v[152:155], v[160:163], v[122:125]
	v_mfma_f32_16x16x32_bf16 v[118:121], v[144:147], v[168:171], v[118:121]
	v_mfma_f32_16x16x32_bf16 v[114:117], v[152:155], v[168:171], v[114:117]
	v_mfma_f32_16x16x32_bf16 v[102:105], v[144:147], v[176:179], v[102:105]
	v_mfma_f32_16x16x32_bf16 v[98:101], v[152:155], v[176:179], v[98:101]
	v_mfma_f32_16x16x32_bf16 v[86:89], v[144:147], v[184:187], v[86:89]
	v_mfma_f32_16x16x32_bf16 v[82:85], v[152:155], v[184:187], v[82:85]
	v_mfma_f32_16x16x32_bf16 v[126:129], v[148:151], v[164:167], v[126:129]
	v_mfma_f32_16x16x32_bf16 v[122:125], v[156:159], v[164:167], v[122:125]
	v_mfma_f32_16x16x32_bf16 v[118:121], v[148:151], v[172:175], v[118:121]
	v_mfma_f32_16x16x32_bf16 v[114:117], v[156:159], v[172:175], v[114:117]
	v_mfma_f32_16x16x32_bf16 v[102:105], v[148:151], v[180:183], v[102:105]
	v_mfma_f32_16x16x32_bf16 v[98:101], v[156:159], v[180:183], v[98:101]
	v_mfma_f32_16x16x32_bf16 v[86:89], v[148:151], v[188:191], v[86:89]
	v_mfma_f32_16x16x32_bf16 v[82:85], v[156:159], v[188:191], v[82:85]
	s_barrier
	s_add_i32 s28, 0, 0x1c000
	s_add_i32 s0, s33, s64
	v_add_u32_e32 v196, s28, v141
	v_lshl_add_u64 v[192:193], v[192:193], 0, s[54:55]
	s_mov_b32 m0, s0
	ds_read_b128 v[198:201], v196
	ds_read_b128 v[202:205], v196 offset:1024
	ds_read_b128 v[206:209], v196 offset:2048
	ds_read_b128 v[210:213], v196 offset:3072
	global_load_lds_dwordx4 v[192:193], off
	v_lshl_add_u64 v[192:193], v[214:215], 0, s[54:55]
	s_add_i32 m0, s0, 0x2000
	s_nop 0
	global_load_lds_dwordx4 v[192:193], off
	s_barrier
	s_waitcnt lgkmcnt(0)
	v_mfma_f32_16x16x32_bf16 v[110:113], v[198:201], v[160:163], v[110:113]
	v_mfma_f32_16x16x32_bf16 v[106:109], v[206:209], v[160:163], v[106:109]
	v_mfma_f32_16x16x32_bf16 v[94:97], v[198:201], v[168:171], v[94:97]
	v_mfma_f32_16x16x32_bf16 v[90:93], v[206:209], v[168:171], v[90:93]
	v_mfma_f32_16x16x32_bf16 v[78:81], v[198:201], v[176:179], v[78:81]
	v_mfma_f32_16x16x32_bf16 v[74:77], v[206:209], v[176:179], v[74:77]
	v_mfma_f32_16x16x32_bf16 v[70:73], v[198:201], v[184:187], v[70:73]
	v_mfma_f32_16x16x32_bf16 v[66:69], v[206:209], v[184:187], v[66:69]
	v_mfma_f32_16x16x32_bf16 v[110:113], v[202:205], v[164:167], v[110:113]
	v_mfma_f32_16x16x32_bf16 v[106:109], v[210:213], v[164:167], v[106:109]
	v_mfma_f32_16x16x32_bf16 v[94:97], v[202:205], v[172:175], v[94:97]
	v_mfma_f32_16x16x32_bf16 v[90:93], v[210:213], v[172:175], v[90:93]
	v_mfma_f32_16x16x32_bf16 v[78:81], v[202:205], v[180:183], v[78:81]
	v_mfma_f32_16x16x32_bf16 v[74:77], v[210:213], v[180:183], v[74:77]
	v_mfma_f32_16x16x32_bf16 v[70:73], v[202:205], v[188:191], v[70:73]
	v_mfma_f32_16x16x32_bf16 v[66:69], v[210:213], v[188:191], v[66:69]
	s_mov_b32 m0, s71
	v_lshl_add_u64 v[192:193], v[216:217], 0, s[54:55]
	s_barrier
	ds_read_b128 v[160:163], v143 offset:49152
	ds_read_b128 v[164:167], v143 offset:50176
	ds_read_b128 v[168:171], v143 offset:51200
	ds_read_b128 v[172:175], v143 offset:52224
	ds_read_b128 v[176:179], v143 offset:53248
	ds_read_b128 v[180:183], v143 offset:54272
	ds_read_b128 v[184:187], v143 offset:55296
	ds_read_b128 v[188:191], v143 offset:56320
	global_load_lds_dwordx4 v[192:193], off
	v_lshl_add_u64 v[192:193], v[218:219], 0, s[54:55]
	s_mov_b32 m0, s72
	s_nop 0
	global_load_lds_dwordx4 v[192:193], off
	s_waitcnt vmcnt(10)
	s_barrier
	s_waitcnt lgkmcnt(0)
	v_mfma_f32_16x16x32_bf16 v[62:65], v[144:147], v[160:163], v[62:65]
	v_mfma_f32_16x16x32_bf16 v[58:61], v[152:155], v[160:163], v[58:61]
	v_mfma_f32_16x16x32_bf16 v[54:57], v[144:147], v[168:171], v[54:57]
	v_mfma_f32_16x16x32_bf16 v[50:53], v[152:155], v[168:171], v[50:53]
	v_mfma_f32_16x16x32_bf16 v[38:41], v[144:147], v[176:179], v[38:41]
	v_mfma_f32_16x16x32_bf16 v[34:37], v[152:155], v[176:179], v[34:37]
	v_mfma_f32_16x16x32_bf16 v[22:25], v[144:147], v[184:187], v[22:25]
	v_mfma_f32_16x16x32_bf16 v[18:21], v[152:155], v[184:187], v[18:21]
	v_mfma_f32_16x16x32_bf16 v[62:65], v[148:151], v[164:167], v[62:65]
	v_mfma_f32_16x16x32_bf16 v[58:61], v[156:159], v[164:167], v[58:61]
	v_mfma_f32_16x16x32_bf16 v[54:57], v[148:151], v[172:175], v[54:57]
	v_mfma_f32_16x16x32_bf16 v[50:53], v[156:159], v[172:175], v[50:53]
	v_mfma_f32_16x16x32_bf16 v[38:41], v[148:151], v[180:183], v[38:41]
	v_mfma_f32_16x16x32_bf16 v[34:37], v[156:159], v[180:183], v[34:37]
	v_mfma_f32_16x16x32_bf16 v[22:25], v[148:151], v[188:191], v[22:25]
	v_mfma_f32_16x16x32_bf16 v[18:21], v[156:159], v[188:191], v[18:21]
	s_barrier
	s_add_u32 s0, s26, 0x40080
	s_addc_u32 s1, s27, 0
	s_add_i32 s26, s28, s64
	v_lshl_add_u64 v[144:145], s[0:1], 0, v[194:195]
	s_mov_b32 m0, s26
	s_nop 0
	global_load_lds_dwordx4 v[144:145], off
	v_lshl_add_u64 v[144:145], s[0:1], 0, v[130:131]
	s_add_i32 m0, s26, 0x2000
	s_nop 0
	global_load_lds_dwordx4 v[144:145], off
	v_add_u32_e32 v156, 0x10000, v141
	ds_read_b128 v[144:147], v156
	ds_read_b128 v[148:151], v156 offset:1024
	ds_read_b128 v[152:155], v156 offset:2048
	ds_read_b128 v[156:159], v156 offset:3072
	s_waitcnt vmcnt(6)
	s_barrier
	v_mfma_f32_16x16x32_bf16 v[46:49], v[198:201], v[160:163], v[46:49]
	v_mfma_f32_16x16x32_bf16 v[42:45], v[206:209], v[160:163], v[42:45]
	v_mfma_f32_16x16x32_bf16 v[30:33], v[198:201], v[168:171], v[30:33]
	v_mfma_f32_16x16x32_bf16 v[26:29], v[206:209], v[168:171], v[26:29]
	v_mfma_f32_16x16x32_bf16 v[14:17], v[198:201], v[176:179], v[14:17]
	v_mfma_f32_16x16x32_bf16 v[10:13], v[206:209], v[176:179], v[10:13]
	v_mfma_f32_16x16x32_bf16 v[6:9], v[198:201], v[184:187], v[6:9]
	v_mfma_f32_16x16x32_bf16 v[2:5], v[206:209], v[184:187], v[2:5]
	v_mfma_f32_16x16x32_bf16 v[46:49], v[202:205], v[164:167], v[46:49]
	v_mfma_f32_16x16x32_bf16 v[42:45], v[210:213], v[164:167], v[42:45]
	v_mfma_f32_16x16x32_bf16 v[30:33], v[202:205], v[172:175], v[30:33]
	v_mfma_f32_16x16x32_bf16 v[26:29], v[210:213], v[172:175], v[26:29]
	v_mfma_f32_16x16x32_bf16 v[14:17], v[202:205], v[180:183], v[14:17]
	v_mfma_f32_16x16x32_bf16 v[10:13], v[210:213], v[180:183], v[10:13]
	v_mfma_f32_16x16x32_bf16 v[6:9], v[202:205], v[188:191], v[6:9]
	v_mfma_f32_16x16x32_bf16 v[2:5], v[210:213], v[188:191], v[2:5]
	s_add_i32 s82, s82, 2
	s_add_u32 s24, s24, 0x100
	s_addc_u32 s25, s25, 0
	s_add_u32 s78, s78, 0x100
	s_addc_u32 s79, s79, 0
	s_cmp_gt_u32 s82, 13
	s_barrier
	s_cbranch_scc0 .LBB0_1765
	s_waitcnt lgkmcnt(0)
	v_lshl_add_u32 v144, s12, 8, v1
	v_lshl_or_b32 v146, s75, 8, v142
	v_ashrrev_i32_e32 v145, 31, v144
	v_lshlrev_b64 v[148:149], 11, v[144:145]
	v_ashrrev_i32_e32 v147, 31, v146
	v_lshl_add_u64 v[148:149], s[10:11], 0, v[148:149]
	v_cvt_pk_bf16_f32 v126, v126, v127
	v_cvt_pk_bf16_f32 v127, v128, v129
	v_cvt_pk_bf16_f32 v128, v122, v123
	v_lshlrev_b64 v[122:123], 1, v[146:147]
	v_cvt_pk_bf16_f32 v129, v124, v125
	v_lshl_add_u64 v[124:125], v[148:149], 0, v[122:123]
	s_mov_b64 s[0:1], 0x40000
	v_cvt_pk_bf16_f32 v62, v62, v63
	v_cvt_pk_bf16_f32 v63, v64, v65
	v_cvt_pk_bf16_f32 v64, v58, v59
	v_lshl_add_u64 v[58:59], v[124:125], 0, s[0:1]
	s_mov_b32 s0, 0x40000
	v_cvt_pk_bf16_f32 v110, v110, v111
	v_cvt_pk_bf16_f32 v111, v112, v113
	v_cvt_pk_bf16_f32 v112, v106, v107
	v_or_b32_e32 v106, 16, v144
	v_cvt_pk_bf16_f32 v65, v60, v61
	v_add_co_u32_e32 v60, vcc, s0, v124
	v_cvt_pk_bf16_f32 v46, v46, v47
	v_cvt_pk_bf16_f32 v47, v48, v49
	v_cvt_pk_bf16_f32 v48, v42, v43
	v_cvt_pk_bf16_f32 v49, v44, v45
	s_mov_b64 s[0:1], 0x48000
	v_ashrrev_i32_e32 v107, 31, v106
	v_addc_co_u32_e32 v61, vcc, 0, v125, vcc
	global_store_dwordx4 v[58:59], v[46:49], off offset:256
	v_cvt_pk_bf16_f32 v113, v108, v109
	v_lshlrev_b64 v[106:107], 11, v[106:107]
	v_lshl_add_u64 v[46:47], v[124:125], 0, s[0:1]
	s_mov_b32 s0, 0x48000
	v_cvt_pk_bf16_f32 v94, v94, v95
	v_cvt_pk_bf16_f32 v95, v96, v97
	v_cvt_pk_bf16_f32 v96, v90, v91
	v_or_b32_e32 v90, 32, v144
	v_add_co_u32_e32 v48, vcc, s0, v124
	v_cvt_pk_bf16_f32 v30, v30, v31
	v_cvt_pk_bf16_f32 v31, v32, v33
	v_cvt_pk_bf16_f32 v32, v26, v27
	v_cvt_pk_bf16_f32 v33, v28, v29
	s_mov_b64 s[0:1], 0x50000
	global_store_dwordx4 v[124:125], v[110:113], off offset:256
	v_ashrrev_i32_e32 v91, 31, v90
	v_addc_co_u32_e32 v49, vcc, 0, v125, vcc
	v_lshl_add_u64 v[110:111], s[10:11], 0, v[106:107]
	global_store_dwordx4 v[46:47], v[30:33], off offset:256
	v_lshl_add_u64 v[110:111], v[110:111], 0, v[122:123]
	v_cvt_pk_bf16_f32 v97, v92, v93
	v_lshl_add_u64 v[30:31], v[124:125], 0, s[0:1]
	s_mov_b32 s0, 0x50000
	v_lshlrev_b64 v[90:91], 11, v[90:91]
	v_cvt_pk_bf16_f32 v78, v78, v79
	v_cvt_pk_bf16_f32 v79, v80, v81
	v_cvt_pk_bf16_f32 v80, v74, v75
	v_or_b32_e32 v74, 48, v144
	v_add_co_u32_e32 v32, vcc, s0, v124
	v_cvt_pk_bf16_f32 v14, v14, v15
	v_cvt_pk_bf16_f32 v15, v16, v17
	v_cvt_pk_bf16_f32 v16, v10, v11
	v_cvt_pk_bf16_f32 v17, v12, v13
	s_mov_b64 s[0:1], 0x58000
	global_store_dwordx4 v[110:111], v[94:97], off offset:256
	v_ashrrev_i32_e32 v75, 31, v74
	v_addc_co_u32_e32 v33, vcc, 0, v125, vcc
	v_lshl_add_u64 v[94:95], s[10:11], 0, v[90:91]
	global_store_dwordx4 v[30:31], v[14:17], off offset:256
	v_lshl_add_u64 v[94:95], v[94:95], 0, v[122:123]
	v_cvt_pk_bf16_f32 v81, v76, v77
	v_lshl_add_u64 v[14:15], v[124:125], 0, s[0:1]
	s_mov_b32 s0, 0x58000
	v_lshlrev_b64 v[74:75], 11, v[74:75]
	v_add_co_u32_e32 v16, vcc, s0, v124
	global_store_dwordx4 v[94:95], v[78:81], off offset:256
	s_nop 0
	v_addc_co_u32_e32 v17, vcc, 0, v125, vcc
	v_lshl_add_u64 v[78:79], s[10:11], 0, v[74:75]
	v_cvt_pk_bf16_f32 v106, v118, v119
	v_cvt_pk_bf16_f32 v107, v120, v121
	v_cvt_pk_bf16_f32 v108, v114, v115
	v_cvt_pk_bf16_f32 v109, v116, v117
	v_cvt_pk_bf16_f32 v90, v102, v103
	v_cvt_pk_bf16_f32 v91, v104, v105
	v_cvt_pk_bf16_f32 v92, v98, v99
	v_cvt_pk_bf16_f32 v93, v100, v101
	v_cvt_pk_bf16_f32 v74, v86, v87
	v_cvt_pk_bf16_f32 v75, v88, v89
	v_cvt_pk_bf16_f32 v76, v82, v83
	v_cvt_pk_bf16_f32 v77, v84, v85
	v_lshl_add_u64 v[78:79], v[78:79], 0, v[122:123]
	v_cvt_pk_bf16_f32 v70, v70, v71
	v_cvt_pk_bf16_f32 v71, v72, v73
	v_cvt_pk_bf16_f32 v72, v66, v67
	v_cvt_pk_bf16_f32 v73, v68, v69
	v_cvt_pk_bf16_f32 v42, v54, v55
	v_cvt_pk_bf16_f32 v43, v56, v57
	v_cvt_pk_bf16_f32 v44, v50, v51
	v_cvt_pk_bf16_f32 v45, v52, v53
	v_cvt_pk_bf16_f32 v26, v38, v39
	v_cvt_pk_bf16_f32 v27, v40, v41
	v_cvt_pk_bf16_f32 v28, v34, v35
	v_cvt_pk_bf16_f32 v29, v36, v37
	v_cvt_pk_bf16_f32 v10, v22, v23
	v_cvt_pk_bf16_f32 v11, v24, v25
	v_cvt_pk_bf16_f32 v12, v18, v19
	v_cvt_pk_bf16_f32 v13, v20, v21
	v_cvt_pk_bf16_f32 v6, v6, v7
	v_cvt_pk_bf16_f32 v7, v8, v9
	v_cvt_pk_bf16_f32 v8, v2, v3
	v_cvt_pk_bf16_f32 v9, v4, v5
	s_and_b64 vcc, exec, s[4:5]
	s_mov_b32 s75, s14
	s_mov_b32 s12, s18
	s_mov_b64 s[26:27], s[22:23]
	s_mov_b64 s[24:25], s[20:21]
	global_store_dwordx4 v[124:125], v[126:129], off
	global_store_dwordx4 v[110:111], v[106:109], off
	global_store_dwordx4 v[94:95], v[90:93], off
	global_store_dwordx4 v[78:79], v[74:77], off
	global_store_dwordx4 v[78:79], v[70:73], off offset:256
	global_store_dwordx4 v[60:61], v[62:65], off
	global_store_dwordx4 v[48:49], v[42:45], off
	global_store_dwordx4 v[32:33], v[26:29], off
	global_store_dwordx4 v[16:17], v[10:13], off
	global_store_dwordx4 v[14:15], v[6:9], off offset:256
	s_cbranch_vccz .LBB0_1762
	s_waitcnt vmcnt(0)
	s_cmpk_gt_u32 s34, 0xff
	s_cbranch_scc1 .LBB0_1769
	s_barrier

.LBB0_2475:
	s_add_u32 s22, s20, 0x100
	s_addc_u32 s23, s21, 0
	s_add_u32 s24, s75, s20
	s_addc_u32 s25, s76, s21
	s_cmpk_eq_i32 s20, 0x700
	s_cselect_b64 vcc, -1, 0
	s_and_b64 s[0:1], vcc, exec
	s_cselect_b32 s0, 0, s22
	s_cselect_b32 s25, s13, s25
	s_cselect_b32 s24, s15, s24
	s_add_i32 s1, 0, 0x10000
	s_add_u32 s26, s4, s0
	v_cndmask_b32_e32 v194, v136, v155, vcc
	v_cndmask_b32_e32 v192, v138, v156, vcc
	v_cndmask_b32_e32 v141, v140, v157, vcc
	v_cndmask_b32_e32 v143, v142, v158, vcc
	s_addc_u32 s27, s5, 0
	v_lshl_add_u64 v[214:215], v[146:147], 0, s[20:21]
	s_add_i32 m0, s38, 0xc000
	ds_read_b128 v[176:179], v154
	ds_read_b128 v[180:183], v154 offset:1024
	ds_read_b128 v[184:187], v154 offset:2048
	ds_read_b128 v[188:191], v154 offset:3072
	ds_read_b128 v[198:201], v154 offset:4096
	ds_read_b128 v[202:205], v154 offset:5120
	ds_read_b128 v[206:209], v154 offset:6144
	ds_read_b128 v[210:213], v154 offset:7168
	global_load_lds_dwordx4 v[214:215], off
	v_lshl_add_u64 v[214:215], v[144:145], 0, s[20:21]
	s_add_i32 m0, s38, 0xe000
	s_nop 0
	global_load_lds_dwordx4 v[214:215], off
	s_waitcnt lgkmcnt(8)
	s_barrier
	s_waitcnt lgkmcnt(0)
	v_mfma_f32_16x16x32_bf16 v[126:129], v[160:163], v[176:179], v[126:129]
	v_mfma_f32_16x16x32_bf16 v[122:125], v[168:171], v[176:179], v[122:125]
	v_mfma_f32_16x16x32_bf16 v[118:121], v[160:163], v[184:187], v[118:121]
	v_mfma_f32_16x16x32_bf16 v[114:117], v[168:171], v[184:187], v[114:117]
	v_mfma_f32_16x16x32_bf16 v[94:97], v[160:163], v[198:201], v[94:97]
	v_mfma_f32_16x16x32_bf16 v[90:93], v[168:171], v[198:201], v[90:93]
	v_mfma_f32_16x16x32_bf16 v[86:89], v[160:163], v[206:209], v[86:89]
	v_mfma_f32_16x16x32_bf16 v[82:85], v[168:171], v[206:209], v[82:85]
	v_mfma_f32_16x16x32_bf16 v[126:129], v[164:167], v[180:183], v[126:129]
	v_mfma_f32_16x16x32_bf16 v[122:125], v[172:175], v[180:183], v[122:125]
	v_mfma_f32_16x16x32_bf16 v[118:121], v[164:167], v[188:191], v[118:121]
	v_mfma_f32_16x16x32_bf16 v[114:117], v[172:175], v[188:191], v[114:117]
	v_mfma_f32_16x16x32_bf16 v[94:97], v[164:167], v[202:205], v[94:97]
	v_mfma_f32_16x16x32_bf16 v[90:93], v[172:175], v[202:205], v[90:93]
	v_mfma_f32_16x16x32_bf16 v[86:89], v[164:167], v[210:213], v[86:89]
	v_mfma_f32_16x16x32_bf16 v[82:85], v[172:175], v[210:213], v[82:85]
	s_barrier
	s_add_i32 s20, 0, 0x14000
	s_add_i32 s0, s1, s35
	v_add_u32_e32 v159, s20, v139
	v_lshl_add_u64 v[224:225], s[24:25], 0, v[130:131]
	s_mov_b32 m0, s0
	ds_read_b128 v[214:217], v159
	ds_read_b128 v[218:221], v159 offset:1024
	ds_read_b128 v[238:241], v159 offset:2048
	ds_read_b128 v[242:245], v159 offset:3072
	global_load_lds_dwordx4 v[224:225], off
	v_lshl_add_u64 v[230:231], s[24:25], 0, v[132:133]
	s_add_i32 m0, s0, 0x2000
	s_nop 0
	global_load_lds_dwordx4 v[230:231], off
	s_barrier
	s_waitcnt lgkmcnt(0)
	v_mfma_f32_16x16x32_bf16 v[110:113], v[214:217], v[176:179], v[110:113]
	v_mfma_f32_16x16x32_bf16 v[106:109], v[238:241], v[176:179], v[106:109]
	v_mfma_f32_16x16x32_bf16 v[102:105], v[214:217], v[184:187], v[102:105]
	v_mfma_f32_16x16x32_bf16 v[98:101], v[238:241], v[184:187], v[98:101]
	v_mfma_f32_16x16x32_bf16 v[78:81], v[214:217], v[198:201], v[78:81]
	v_mfma_f32_16x16x32_bf16 v[74:77], v[238:241], v[198:201], v[74:77]
	v_mfma_f32_16x16x32_bf16 v[70:73], v[214:217], v[206:209], v[70:73]
	v_mfma_f32_16x16x32_bf16 v[66:69], v[238:241], v[206:209], v[66:69]
	v_mfma_f32_16x16x32_bf16 v[110:113], v[218:221], v[180:183], v[110:113]
	v_mfma_f32_16x16x32_bf16 v[106:109], v[242:245], v[180:183], v[106:109]
	v_mfma_f32_16x16x32_bf16 v[102:105], v[218:221], v[188:191], v[102:105]
	v_mfma_f32_16x16x32_bf16 v[98:101], v[242:245], v[188:191], v[98:101]
	v_mfma_f32_16x16x32_bf16 v[78:81], v[218:221], v[202:205], v[78:81]
	v_mfma_f32_16x16x32_bf16 v[74:77], v[242:245], v[202:205], v[74:77]
	v_mfma_f32_16x16x32_bf16 v[70:73], v[218:221], v[210:213], v[70:73]
	v_mfma_f32_16x16x32_bf16 v[66:69], v[242:245], v[210:213], v[66:69]
	s_mov_b32 m0, s38
	s_barrier
	ds_read_b128 v[176:179], v154 offset:16384
	ds_read_b128 v[180:183], v154 offset:17408
	ds_read_b128 v[184:187], v154 offset:18432
	ds_read_b128 v[188:191], v154 offset:19456
	ds_read_b128 v[198:201], v154 offset:20480
	ds_read_b128 v[202:205], v154 offset:21504
	ds_read_b128 v[206:209], v154 offset:22528
	ds_read_b128 v[210:213], v154 offset:23552
	global_load_lds_dwordx4 v194, s[26:27]
	s_mov_b32 m0, s40
	v_mov_b32_e32 v193, v195
	global_load_lds_dwordx4 v192, s[26:27]
	s_waitcnt vmcnt(10)
	s_barrier
	s_waitcnt lgkmcnt(0)
	v_lshl_add_u64 v[232:233], s[26:27], 0, v[194:195]
	v_lshl_add_u64 v[192:193], s[26:27], 0, v[192:193]
	s_waitcnt lgkmcnt(0)
	v_mfma_f32_16x16x32_bf16 v[62:65], v[160:163], v[176:179], v[62:65]
	v_mfma_f32_16x16x32_bf16 v[58:61], v[168:171], v[176:179], v[58:61]
	v_mfma_f32_16x16x32_bf16 v[54:57], v[160:163], v[184:187], v[54:57]
	v_mfma_f32_16x16x32_bf16 v[50:53], v[168:171], v[184:187], v[50:53]
	v_mfma_f32_16x16x32_bf16 v[30:33], v[160:163], v[198:201], v[30:33]
	v_mfma_f32_16x16x32_bf16 v[26:29], v[168:171], v[198:201], v[26:29]
	v_mfma_f32_16x16x32_bf16 v[22:25], v[160:163], v[206:209], v[22:25]
	v_mfma_f32_16x16x32_bf16 v[18:21], v[168:171], v[206:209], v[18:21]
	v_mfma_f32_16x16x32_bf16 v[62:65], v[164:167], v[180:183], v[62:65]
	v_mfma_f32_16x16x32_bf16 v[58:61], v[172:175], v[180:183], v[58:61]
	v_mfma_f32_16x16x32_bf16 v[54:57], v[164:167], v[188:191], v[54:57]
	v_mfma_f32_16x16x32_bf16 v[50:53], v[172:175], v[188:191], v[50:53]
	v_mfma_f32_16x16x32_bf16 v[30:33], v[164:167], v[202:205], v[30:33]
	v_mfma_f32_16x16x32_bf16 v[26:29], v[172:175], v[202:205], v[26:29]
	v_mfma_f32_16x16x32_bf16 v[22:25], v[164:167], v[210:213], v[22:25]
	v_mfma_f32_16x16x32_bf16 v[18:21], v[172:175], v[210:213], v[18:21]
	s_barrier
	s_add_u32 s0, s24, 0x40000
	s_addc_u32 s1, s25, 0
	s_add_i32 s20, s20, s35
	v_lshl_add_u64 v[160:161], s[0:1], 0, v[130:131]
	s_mov_b32 m0, s20
	s_nop 0
	global_load_lds_dwordx4 v[160:161], off
	v_lshl_add_u64 v[160:161], s[0:1], 0, v[132:133]
	s_add_i32 m0, s20, 0x2000
	s_nop 0
	global_load_lds_dwordx4 v[160:161], off
	v_add_u32_e32 v172, 0x18000, v139
	ds_read_b128 v[160:163], v172
	ds_read_b128 v[164:167], v172 offset:1024
	ds_read_b128 v[168:171], v172 offset:2048
	ds_read_b128 v[172:175], v172 offset:3072
	s_waitcnt vmcnt(6)
	s_barrier
	v_mfma_f32_16x16x32_bf16 v[46:49], v[214:217], v[176:179], v[46:49]
	v_mfma_f32_16x16x32_bf16 v[42:45], v[238:241], v[176:179], v[42:45]
	v_mfma_f32_16x16x32_bf16 v[38:41], v[214:217], v[184:187], v[38:41]
	v_mfma_f32_16x16x32_bf16 v[34:37], v[238:241], v[184:187], v[34:37]
	v_mfma_f32_16x16x32_bf16 v[14:17], v[214:217], v[198:201], v[14:17]
	v_mfma_f32_16x16x32_bf16 v[10:13], v[238:241], v[198:201], v[10:13]
	v_mfma_f32_16x16x32_bf16 v[6:9], v[214:217], v[206:209], v[6:9]
	v_mfma_f32_16x16x32_bf16 v[2:5], v[238:241], v[206:209], v[2:5]
	v_mfma_f32_16x16x32_bf16 v[46:49], v[218:221], v[180:183], v[46:49]
	v_mfma_f32_16x16x32_bf16 v[42:45], v[242:245], v[180:183], v[42:45]
	v_mfma_f32_16x16x32_bf16 v[38:41], v[218:221], v[188:191], v[38:41]
	v_mfma_f32_16x16x32_bf16 v[34:37], v[242:245], v[188:191], v[34:37]
	v_mfma_f32_16x16x32_bf16 v[14:17], v[218:221], v[202:205], v[14:17]
	v_mfma_f32_16x16x32_bf16 v[10:13], v[242:245], v[202:205], v[10:13]
	v_mfma_f32_16x16x32_bf16 v[6:9], v[218:221], v[210:213], v[6:9]
	v_mfma_f32_16x16x32_bf16 v[2:5], v[242:245], v[210:213], v[2:5]
	s_add_i32 s0, 0, 0x18000
	s_barrier
	s_mov_b32 m0, s43
	ds_read_b128 v[176:179], v154 offset:32768
	ds_read_b128 v[180:183], v154 offset:33792
	ds_read_b128 v[184:187], v154 offset:34816
	ds_read_b128 v[188:191], v154 offset:35840
	ds_read_b128 v[198:201], v154 offset:36864
	ds_read_b128 v[202:205], v154 offset:37888
	ds_read_b128 v[206:209], v154 offset:38912
	ds_read_b128 v[210:213], v154 offset:39936
	global_load_lds_dwordx4 v141, s[26:27]
	s_mov_b32 m0, s64
	s_nop 0
	global_load_lds_dwordx4 v143, s[26:27]
	s_waitcnt lgkmcnt(8)
	s_barrier
	s_waitcnt lgkmcnt(0)
	v_mfma_f32_16x16x32_bf16 v[126:129], v[160:163], v[176:179], v[126:129]
	v_mfma_f32_16x16x32_bf16 v[122:125], v[168:171], v[176:179], v[122:125]
	v_mfma_f32_16x16x32_bf16 v[118:121], v[160:163], v[184:187], v[118:121]
	v_mfma_f32_16x16x32_bf16 v[114:117], v[168:171], v[184:187], v[114:117]
	v_mfma_f32_16x16x32_bf16 v[94:97], v[160:163], v[198:201], v[94:97]
	v_mfma_f32_16x16x32_bf16 v[90:93], v[168:171], v[198:201], v[90:93]
	v_mfma_f32_16x16x32_bf16 v[86:89], v[160:163], v[206:209], v[86:89]
	v_mfma_f32_16x16x32_bf16 v[82:85], v[168:171], v[206:209], v[82:85]
	v_mfma_f32_16x16x32_bf16 v[126:129], v[164:167], v[180:183], v[126:129]
	v_mfma_f32_16x16x32_bf16 v[122:125], v[172:175], v[180:183], v[122:125]
	v_mfma_f32_16x16x32_bf16 v[118:121], v[164:167], v[188:191], v[118:121]
	v_mfma_f32_16x16x32_bf16 v[114:117], v[172:175], v[188:191], v[114:117]
	v_mfma_f32_16x16x32_bf16 v[94:97], v[164:167], v[202:205], v[94:97]
	v_mfma_f32_16x16x32_bf16 v[90:93], v[172:175], v[202:205], v[90:93]
	v_mfma_f32_16x16x32_bf16 v[86:89], v[164:167], v[210:213], v[86:89]
	v_mfma_f32_16x16x32_bf16 v[82:85], v[172:175], v[210:213], v[82:85]
	s_barrier
	s_add_i32 s20, 0, 0x1c000
	s_add_i32 s0, s0, s35
	v_add_u32_e32 v141, s20, v139
	v_lshl_add_u64 v[224:225], v[224:225], 0, s[54:55]
	s_mov_b32 m0, s0
	ds_read_b128 v[214:217], v141
	ds_read_b128 v[218:221], v141 offset:1024
	ds_read_b128 v[238:241], v141 offset:2048
	ds_read_b128 v[242:245], v141 offset:3072
	global_load_lds_dwordx4 v[224:225], off
	v_lshl_add_u64 v[224:225], v[230:231], 0, s[54:55]
	s_add_i32 m0, s0, 0x2000
	s_nop 0
	global_load_lds_dwordx4 v[224:225], off
	s_barrier
	s_waitcnt lgkmcnt(0)
	v_mfma_f32_16x16x32_bf16 v[110:113], v[214:217], v[176:179], v[110:113]
	v_mfma_f32_16x16x32_bf16 v[106:109], v[238:241], v[176:179], v[106:109]
	v_mfma_f32_16x16x32_bf16 v[102:105], v[214:217], v[184:187], v[102:105]
	v_mfma_f32_16x16x32_bf16 v[98:101], v[238:241], v[184:187], v[98:101]
	v_mfma_f32_16x16x32_bf16 v[78:81], v[214:217], v[198:201], v[78:81]
	v_mfma_f32_16x16x32_bf16 v[74:77], v[238:241], v[198:201], v[74:77]
	v_mfma_f32_16x16x32_bf16 v[70:73], v[214:217], v[206:209], v[70:73]
	v_mfma_f32_16x16x32_bf16 v[66:69], v[238:241], v[206:209], v[66:69]
	v_mfma_f32_16x16x32_bf16 v[110:113], v[218:221], v[180:183], v[110:113]
	v_mfma_f32_16x16x32_bf16 v[106:109], v[242:245], v[180:183], v[106:109]
	v_mfma_f32_16x16x32_bf16 v[102:105], v[218:221], v[188:191], v[102:105]
	v_mfma_f32_16x16x32_bf16 v[98:101], v[242:245], v[188:191], v[98:101]
	v_mfma_f32_16x16x32_bf16 v[78:81], v[218:221], v[202:205], v[78:81]
	v_mfma_f32_16x16x32_bf16 v[74:77], v[242:245], v[202:205], v[74:77]
	v_mfma_f32_16x16x32_bf16 v[70:73], v[218:221], v[210:213], v[70:73]
	v_mfma_f32_16x16x32_bf16 v[66:69], v[242:245], v[210:213], v[66:69]
	s_mov_b32 m0, s65
	v_lshl_add_u64 v[224:225], v[232:233], 0, s[54:55]
	s_barrier
	ds_read_b128 v[176:179], v154 offset:49152
	ds_read_b128 v[180:183], v154 offset:50176
	ds_read_b128 v[184:187], v154 offset:51200
	ds_read_b128 v[188:191], v154 offset:52224
	ds_read_b128 v[198:201], v154 offset:53248
	ds_read_b128 v[202:205], v154 offset:54272
	ds_read_b128 v[206:209], v154 offset:55296
	ds_read_b128 v[210:213], v154 offset:56320
	global_load_lds_dwordx4 v[224:225], off
	v_lshl_add_u64 v[192:193], v[192:193], 0, s[54:55]
	s_mov_b32 m0, s66
	s_nop 0
	global_load_lds_dwordx4 v[192:193], off
	s_waitcnt vmcnt(10)
	s_barrier
	s_waitcnt lgkmcnt(0)
	v_mfma_f32_16x16x32_bf16 v[62:65], v[160:163], v[176:179], v[62:65]
	v_mfma_f32_16x16x32_bf16 v[58:61], v[168:171], v[176:179], v[58:61]
	v_mfma_f32_16x16x32_bf16 v[54:57], v[160:163], v[184:187], v[54:57]
	v_mfma_f32_16x16x32_bf16 v[50:53], v[168:171], v[184:187], v[50:53]
	v_mfma_f32_16x16x32_bf16 v[30:33], v[160:163], v[198:201], v[30:33]
	v_mfma_f32_16x16x32_bf16 v[26:29], v[168:171], v[198:201], v[26:29]
	v_mfma_f32_16x16x32_bf16 v[22:25], v[160:163], v[206:209], v[22:25]
	v_mfma_f32_16x16x32_bf16 v[18:21], v[168:171], v[206:209], v[18:21]
	v_mfma_f32_16x16x32_bf16 v[62:65], v[164:167], v[180:183], v[62:65]
	v_mfma_f32_16x16x32_bf16 v[58:61], v[172:175], v[180:183], v[58:61]
	v_mfma_f32_16x16x32_bf16 v[54:57], v[164:167], v[188:191], v[54:57]
	v_mfma_f32_16x16x32_bf16 v[50:53], v[172:175], v[188:191], v[50:53]
	v_mfma_f32_16x16x32_bf16 v[30:33], v[164:167], v[202:205], v[30:33]
	v_mfma_f32_16x16x32_bf16 v[26:29], v[172:175], v[202:205], v[26:29]
	v_mfma_f32_16x16x32_bf16 v[22:25], v[164:167], v[210:213], v[22:25]
	v_mfma_f32_16x16x32_bf16 v[18:21], v[172:175], v[210:213], v[18:21]
	s_barrier
	s_add_u32 s0, s24, 0x40080
	s_addc_u32 s1, s25, 0
	s_add_i32 s20, s20, s35
	v_lshl_add_u64 v[160:161], s[0:1], 0, v[130:131]
	s_mov_b32 m0, s20
	s_nop 0
	global_load_lds_dwordx4 v[160:161], off
	v_lshl_add_u64 v[160:161], s[0:1], 0, v[132:133]
	s_add_i32 m0, s20, 0x2000
	s_nop 0
	global_load_lds_dwordx4 v[160:161], off
	v_add_u32_e32 v172, 0x10000, v139
	ds_read_b128 v[160:163], v172
	ds_read_b128 v[164:167], v172 offset:1024
	ds_read_b128 v[168:171], v172 offset:2048
	ds_read_b128 v[172:175], v172 offset:3072
	s_waitcnt vmcnt(6)
	s_barrier
	v_mfma_f32_16x16x32_bf16 v[46:49], v[214:217], v[176:179], v[46:49]
	v_mfma_f32_16x16x32_bf16 v[42:45], v[238:241], v[176:179], v[42:45]
	v_mfma_f32_16x16x32_bf16 v[38:41], v[214:217], v[184:187], v[38:41]
	v_mfma_f32_16x16x32_bf16 v[34:37], v[238:241], v[184:187], v[34:37]
	v_mfma_f32_16x16x32_bf16 v[14:17], v[214:217], v[198:201], v[14:17]
	v_mfma_f32_16x16x32_bf16 v[10:13], v[238:241], v[198:201], v[10:13]
	v_mfma_f32_16x16x32_bf16 v[6:9], v[214:217], v[206:209], v[6:9]
	v_mfma_f32_16x16x32_bf16 v[2:5], v[238:241], v[206:209], v[2:5]
	v_mfma_f32_16x16x32_bf16 v[46:49], v[218:221], v[180:183], v[46:49]
	v_mfma_f32_16x16x32_bf16 v[42:45], v[242:245], v[180:183], v[42:45]
	v_mfma_f32_16x16x32_bf16 v[38:41], v[218:221], v[188:191], v[38:41]
	v_mfma_f32_16x16x32_bf16 v[34:37], v[242:245], v[188:191], v[34:37]
	v_mfma_f32_16x16x32_bf16 v[14:17], v[218:221], v[202:205], v[14:17]
	v_mfma_f32_16x16x32_bf16 v[10:13], v[242:245], v[202:205], v[10:13]
	v_mfma_f32_16x16x32_bf16 v[6:9], v[218:221], v[210:213], v[6:9]
	v_mfma_f32_16x16x32_bf16 v[2:5], v[242:245], v[210:213], v[2:5]
	s_add_i32 s77, s77, 2
	s_cmp_gt_u32 s77, 13
	s_mov_b64 s[20:21], s[22:23]
	s_barrier
	s_cbranch_scc0 .LBB0_2475
	s_waitcnt lgkmcnt(0)
	v_mul_f32_e32 v142, 0xbfb8aa3b, v126
	v_mul_f32_e32 v143, 0xbfb8aa3b, v127
	v_exp_f32_e32 v142, v142
	v_exp_f32_e32 v143, v143
	v_lshl_add_u32 v136, s73, 8, v137
	v_lshl_or_b32 v138, s74, 8, v153
	v_add_f32_e32 v142, 1.0, v142
	v_add_f32_e32 v143, 1.0, v143
	v_rcp_f32_e32 v142, v142
	v_rcp_f32_e32 v143, v143
	v_or_b32_e32 v140, v136, v151
	v_ashrrev_i32_e32 v141, 31, v140
	v_lshlrev_b64 v[140:141], 10, v[140:141]
	v_pk_mul_f32 v[126:127], v[126:127], v[142:143]
	v_lshl_add_u64 v[140:141], v[134:135], 0, v[140:141]
	v_pk_mul_f32 v[122:123], v[122:123], v[126:127]
	s_and_b64 vcc, exec, s[16:17]
	v_cvt_pk_bf16_f32 v122, v122, v123
	v_mul_f32_e32 v123, 0xbfb8aa3b, v128
	v_exp_f32_e32 v123, v123
	v_mov_b32_e32 v142, v158
	s_mov_b32 s74, s14
	s_mov_b32 s73, s72
	v_add_f32_e32 v123, 1.0, v123
	v_rcp_f32_e32 v126, v123
	v_mul_f32_e32 v123, 0xbfb8aa3b, v129
	v_exp_f32_e32 v123, v123
	s_mov_b64 s[20:21], s[18:19]
	v_add_f32_e32 v123, 1.0, v123
	v_rcp_f32_e32 v127, v123
	s_nop 0
	v_pk_mul_f32 v[126:127], v[128:129], v[126:127]
	s_nop 0
	v_pk_mul_f32 v[124:125], v[124:125], v[126:127]
	s_nop 0
	v_cvt_pk_bf16_f32 v123, v124, v125
	v_mul_f32_e32 v124, 0xbfb8aa3b, v118
	v_mul_f32_e32 v125, 0xbfb8aa3b, v119
	v_exp_f32_e32 v124, v124
	v_exp_f32_e32 v125, v125
	v_add_f32_e32 v124, 1.0, v124
	v_add_f32_e32 v125, 1.0, v125
	v_rcp_f32_e32 v124, v124
	v_rcp_f32_e32 v125, v125
	s_nop 0
	v_pk_mul_f32 v[118:119], v[118:119], v[124:125]
	s_nop 0
	v_pk_mul_f32 v[114:115], v[114:115], v[118:119]
	v_mul_f32_e32 v118, 0xbfb8aa3b, v110
	v_mul_f32_e32 v119, 0xbfb8aa3b, v111
	v_exp_f32_e32 v118, v118
	v_exp_f32_e32 v119, v119
	v_cvt_pk_bf16_f32 v124, v114, v115
	v_mul_f32_e32 v114, 0xbfb8aa3b, v120
	v_add_f32_e32 v118, 1.0, v118
	v_add_f32_e32 v119, 1.0, v119
	v_rcp_f32_e32 v118, v118
	v_rcp_f32_e32 v119, v119
	v_mul_f32_e32 v115, 0xbfb8aa3b, v121
	v_exp_f32_e32 v114, v114
	v_exp_f32_e32 v115, v115
	v_pk_mul_f32 v[110:111], v[110:111], v[118:119]
	v_permlane16_swap_b32_e32 v122, v124
	v_pk_mul_f32 v[106:107], v[106:107], v[110:111]
	v_add_f32_e32 v114, 1.0, v114
	v_cvt_pk_bf16_f32 v106, v106, v107
	v_mul_f32_e32 v107, 0xbfb8aa3b, v112
	v_exp_f32_e32 v107, v107
	v_add_f32_e32 v115, 1.0, v115
	v_rcp_f32_e32 v114, v114
	v_rcp_f32_e32 v115, v115
	v_add_f32_e32 v107, 1.0, v107
	v_rcp_f32_e32 v110, v107
	v_mul_f32_e32 v107, 0xbfb8aa3b, v113
	v_exp_f32_e32 v107, v107
	v_pk_mul_f32 v[114:115], v[120:121], v[114:115]
	v_add_f32_e32 v107, 1.0, v107
	v_rcp_f32_e32 v111, v107
	v_pk_mul_f32 v[114:115], v[116:117], v[114:115]
	v_pk_mul_f32 v[110:111], v[112:113], v[110:111]
	s_nop 0
	v_pk_mul_f32 v[108:109], v[108:109], v[110:111]
	v_cvt_pk_bf16_f32 v125, v114, v115
	v_cvt_pk_bf16_f32 v107, v108, v109
	v_mul_f32_e32 v108, 0xbfb8aa3b, v102
	v_mul_f32_e32 v109, 0xbfb8aa3b, v103
	v_exp_f32_e32 v108, v108
	v_exp_f32_e32 v109, v109
	v_ashrrev_i32_e32 v114, 1, v138
	v_ashrrev_i32_e32 v115, 31, v114
	v_add_f32_e32 v108, 1.0, v108
	v_add_f32_e32 v109, 1.0, v109
	v_rcp_f32_e32 v108, v108
	v_rcp_f32_e32 v109, v109
	v_lshlrev_b64 v[114:115], 1, v[114:115]
	v_permlane16_swap_b32_e32 v123, v125
	v_pk_mul_f32 v[102:103], v[102:103], v[108:109]
	v_lshl_add_u64 v[116:117], v[140:141], 0, v[114:115]
	v_pk_mul_f32 v[98:99], v[98:99], v[102:103]
	v_mov_b32_e32 v138, v156
	v_cvt_pk_bf16_f32 v108, v98, v99
	v_mul_f32_e32 v98, 0xbfb8aa3b, v104
	v_mul_f32_e32 v99, 0xbfb8aa3b, v105
	v_exp_f32_e32 v98, v98
	v_exp_f32_e32 v99, v99
	v_permlane16_swap_b32_e32 v106, v108
	v_add_f32_e32 v98, 1.0, v98
	v_add_f32_e32 v99, 1.0, v99
	v_rcp_f32_e32 v98, v98
	v_rcp_f32_e32 v99, v99
	v_mov_b32_e32 v140, v157
	global_store_dwordx4 v[116:117], v[122:125], off
	v_pk_mul_f32 v[98:99], v[104:105], v[98:99]
	s_nop 0
	v_pk_mul_f32 v[98:99], v[100:101], v[98:99]
	v_mul_f32_e32 v100, 0xbfb8aa3b, v94
	v_mul_f32_e32 v101, 0xbfb8aa3b, v95
	v_exp_f32_e32 v100, v100
	v_exp_f32_e32 v101, v101
	v_cvt_pk_bf16_f32 v109, v98, v99
	v_or_b32_e32 v98, v136, v152
	v_add_f32_e32 v100, 1.0, v100
	v_add_f32_e32 v101, 1.0, v101
	v_rcp_f32_e32 v100, v100
	v_rcp_f32_e32 v101, v101
	v_ashrrev_i32_e32 v99, 31, v98
	v_lshlrev_b64 v[98:99], 10, v[98:99]
	v_lshl_add_u64 v[98:99], v[134:135], 0, v[98:99]
	v_pk_mul_f32 v[94:95], v[94:95], v[100:101]
	v_permlane16_swap_b32_e32 v107, v109
	v_pk_mul_f32 v[90:91], v[90:91], v[94:95]
	global_store_dwordx4 v[116:117], v[106:109], off offset:128
	v_cvt_pk_bf16_f32 v90, v90, v91
	v_mul_f32_e32 v91, 0xbfb8aa3b, v96
	v_exp_f32_e32 v91, v91
	s_nop 0
	v_add_f32_e32 v91, 1.0, v91
	v_rcp_f32_e32 v94, v91
	v_mul_f32_e32 v91, 0xbfb8aa3b, v97
	v_exp_f32_e32 v91, v91
	s_nop 0
	v_add_f32_e32 v91, 1.0, v91
	v_rcp_f32_e32 v95, v91
	s_nop 0
	v_pk_mul_f32 v[94:95], v[96:97], v[94:95]
	s_nop 0
	v_pk_mul_f32 v[92:93], v[92:93], v[94:95]
	s_nop 0
	v_cvt_pk_bf16_f32 v91, v92, v93
	v_mul_f32_e32 v92, 0xbfb8aa3b, v86
	v_mul_f32_e32 v93, 0xbfb8aa3b, v87
	v_exp_f32_e32 v92, v92
	v_exp_f32_e32 v93, v93
	v_add_f32_e32 v92, 1.0, v92
	v_add_f32_e32 v93, 1.0, v93
	v_rcp_f32_e32 v92, v92
	v_rcp_f32_e32 v93, v93
	s_nop 0
	v_pk_mul_f32 v[86:87], v[86:87], v[92:93]
	s_nop 0
	v_pk_mul_f32 v[82:83], v[82:83], v[86:87]
	s_nop 0
	v_cvt_pk_bf16_f32 v92, v82, v83
	v_mul_f32_e32 v82, 0xbfb8aa3b, v88
	v_mul_f32_e32 v83, 0xbfb8aa3b, v89
	v_exp_f32_e32 v82, v82
	v_exp_f32_e32 v83, v83
	v_permlane16_swap_b32_e32 v90, v92
	v_add_f32_e32 v82, 1.0, v82
	v_add_f32_e32 v83, 1.0, v83
	v_rcp_f32_e32 v82, v82
	v_rcp_f32_e32 v83, v83
	s_nop 0
	v_pk_mul_f32 v[82:83], v[88:89], v[82:83]
	s_nop 0
	v_pk_mul_f32 v[82:83], v[84:85], v[82:83]
	v_mul_f32_e32 v84, 0xbfb8aa3b, v78
	v_mul_f32_e32 v85, 0xbfb8aa3b, v79
	v_exp_f32_e32 v84, v84
	v_exp_f32_e32 v85, v85
	v_cvt_pk_bf16_f32 v93, v82, v83
	s_nop 1
	v_permlane16_swap_b32_e32 v91, v93
	v_add_f32_e32 v84, 1.0, v84
	v_add_f32_e32 v85, 1.0, v85
	v_rcp_f32_e32 v84, v84
	v_rcp_f32_e32 v85, v85
	v_lshl_add_u64 v[82:83], v[98:99], 0, v[114:115]
	global_store_dwordx4 v[82:83], v[90:93], off
	v_pk_mul_f32 v[78:79], v[78:79], v[84:85]
	s_nop 0
	v_pk_mul_f32 v[74:75], v[74:75], v[78:79]
	s_nop 0
	v_cvt_pk_bf16_f32 v74, v74, v75
	v_mul_f32_e32 v75, 0xbfb8aa3b, v80
	v_exp_f32_e32 v75, v75
	s_nop 0
	v_add_f32_e32 v75, 1.0, v75
	v_rcp_f32_e32 v78, v75
	v_mul_f32_e32 v75, 0xbfb8aa3b, v81
	v_exp_f32_e32 v75, v75
	s_nop 0
	v_add_f32_e32 v75, 1.0, v75
	v_rcp_f32_e32 v79, v75
	s_nop 0
	v_pk_mul_f32 v[78:79], v[80:81], v[78:79]
	s_nop 0
	v_pk_mul_f32 v[76:77], v[76:77], v[78:79]
	s_nop 0
	v_cvt_pk_bf16_f32 v75, v76, v77
	v_mul_f32_e32 v76, 0xbfb8aa3b, v70
	v_mul_f32_e32 v77, 0xbfb8aa3b, v71
	v_exp_f32_e32 v76, v76
	v_exp_f32_e32 v77, v77
	v_add_f32_e32 v76, 1.0, v76
	v_add_f32_e32 v77, 1.0, v77
	v_rcp_f32_e32 v76, v76
	v_rcp_f32_e32 v77, v77
	s_nop 0
	v_pk_mul_f32 v[70:71], v[70:71], v[76:77]
	s_nop 0
	v_pk_mul_f32 v[66:67], v[66:67], v[70:71]
	v_add_u32_e32 v70, 0x80, v136
	v_cvt_pk_bf16_f32 v76, v66, v67
	v_mul_f32_e32 v66, 0xbfb8aa3b, v72
	v_mul_f32_e32 v67, 0xbfb8aa3b, v73
	v_exp_f32_e32 v66, v66
	v_exp_f32_e32 v67, v67
	v_permlane16_swap_b32_e32 v74, v76
	v_add_f32_e32 v66, 1.0, v66
	v_add_f32_e32 v67, 1.0, v67
	v_rcp_f32_e32 v66, v66
	v_rcp_f32_e32 v67, v67
	v_mov_b32_e32 v136, v155
	v_pk_mul_f32 v[66:67], v[72:73], v[66:67]
	s_nop 0
	v_pk_mul_f32 v[66:67], v[68:69], v[66:67]
	v_mul_f32_e32 v68, 0xbfb8aa3b, v62
	v_mul_f32_e32 v69, 0xbfb8aa3b, v63
	v_exp_f32_e32 v68, v68
	v_exp_f32_e32 v69, v69
	v_cvt_pk_bf16_f32 v77, v66, v67
	v_or_b32_e32 v66, v70, v151
	v_add_f32_e32 v68, 1.0, v68
	v_add_f32_e32 v69, 1.0, v69
	v_rcp_f32_e32 v68, v68
	v_rcp_f32_e32 v69, v69
	v_ashrrev_i32_e32 v67, 31, v66
	v_lshlrev_b64 v[66:67], 10, v[66:67]
	v_lshl_add_u64 v[66:67], v[134:135], 0, v[66:67]
	v_pk_mul_f32 v[62:63], v[62:63], v[68:69]
	v_permlane16_swap_b32_e32 v75, v77
	v_pk_mul_f32 v[58:59], v[58:59], v[62:63]
	global_store_dwordx4 v[82:83], v[74:77], off offset:128
	v_cvt_pk_bf16_f32 v58, v58, v59
	v_mul_f32_e32 v59, 0xbfb8aa3b, v64
	v_exp_f32_e32 v59, v59
	s_nop 0
	v_add_f32_e32 v59, 1.0, v59
	v_rcp_f32_e32 v62, v59
	v_mul_f32_e32 v59, 0xbfb8aa3b, v65
	v_exp_f32_e32 v59, v59
	s_nop 0
	v_add_f32_e32 v59, 1.0, v59
	v_rcp_f32_e32 v63, v59
	s_nop 0
	v_pk_mul_f32 v[62:63], v[64:65], v[62:63]
	s_nop 0
	v_pk_mul_f32 v[60:61], v[60:61], v[62:63]
	s_nop 0
	v_cvt_pk_bf16_f32 v59, v60, v61
	v_mul_f32_e32 v60, 0xbfb8aa3b, v54
	v_mul_f32_e32 v61, 0xbfb8aa3b, v55
	v_exp_f32_e32 v60, v60
	v_exp_f32_e32 v61, v61
	v_add_f32_e32 v60, 1.0, v60
	v_add_f32_e32 v61, 1.0, v61
	v_rcp_f32_e32 v60, v60
	v_rcp_f32_e32 v61, v61
	s_nop 0
	v_pk_mul_f32 v[54:55], v[54:55], v[60:61]
	s_nop 0
	v_pk_mul_f32 v[50:51], v[50:51], v[54:55]
	s_nop 0
	v_cvt_pk_bf16_f32 v60, v50, v51
	v_mul_f32_e32 v50, 0xbfb8aa3b, v56
	v_mul_f32_e32 v51, 0xbfb8aa3b, v57
	v_exp_f32_e32 v50, v50
	v_exp_f32_e32 v51, v51
	v_permlane16_swap_b32_e32 v58, v60
	v_add_f32_e32 v50, 1.0, v50
	v_add_f32_e32 v51, 1.0, v51
	v_rcp_f32_e32 v50, v50
	v_rcp_f32_e32 v51, v51
	s_nop 0
	v_pk_mul_f32 v[50:51], v[56:57], v[50:51]
	s_nop 0
	v_pk_mul_f32 v[50:51], v[52:53], v[50:51]
	v_mul_f32_e32 v52, 0xbfb8aa3b, v46
	v_mul_f32_e32 v53, 0xbfb8aa3b, v47
	v_exp_f32_e32 v52, v52
	v_exp_f32_e32 v53, v53
	v_cvt_pk_bf16_f32 v61, v50, v51
	s_nop 1
	v_permlane16_swap_b32_e32 v59, v61
	v_add_f32_e32 v52, 1.0, v52
	v_add_f32_e32 v53, 1.0, v53
	v_rcp_f32_e32 v52, v52
	v_rcp_f32_e32 v53, v53
	v_lshl_add_u64 v[50:51], v[66:67], 0, v[114:115]
	global_store_dwordx4 v[50:51], v[58:61], off
	v_pk_mul_f32 v[46:47], v[46:47], v[52:53]
	s_nop 0
	v_pk_mul_f32 v[42:43], v[42:43], v[46:47]
	s_nop 0
	v_cvt_pk_bf16_f32 v42, v42, v43
	v_mul_f32_e32 v43, 0xbfb8aa3b, v48
	v_exp_f32_e32 v43, v43
	s_nop 0
	v_add_f32_e32 v43, 1.0, v43
	v_rcp_f32_e32 v46, v43
	v_mul_f32_e32 v43, 0xbfb8aa3b, v49
	v_exp_f32_e32 v43, v43
	s_nop 0
	v_add_f32_e32 v43, 1.0, v43
	v_rcp_f32_e32 v47, v43
	s_nop 0
	v_pk_mul_f32 v[46:47], v[48:49], v[46:47]
	s_nop 0
	v_pk_mul_f32 v[44:45], v[44:45], v[46:47]
	s_nop 0
	v_cvt_pk_bf16_f32 v43, v44, v45
	v_mul_f32_e32 v44, 0xbfb8aa3b, v38
	v_mul_f32_e32 v45, 0xbfb8aa3b, v39
	v_exp_f32_e32 v44, v44
	v_exp_f32_e32 v45, v45
	v_add_f32_e32 v44, 1.0, v44
	v_add_f32_e32 v45, 1.0, v45
	v_rcp_f32_e32 v44, v44
	v_rcp_f32_e32 v45, v45
	s_nop 0
	v_pk_mul_f32 v[38:39], v[38:39], v[44:45]
	s_nop 0
	v_pk_mul_f32 v[34:35], v[34:35], v[38:39]
	s_nop 0
	v_cvt_pk_bf16_f32 v44, v34, v35
	v_mul_f32_e32 v34, 0xbfb8aa3b, v40
	v_mul_f32_e32 v35, 0xbfb8aa3b, v41
	v_exp_f32_e32 v34, v34
	v_exp_f32_e32 v35, v35
	v_permlane16_swap_b32_e32 v42, v44
	v_add_f32_e32 v34, 1.0, v34
	v_add_f32_e32 v35, 1.0, v35
	v_rcp_f32_e32 v34, v34
	v_rcp_f32_e32 v35, v35
	s_nop 0
	v_pk_mul_f32 v[34:35], v[40:41], v[34:35]
	s_nop 0
	v_pk_mul_f32 v[34:35], v[36:37], v[34:35]
	v_mul_f32_e32 v36, 0xbfb8aa3b, v30
	v_mul_f32_e32 v37, 0xbfb8aa3b, v31
	v_exp_f32_e32 v36, v36
	v_exp_f32_e32 v37, v37
	v_cvt_pk_bf16_f32 v45, v34, v35
	v_or_b32_e32 v34, v70, v152
	v_add_f32_e32 v36, 1.0, v36
	v_add_f32_e32 v37, 1.0, v37
	v_rcp_f32_e32 v36, v36
	v_rcp_f32_e32 v37, v37
	v_ashrrev_i32_e32 v35, 31, v34
	v_lshlrev_b64 v[34:35], 10, v[34:35]
	v_lshl_add_u64 v[34:35], v[134:135], 0, v[34:35]
	v_pk_mul_f32 v[30:31], v[30:31], v[36:37]
	v_permlane16_swap_b32_e32 v43, v45
	v_pk_mul_f32 v[26:27], v[26:27], v[30:31]
	global_store_dwordx4 v[50:51], v[42:45], off offset:128
	v_cvt_pk_bf16_f32 v26, v26, v27
	v_mul_f32_e32 v27, 0xbfb8aa3b, v32
	v_exp_f32_e32 v27, v27
	s_nop 0
	v_add_f32_e32 v27, 1.0, v27
	v_rcp_f32_e32 v30, v27
	v_mul_f32_e32 v27, 0xbfb8aa3b, v33
	v_exp_f32_e32 v27, v27
	s_nop 0
	v_add_f32_e32 v27, 1.0, v27
	v_rcp_f32_e32 v31, v27
	s_nop 0
	v_pk_mul_f32 v[30:31], v[32:33], v[30:31]
	s_nop 0
	v_pk_mul_f32 v[28:29], v[28:29], v[30:31]
	s_nop 0
	v_cvt_pk_bf16_f32 v27, v28, v29
	v_mul_f32_e32 v28, 0xbfb8aa3b, v22
	v_mul_f32_e32 v29, 0xbfb8aa3b, v23
	v_exp_f32_e32 v28, v28
	v_exp_f32_e32 v29, v29
	v_add_f32_e32 v28, 1.0, v28
	v_add_f32_e32 v29, 1.0, v29
	v_rcp_f32_e32 v28, v28
	v_rcp_f32_e32 v29, v29
	s_nop 0
	v_pk_mul_f32 v[22:23], v[22:23], v[28:29]
	s_nop 0
	v_pk_mul_f32 v[18:19], v[18:19], v[22:23]
	s_nop 0
	v_cvt_pk_bf16_f32 v28, v18, v19
	v_mul_f32_e32 v18, 0xbfb8aa3b, v24
	v_mul_f32_e32 v19, 0xbfb8aa3b, v25
	v_exp_f32_e32 v18, v18
	v_exp_f32_e32 v19, v19
	v_permlane16_swap_b32_e32 v26, v28
	v_add_f32_e32 v18, 1.0, v18
	v_add_f32_e32 v19, 1.0, v19
	v_rcp_f32_e32 v18, v18
	v_rcp_f32_e32 v19, v19
	s_nop 0
	v_pk_mul_f32 v[18:19], v[24:25], v[18:19]
	s_nop 0
	v_pk_mul_f32 v[18:19], v[20:21], v[18:19]
	v_mul_f32_e32 v20, 0xbfb8aa3b, v14
	v_mul_f32_e32 v21, 0xbfb8aa3b, v15
	v_exp_f32_e32 v20, v20
	v_exp_f32_e32 v21, v21
	v_cvt_pk_bf16_f32 v29, v18, v19
	s_nop 1
	v_permlane16_swap_b32_e32 v27, v29
	v_add_f32_e32 v20, 1.0, v20
	v_add_f32_e32 v21, 1.0, v21
	v_rcp_f32_e32 v20, v20
	v_rcp_f32_e32 v21, v21
	v_lshl_add_u64 v[18:19], v[34:35], 0, v[114:115]
	global_store_dwordx4 v[18:19], v[26:29], off
	v_pk_mul_f32 v[14:15], v[14:15], v[20:21]
	s_nop 0
	v_pk_mul_f32 v[10:11], v[10:11], v[14:15]
	s_nop 0
	v_cvt_pk_bf16_f32 v10, v10, v11
	v_mul_f32_e32 v11, 0xbfb8aa3b, v16
	v_exp_f32_e32 v11, v11
	s_nop 0
	v_add_f32_e32 v11, 1.0, v11
	v_rcp_f32_e32 v14, v11
	v_mul_f32_e32 v11, 0xbfb8aa3b, v17
	v_exp_f32_e32 v11, v11
	s_nop 0
	v_add_f32_e32 v11, 1.0, v11
	v_rcp_f32_e32 v15, v11
	s_nop 0
	v_pk_mul_f32 v[14:15], v[16:17], v[14:15]
	s_nop 0
	v_pk_mul_f32 v[12:13], v[12:13], v[14:15]
	s_nop 0
	v_cvt_pk_bf16_f32 v11, v12, v13
	v_mul_f32_e32 v12, 0xbfb8aa3b, v6
	v_mul_f32_e32 v13, 0xbfb8aa3b, v7
	v_exp_f32_e32 v12, v12
	v_exp_f32_e32 v13, v13
	v_add_f32_e32 v12, 1.0, v12
	v_add_f32_e32 v13, 1.0, v13
	v_rcp_f32_e32 v12, v12
	v_rcp_f32_e32 v13, v13
	s_nop 0
	v_pk_mul_f32 v[6:7], v[6:7], v[12:13]
	s_nop 0
	v_pk_mul_f32 v[2:3], v[2:3], v[6:7]
	s_nop 0
	v_cvt_pk_bf16_f32 v12, v2, v3
	v_mul_f32_e32 v2, 0xbfb8aa3b, v8
	v_mul_f32_e32 v3, 0xbfb8aa3b, v9
	v_exp_f32_e32 v2, v2
	v_exp_f32_e32 v3, v3
	v_permlane16_swap_b32_e32 v10, v12
	v_add_f32_e32 v2, 1.0, v2
	v_add_f32_e32 v3, 1.0, v3
	v_rcp_f32_e32 v2, v2
	v_rcp_f32_e32 v3, v3
	s_nop 0
	v_pk_mul_f32 v[2:3], v[8:9], v[2:3]
	s_nop 0
	v_pk_mul_f32 v[2:3], v[4:5], v[2:3]
	s_nop 0
	v_cvt_pk_bf16_f32 v13, v2, v3
	s_nop 1
	v_permlane16_swap_b32_e32 v11, v13
	global_store_dwordx4 v[18:19], v[10:13], off offset:128
	s_cbranch_vccz .LBB0_2465
	s_waitcnt vmcnt(0)
	s_cmpk_gt_u32 s29, 0xff
	s_cbranch_scc1 .LBB0_2479
	s_barrier

.LBB0_2563:
	s_add_u32 s0, s22, 0xfffe0080
	s_addc_u32 s1, s23, -1
	s_add_i32 s33, 0, 0x10000
	s_cmp_eq_u32 s77, 4
	s_cselect_b32 s27, s11, s1
	s_cselect_b32 s26, s74, s0
	s_cselect_b32 s25, s13, s76
	s_cselect_b32 s24, s15, s75
	v_lshl_add_u64 v[192:193], s[22:23], 0, v[136:137]
	s_add_i32 m0, s9, 0xc000
	ds_read_b128 v[160:163], v142
	ds_read_b128 v[164:167], v142 offset:1024
	ds_read_b128 v[168:171], v142 offset:2048
	ds_read_b128 v[172:175], v142 offset:3072
	ds_read_b128 v[176:179], v142 offset:4096
	ds_read_b128 v[180:183], v142 offset:5120
	ds_read_b128 v[184:187], v142 offset:6144
	ds_read_b128 v[188:191], v142 offset:7168
	global_load_lds_dwordx4 v[192:193], off
	v_lshl_add_u64 v[192:193], s[22:23], 0, v[138:139]
	s_add_i32 m0, s9, 0xe000
	s_nop 0
	global_load_lds_dwordx4 v[192:193], off
	s_waitcnt lgkmcnt(8)
	s_barrier
	s_waitcnt lgkmcnt(0)
	v_mfma_f32_16x16x32_bf16 v[126:129], v[144:147], v[160:163], v[126:129]
	v_mfma_f32_16x16x32_bf16 v[122:125], v[152:155], v[160:163], v[122:125]
	v_mfma_f32_16x16x32_bf16 v[118:121], v[144:147], v[168:171], v[118:121]
	v_mfma_f32_16x16x32_bf16 v[114:117], v[152:155], v[168:171], v[114:117]
	v_mfma_f32_16x16x32_bf16 v[102:105], v[144:147], v[176:179], v[102:105]
	v_mfma_f32_16x16x32_bf16 v[98:101], v[152:155], v[176:179], v[98:101]
	v_mfma_f32_16x16x32_bf16 v[86:89], v[144:147], v[184:187], v[86:89]
	v_mfma_f32_16x16x32_bf16 v[82:85], v[152:155], v[184:187], v[82:85]
	v_mfma_f32_16x16x32_bf16 v[126:129], v[148:151], v[164:167], v[126:129]
	v_mfma_f32_16x16x32_bf16 v[122:125], v[156:159], v[164:167], v[122:125]
	v_mfma_f32_16x16x32_bf16 v[118:121], v[148:151], v[172:175], v[118:121]
	v_mfma_f32_16x16x32_bf16 v[114:117], v[156:159], v[172:175], v[114:117]
	v_mfma_f32_16x16x32_bf16 v[102:105], v[148:151], v[180:183], v[102:105]
	v_mfma_f32_16x16x32_bf16 v[98:101], v[156:159], v[180:183], v[98:101]
	v_mfma_f32_16x16x32_bf16 v[86:89], v[148:151], v[188:191], v[86:89]
	v_mfma_f32_16x16x32_bf16 v[82:85], v[156:159], v[188:191], v[82:85]
	s_barrier
	s_add_i32 s36, 0, 0x14000
	s_add_i32 s0, s33, s40
	v_add_u32_e32 v143, s36, v140
	v_lshl_add_u64 v[192:193], s[24:25], 0, v[194:195]
	s_mov_b32 m0, s0
	ds_read_b128 v[198:201], v143
	ds_read_b128 v[202:205], v143 offset:1024
	ds_read_b128 v[206:209], v143 offset:2048
	ds_read_b128 v[210:213], v143 offset:3072
	global_load_lds_dwordx4 v[192:193], off
	v_lshl_add_u64 v[214:215], s[24:25], 0, v[134:135]
	s_add_i32 m0, s0, 0x2000
	s_nop 0
	global_load_lds_dwordx4 v[214:215], off
	s_barrier
	s_waitcnt lgkmcnt(0)
	v_mfma_f32_16x16x32_bf16 v[110:113], v[198:201], v[160:163], v[110:113]
	v_mfma_f32_16x16x32_bf16 v[106:109], v[206:209], v[160:163], v[106:109]
	v_mfma_f32_16x16x32_bf16 v[94:97], v[198:201], v[168:171], v[94:97]
	v_mfma_f32_16x16x32_bf16 v[90:93], v[206:209], v[168:171], v[90:93]
	v_mfma_f32_16x16x32_bf16 v[78:81], v[198:201], v[176:179], v[78:81]
	v_mfma_f32_16x16x32_bf16 v[74:77], v[206:209], v[176:179], v[74:77]
	v_mfma_f32_16x16x32_bf16 v[70:73], v[198:201], v[184:187], v[70:73]
	v_mfma_f32_16x16x32_bf16 v[66:69], v[206:209], v[184:187], v[66:69]
	v_mfma_f32_16x16x32_bf16 v[110:113], v[202:205], v[164:167], v[110:113]
	v_mfma_f32_16x16x32_bf16 v[106:109], v[210:213], v[164:167], v[106:109]
	v_mfma_f32_16x16x32_bf16 v[94:97], v[202:205], v[172:175], v[94:97]
	v_mfma_f32_16x16x32_bf16 v[90:93], v[210:213], v[172:175], v[90:93]
	v_mfma_f32_16x16x32_bf16 v[78:81], v[202:205], v[180:183], v[78:81]
	v_mfma_f32_16x16x32_bf16 v[74:77], v[210:213], v[180:183], v[74:77]
	v_mfma_f32_16x16x32_bf16 v[70:73], v[202:205], v[188:191], v[70:73]
	v_mfma_f32_16x16x32_bf16 v[66:69], v[210:213], v[188:191], v[66:69]
	s_mov_b32 m0, s9
	v_lshl_add_u64 v[216:217], s[26:27], 0, v[130:131]
	s_barrier
	ds_read_b128 v[160:163], v142 offset:16384
	ds_read_b128 v[164:167], v142 offset:17408
	ds_read_b128 v[168:171], v142 offset:18432
	ds_read_b128 v[172:175], v142 offset:19456
	ds_read_b128 v[176:179], v142 offset:20480
	ds_read_b128 v[180:183], v142 offset:21504
	ds_read_b128 v[184:187], v142 offset:22528
	ds_read_b128 v[188:191], v142 offset:23552
	global_load_lds_dwordx4 v[216:217], off
	v_lshl_add_u64 v[218:219], s[26:27], 0, v[132:133]
	s_mov_b32 m0, s43
	s_nop 0
	global_load_lds_dwordx4 v[218:219], off
	s_waitcnt vmcnt(10)
	s_barrier
	s_waitcnt lgkmcnt(0)
	v_mfma_f32_16x16x32_bf16 v[62:65], v[144:147], v[160:163], v[62:65]
	v_mfma_f32_16x16x32_bf16 v[58:61], v[152:155], v[160:163], v[58:61]
	v_mfma_f32_16x16x32_bf16 v[54:57], v[144:147], v[168:171], v[54:57]
	v_mfma_f32_16x16x32_bf16 v[50:53], v[152:155], v[168:171], v[50:53]
	v_mfma_f32_16x16x32_bf16 v[38:41], v[144:147], v[176:179], v[38:41]
	v_mfma_f32_16x16x32_bf16 v[34:37], v[152:155], v[176:179], v[34:37]
	v_mfma_f32_16x16x32_bf16 v[22:25], v[144:147], v[184:187], v[22:25]
	v_mfma_f32_16x16x32_bf16 v[18:21], v[152:155], v[184:187], v[18:21]
	v_mfma_f32_16x16x32_bf16 v[62:65], v[148:151], v[164:167], v[62:65]
	v_mfma_f32_16x16x32_bf16 v[58:61], v[156:159], v[164:167], v[58:61]
	v_mfma_f32_16x16x32_bf16 v[54:57], v[148:151], v[172:175], v[54:57]
	v_mfma_f32_16x16x32_bf16 v[50:53], v[156:159], v[172:175], v[50:53]
	v_mfma_f32_16x16x32_bf16 v[38:41], v[148:151], v[180:183], v[38:41]
	v_mfma_f32_16x16x32_bf16 v[34:37], v[156:159], v[180:183], v[34:37]
	v_mfma_f32_16x16x32_bf16 v[22:25], v[148:151], v[188:191], v[22:25]
	v_mfma_f32_16x16x32_bf16 v[18:21], v[156:159], v[188:191], v[18:21]
	s_barrier
	s_add_u32 s0, s24, 0x20000
	s_addc_u32 s1, s25, 0
	s_add_i32 s33, s36, s40
	v_lshl_add_u64 v[144:145], s[0:1], 0, v[194:195]
	s_mov_b32 m0, s33
	s_nop 0
	global_load_lds_dwordx4 v[144:145], off
	v_lshl_add_u64 v[144:145], s[0:1], 0, v[134:135]
	s_add_i32 m0, s33, 0x2000
	s_nop 0
	global_load_lds_dwordx4 v[144:145], off
	v_add_u32_e32 v156, 0x18000, v140
	ds_read_b128 v[144:147], v156
	ds_read_b128 v[148:151], v156 offset:1024
	ds_read_b128 v[152:155], v156 offset:2048
	ds_read_b128 v[156:159], v156 offset:3072
	s_waitcnt vmcnt(6)
	s_barrier
	v_mfma_f32_16x16x32_bf16 v[46:49], v[198:201], v[160:163], v[46:49]
	v_mfma_f32_16x16x32_bf16 v[42:45], v[206:209], v[160:163], v[42:45]
	v_mfma_f32_16x16x32_bf16 v[30:33], v[198:201], v[168:171], v[30:33]
	v_mfma_f32_16x16x32_bf16 v[26:29], v[206:209], v[168:171], v[26:29]
	v_mfma_f32_16x16x32_bf16 v[14:17], v[198:201], v[176:179], v[14:17]
	v_mfma_f32_16x16x32_bf16 v[10:13], v[206:209], v[176:179], v[10:13]
	v_mfma_f32_16x16x32_bf16 v[6:9], v[198:201], v[184:187], v[6:9]
	v_mfma_f32_16x16x32_bf16 v[2:5], v[206:209], v[184:187], v[2:5]
	v_mfma_f32_16x16x32_bf16 v[46:49], v[202:205], v[164:167], v[46:49]
	v_mfma_f32_16x16x32_bf16 v[42:45], v[210:213], v[164:167], v[42:45]
	v_mfma_f32_16x16x32_bf16 v[30:33], v[202:205], v[172:175], v[30:33]
	v_mfma_f32_16x16x32_bf16 v[26:29], v[210:213], v[172:175], v[26:29]
	v_mfma_f32_16x16x32_bf16 v[14:17], v[202:205], v[180:183], v[14:17]
	v_mfma_f32_16x16x32_bf16 v[10:13], v[210:213], v[180:183], v[10:13]
	v_mfma_f32_16x16x32_bf16 v[6:9], v[202:205], v[188:191], v[6:9]
	v_mfma_f32_16x16x32_bf16 v[2:5], v[210:213], v[188:191], v[2:5]
	s_add_i32 s33, 0, 0x18000
	s_barrier
	s_add_u32 s0, s26, 0x20000
	s_addc_u32 s1, s27, 0
	s_mov_b32 m0, s64
	v_lshl_add_u64 v[198:199], s[0:1], 0, v[130:131]
	ds_read_b128 v[160:163], v142 offset:32768
	ds_read_b128 v[164:167], v142 offset:33792
	ds_read_b128 v[168:171], v142 offset:34816
	ds_read_b128 v[172:175], v142 offset:35840
	ds_read_b128 v[176:179], v142 offset:36864
	ds_read_b128 v[180:183], v142 offset:37888
	ds_read_b128 v[184:187], v142 offset:38912
	ds_read_b128 v[188:191], v142 offset:39936
	global_load_lds_dwordx4 v[198:199], off
	v_lshl_add_u64 v[198:199], s[0:1], 0, v[132:133]
	s_mov_b32 m0, s65
	s_nop 0
	global_load_lds_dwordx4 v[198:199], off
	s_waitcnt lgkmcnt(8)
	s_barrier
	s_waitcnt lgkmcnt(0)
	v_mfma_f32_16x16x32_bf16 v[126:129], v[144:147], v[160:163], v[126:129]
	v_mfma_f32_16x16x32_bf16 v[122:125], v[152:155], v[160:163], v[122:125]
	v_mfma_f32_16x16x32_bf16 v[118:121], v[144:147], v[168:171], v[118:121]
	v_mfma_f32_16x16x32_bf16 v[114:117], v[152:155], v[168:171], v[114:117]
	v_mfma_f32_16x16x32_bf16 v[102:105], v[144:147], v[176:179], v[102:105]
	v_mfma_f32_16x16x32_bf16 v[98:101], v[152:155], v[176:179], v[98:101]
	v_mfma_f32_16x16x32_bf16 v[86:89], v[144:147], v[184:187], v[86:89]
	v_mfma_f32_16x16x32_bf16 v[82:85], v[152:155], v[184:187], v[82:85]
	v_mfma_f32_16x16x32_bf16 v[126:129], v[148:151], v[164:167], v[126:129]
	v_mfma_f32_16x16x32_bf16 v[122:125], v[156:159], v[164:167], v[122:125]
	v_mfma_f32_16x16x32_bf16 v[118:121], v[148:151], v[172:175], v[118:121]
	v_mfma_f32_16x16x32_bf16 v[114:117], v[156:159], v[172:175], v[114:117]
	v_mfma_f32_16x16x32_bf16 v[102:105], v[148:151], v[180:183], v[102:105]
	v_mfma_f32_16x16x32_bf16 v[98:101], v[156:159], v[180:183], v[98:101]
	v_mfma_f32_16x16x32_bf16 v[86:89], v[148:151], v[188:191], v[86:89]
	v_mfma_f32_16x16x32_bf16 v[82:85], v[156:159], v[188:191], v[82:85]
	s_barrier
	s_add_i32 s26, 0, 0x1c000
	s_add_i32 s0, s33, s40
	v_add_u32_e32 v143, s26, v140
	v_lshl_add_u64 v[192:193], v[192:193], 0, s[54:55]
	s_mov_b32 m0, s0
	ds_read_b128 v[198:201], v143
	ds_read_b128 v[202:205], v143 offset:1024
	ds_read_b128 v[206:209], v143 offset:2048
	ds_read_b128 v[210:213], v143 offset:3072
	global_load_lds_dwordx4 v[192:193], off
	v_lshl_add_u64 v[192:193], v[214:215], 0, s[54:55]
	s_add_i32 m0, s0, 0x2000
	s_nop 0
	global_load_lds_dwordx4 v[192:193], off
	s_barrier
	s_waitcnt lgkmcnt(0)
	v_mfma_f32_16x16x32_bf16 v[110:113], v[198:201], v[160:163], v[110:113]
	v_mfma_f32_16x16x32_bf16 v[106:109], v[206:209], v[160:163], v[106:109]
	v_mfma_f32_16x16x32_bf16 v[94:97], v[198:201], v[168:171], v[94:97]
	v_mfma_f32_16x16x32_bf16 v[90:93], v[206:209], v[168:171], v[90:93]
	v_mfma_f32_16x16x32_bf16 v[78:81], v[198:201], v[176:179], v[78:81]
	v_mfma_f32_16x16x32_bf16 v[74:77], v[206:209], v[176:179], v[74:77]
	v_mfma_f32_16x16x32_bf16 v[70:73], v[198:201], v[184:187], v[70:73]
	v_mfma_f32_16x16x32_bf16 v[66:69], v[206:209], v[184:187], v[66:69]
	v_mfma_f32_16x16x32_bf16 v[110:113], v[202:205], v[164:167], v[110:113]
	v_mfma_f32_16x16x32_bf16 v[106:109], v[210:213], v[164:167], v[106:109]
	v_mfma_f32_16x16x32_bf16 v[94:97], v[202:205], v[172:175], v[94:97]
	v_mfma_f32_16x16x32_bf16 v[90:93], v[210:213], v[172:175], v[90:93]
	v_mfma_f32_16x16x32_bf16 v[78:81], v[202:205], v[180:183], v[78:81]
	v_mfma_f32_16x16x32_bf16 v[74:77], v[210:213], v[180:183], v[74:77]
	v_mfma_f32_16x16x32_bf16 v[70:73], v[202:205], v[188:191], v[70:73]
	v_mfma_f32_16x16x32_bf16 v[66:69], v[210:213], v[188:191], v[66:69]
	s_mov_b32 m0, s66
	v_lshl_add_u64 v[192:193], v[216:217], 0, s[54:55]
	s_barrier
	ds_read_b128 v[160:163], v142 offset:49152
	ds_read_b128 v[164:167], v142 offset:50176
	ds_read_b128 v[168:171], v142 offset:51200
	ds_read_b128 v[172:175], v142 offset:52224
	ds_read_b128 v[176:179], v142 offset:53248
	ds_read_b128 v[180:183], v142 offset:54272
	ds_read_b128 v[184:187], v142 offset:55296
	ds_read_b128 v[188:191], v142 offset:56320
	global_load_lds_dwordx4 v[192:193], off
	v_lshl_add_u64 v[192:193], v[218:219], 0, s[54:55]
	s_mov_b32 m0, s67
	s_nop 0
	global_load_lds_dwordx4 v[192:193], off
	s_waitcnt vmcnt(10)
	s_barrier
	s_waitcnt lgkmcnt(0)
	v_mfma_f32_16x16x32_bf16 v[62:65], v[144:147], v[160:163], v[62:65]
	v_mfma_f32_16x16x32_bf16 v[58:61], v[152:155], v[160:163], v[58:61]
	v_mfma_f32_16x16x32_bf16 v[54:57], v[144:147], v[168:171], v[54:57]
	v_mfma_f32_16x16x32_bf16 v[50:53], v[152:155], v[168:171], v[50:53]
	v_mfma_f32_16x16x32_bf16 v[38:41], v[144:147], v[176:179], v[38:41]
	v_mfma_f32_16x16x32_bf16 v[34:37], v[152:155], v[176:179], v[34:37]
	v_mfma_f32_16x16x32_bf16 v[22:25], v[144:147], v[184:187], v[22:25]
	v_mfma_f32_16x16x32_bf16 v[18:21], v[152:155], v[184:187], v[18:21]
	v_mfma_f32_16x16x32_bf16 v[62:65], v[148:151], v[164:167], v[62:65]
	v_mfma_f32_16x16x32_bf16 v[58:61], v[156:159], v[164:167], v[58:61]
	v_mfma_f32_16x16x32_bf16 v[54:57], v[148:151], v[172:175], v[54:57]
	v_mfma_f32_16x16x32_bf16 v[50:53], v[156:159], v[172:175], v[50:53]
	v_mfma_f32_16x16x32_bf16 v[38:41], v[148:151], v[180:183], v[38:41]
	v_mfma_f32_16x16x32_bf16 v[34:37], v[156:159], v[180:183], v[34:37]
	v_mfma_f32_16x16x32_bf16 v[22:25], v[148:151], v[188:191], v[22:25]
	v_mfma_f32_16x16x32_bf16 v[18:21], v[156:159], v[188:191], v[18:21]
	s_barrier
	s_add_u32 s0, s24, 0x20080
	s_addc_u32 s1, s25, 0
	s_add_i32 s24, s26, s40
	v_lshl_add_u64 v[144:145], s[0:1], 0, v[194:195]
	s_mov_b32 m0, s24
	s_nop 0
	global_load_lds_dwordx4 v[144:145], off
	v_lshl_add_u64 v[144:145], s[0:1], 0, v[134:135]
	s_add_i32 m0, s24, 0x2000
	s_nop 0
	global_load_lds_dwordx4 v[144:145], off
	v_add_u32_e32 v156, 0x10000, v140
	ds_read_b128 v[144:147], v156
	ds_read_b128 v[148:151], v156 offset:1024
	ds_read_b128 v[152:155], v156 offset:2048
	ds_read_b128 v[156:159], v156 offset:3072
	s_waitcnt vmcnt(6)
	s_barrier
	v_mfma_f32_16x16x32_bf16 v[46:49], v[198:201], v[160:163], v[46:49]
	v_mfma_f32_16x16x32_bf16 v[42:45], v[206:209], v[160:163], v[42:45]
	v_mfma_f32_16x16x32_bf16 v[30:33], v[198:201], v[168:171], v[30:33]
	v_mfma_f32_16x16x32_bf16 v[26:29], v[206:209], v[168:171], v[26:29]
	v_mfma_f32_16x16x32_bf16 v[14:17], v[198:201], v[176:179], v[14:17]
	v_mfma_f32_16x16x32_bf16 v[10:13], v[206:209], v[176:179], v[10:13]
	v_mfma_f32_16x16x32_bf16 v[6:9], v[198:201], v[184:187], v[6:9]
	v_mfma_f32_16x16x32_bf16 v[2:5], v[206:209], v[184:187], v[2:5]
	v_mfma_f32_16x16x32_bf16 v[46:49], v[202:205], v[164:167], v[46:49]
	v_mfma_f32_16x16x32_bf16 v[42:45], v[210:213], v[164:167], v[42:45]
	v_mfma_f32_16x16x32_bf16 v[30:33], v[202:205], v[172:175], v[30:33]
	v_mfma_f32_16x16x32_bf16 v[26:29], v[210:213], v[172:175], v[26:29]
	v_mfma_f32_16x16x32_bf16 v[14:17], v[202:205], v[180:183], v[14:17]
	v_mfma_f32_16x16x32_bf16 v[10:13], v[210:213], v[180:183], v[10:13]
	v_mfma_f32_16x16x32_bf16 v[6:9], v[202:205], v[188:191], v[6:9]
	v_mfma_f32_16x16x32_bf16 v[2:5], v[210:213], v[188:191], v[2:5]
	s_add_i32 s77, s77, 2
	s_add_u32 s22, s22, 0x100
	s_addc_u32 s23, s23, 0
	s_add_u32 s75, s75, 0x100
	s_addc_u32 s76, s76, 0
	s_cmp_gt_u32 s77, 5
	s_barrier
	s_cbranch_scc0 .LBB0_2563
	s_waitcnt lgkmcnt(0)
	v_lshl_add_u32 v144, s8, 8, v1
	v_lshl_or_b32 v146, s68, 8, v141
	v_ashrrev_i32_e32 v145, 31, v144
	v_lshlrev_b64 v[148:149], 11, v[144:145]
	v_ashrrev_i32_e32 v147, 31, v146
	v_lshl_add_u64 v[148:149], s[6:7], 0, v[148:149]
	v_cvt_pk_bf16_f32 v126, v126, v127
	v_cvt_pk_bf16_f32 v127, v128, v129
	v_cvt_pk_bf16_f32 v128, v122, v123
	v_lshlrev_b64 v[122:123], 1, v[146:147]
	v_cvt_pk_bf16_f32 v129, v124, v125
	v_lshl_add_u64 v[124:125], v[148:149], 0, v[122:123]
	s_mov_b64 s[0:1], 0x40000
	v_cvt_pk_bf16_f32 v62, v62, v63
	v_cvt_pk_bf16_f32 v63, v64, v65
	v_cvt_pk_bf16_f32 v64, v58, v59
	v_lshl_add_u64 v[58:59], v[124:125], 0, s[0:1]
	s_mov_b32 s0, 0x40000
	v_cvt_pk_bf16_f32 v110, v110, v111
	v_cvt_pk_bf16_f32 v111, v112, v113
	v_cvt_pk_bf16_f32 v112, v106, v107
	v_or_b32_e32 v106, 16, v144
	v_cvt_pk_bf16_f32 v65, v60, v61
	v_add_co_u32_e32 v60, vcc, s0, v124
	v_cvt_pk_bf16_f32 v46, v46, v47
	v_cvt_pk_bf16_f32 v47, v48, v49
	v_cvt_pk_bf16_f32 v48, v42, v43
	v_cvt_pk_bf16_f32 v49, v44, v45
	s_mov_b64 s[0:1], 0x48000
	v_ashrrev_i32_e32 v107, 31, v106
	v_addc_co_u32_e32 v61, vcc, 0, v125, vcc
	global_store_dwordx4 v[58:59], v[46:49], off offset:256
	v_cvt_pk_bf16_f32 v113, v108, v109
	v_lshlrev_b64 v[106:107], 11, v[106:107]
	v_lshl_add_u64 v[46:47], v[124:125], 0, s[0:1]
	s_mov_b32 s0, 0x48000
	v_cvt_pk_bf16_f32 v94, v94, v95
	v_cvt_pk_bf16_f32 v95, v96, v97
	v_cvt_pk_bf16_f32 v96, v90, v91
	v_or_b32_e32 v90, 32, v144
	v_add_co_u32_e32 v48, vcc, s0, v124
	v_cvt_pk_bf16_f32 v30, v30, v31
	v_cvt_pk_bf16_f32 v31, v32, v33
	v_cvt_pk_bf16_f32 v32, v26, v27
	v_cvt_pk_bf16_f32 v33, v28, v29
	s_mov_b64 s[0:1], 0x50000
	global_store_dwordx4 v[124:125], v[110:113], off offset:256
	v_ashrrev_i32_e32 v91, 31, v90
	v_addc_co_u32_e32 v49, vcc, 0, v125, vcc
	v_lshl_add_u64 v[110:111], s[6:7], 0, v[106:107]
	global_store_dwordx4 v[46:47], v[30:33], off offset:256
	v_lshl_add_u64 v[110:111], v[110:111], 0, v[122:123]
	v_cvt_pk_bf16_f32 v97, v92, v93
	v_lshl_add_u64 v[30:31], v[124:125], 0, s[0:1]
	s_mov_b32 s0, 0x50000
	v_lshlrev_b64 v[90:91], 11, v[90:91]
	v_cvt_pk_bf16_f32 v78, v78, v79
	v_cvt_pk_bf16_f32 v79, v80, v81
	v_cvt_pk_bf16_f32 v80, v74, v75
	v_or_b32_e32 v74, 48, v144
	v_add_co_u32_e32 v32, vcc, s0, v124
	v_cvt_pk_bf16_f32 v14, v14, v15
	v_cvt_pk_bf16_f32 v15, v16, v17
	v_cvt_pk_bf16_f32 v16, v10, v11
	v_cvt_pk_bf16_f32 v17, v12, v13
	s_mov_b64 s[0:1], 0x58000
	global_store_dwordx4 v[110:111], v[94:97], off offset:256
	v_ashrrev_i32_e32 v75, 31, v74
	v_addc_co_u32_e32 v33, vcc, 0, v125, vcc
	v_lshl_add_u64 v[94:95], s[6:7], 0, v[90:91]
	global_store_dwordx4 v[30:31], v[14:17], off offset:256
	v_lshl_add_u64 v[94:95], v[94:95], 0, v[122:123]
	v_cvt_pk_bf16_f32 v81, v76, v77
	v_lshl_add_u64 v[14:15], v[124:125], 0, s[0:1]
	s_mov_b32 s0, 0x58000
	v_lshlrev_b64 v[74:75], 11, v[74:75]
	v_add_co_u32_e32 v16, vcc, s0, v124
	global_store_dwordx4 v[94:95], v[78:81], off offset:256
	s_nop 0
	v_addc_co_u32_e32 v17, vcc, 0, v125, vcc
	v_lshl_add_u64 v[78:79], s[6:7], 0, v[74:75]
	v_cvt_pk_bf16_f32 v106, v118, v119
	v_cvt_pk_bf16_f32 v107, v120, v121
	v_cvt_pk_bf16_f32 v108, v114, v115
	v_cvt_pk_bf16_f32 v109, v116, v117
	v_cvt_pk_bf16_f32 v90, v102, v103
	v_cvt_pk_bf16_f32 v91, v104, v105
	v_cvt_pk_bf16_f32 v92, v98, v99
	v_cvt_pk_bf16_f32 v93, v100, v101
	v_cvt_pk_bf16_f32 v74, v86, v87
	v_cvt_pk_bf16_f32 v75, v88, v89
	v_cvt_pk_bf16_f32 v76, v82, v83
	v_cvt_pk_bf16_f32 v77, v84, v85
	v_lshl_add_u64 v[78:79], v[78:79], 0, v[122:123]
	v_cvt_pk_bf16_f32 v70, v70, v71
	v_cvt_pk_bf16_f32 v71, v72, v73
	v_cvt_pk_bf16_f32 v72, v66, v67
	v_cvt_pk_bf16_f32 v73, v68, v69
	v_cvt_pk_bf16_f32 v42, v54, v55
	v_cvt_pk_bf16_f32 v43, v56, v57
	v_cvt_pk_bf16_f32 v44, v50, v51
	v_cvt_pk_bf16_f32 v45, v52, v53
	v_cvt_pk_bf16_f32 v26, v38, v39
	v_cvt_pk_bf16_f32 v27, v40, v41
	v_cvt_pk_bf16_f32 v28, v34, v35
	v_cvt_pk_bf16_f32 v29, v36, v37
	v_cvt_pk_bf16_f32 v10, v22, v23
	v_cvt_pk_bf16_f32 v11, v24, v25
	v_cvt_pk_bf16_f32 v12, v18, v19
	v_cvt_pk_bf16_f32 v13, v20, v21
	v_cvt_pk_bf16_f32 v6, v6, v7
	v_cvt_pk_bf16_f32 v7, v8, v9
	v_cvt_pk_bf16_f32 v8, v2, v3
	v_cvt_pk_bf16_f32 v9, v4, v5
	s_and_b64 vcc, exec, s[18:19]
	s_mov_b32 s68, s14
	s_mov_b32 s8, s10
	s_mov_b64 s[24:25], s[20:21]
	s_mov_b64 s[22:23], s[16:17]
	global_store_dwordx4 v[124:125], v[126:129], off
	global_store_dwordx4 v[110:111], v[106:109], off
	global_store_dwordx4 v[94:95], v[90:93], off
	global_store_dwordx4 v[78:79], v[74:77], off
	global_store_dwordx4 v[78:79], v[70:73], off offset:256
	global_store_dwordx4 v[60:61], v[62:65], off
	global_store_dwordx4 v[48:49], v[42:45], off
	global_store_dwordx4 v[32:33], v[26:29], off
	global_store_dwordx4 v[16:17], v[10:13], off
	global_store_dwordx4 v[14:15], v[6:9], off offset:256
	s_cbranch_vccz .LBB0_2555
	s_waitcnt vmcnt(0)
	s_cmpk_gt_u32 s29, 0xff
	s_cbranch_scc1 .LBB0_2567
	s_barrier
